# attention key loops: counter/exit-test/ring-rotation SALU moved in front of the loop-closing barrier and the back edge taken before it (exit path gets its own barrier copy); packed f32 running-sum add
# baseline (speedup 1.0000x reference)
; template <int DQK, int DV, bool LEAD> ...
;     ...
;     const int tid = tid_, lane = tid & 63, q16 = lane & 15, g4 = lane >> 4, hi = lane >> 5; const int wid = __builtin_amdgcn_readfirstlane(tid >> 6);
;     const int kg = KS ? (wid >> 2) : 0, qoff = KS ? (wid & 3) * 64 : wid * 32;
;     const unsigned lds0 = (unsigned)(uintptr_t)shm;
;     const int krow_l = wid * 8 + (lane >> 3);
;     const int kc_l = (lane & 7) ^ (((krow_l >> 1) & 1) | (((krow_l >> 3) & 1) << 1) | (((krow_l >> 4) & 1) << 2));
;     const int vc_l = (lane & 7) ^ ((krow_l >> 1) & 7);
;     const bf16_t* ksrc = K + (size_t)(krow0 + krow_l) * kpitch + kc_l * 8;
;     const int rrow_l = (wid & 3) * 16 + (lane >> 2), rc_l = (lane & 3) ^ (((rrow_l >> 4) & 1) << 1);
;     const bf16_t* krsrc = (DQK == 96) ? KR + (size_t)(krow0 + rrow_l) * 32 + rc_l * 8 : nullptr;
;     const bf16_t* vsrc = Vt + (size_t)krow_l * NR + krow0 + vc_l * 8;
;     const unsigned kdst = lds0 + KOFF + wid * 1024, krdst = lds0 + KOFF + 8192 + (wid & 3) * 1024, vdst = lds0 + VOFF + wid * 1024;
;     ...
;     const int kr0 = 8 * (q16 >> 2) + (q16 & 3);
;     const int fk = ((kr0 >> 1) & 1) | (((kr0 >> 3) & 1) << 1) | (((kr0 >> 4) & 1) << 2);
;     const LAS unsigned char* kp[2]; const LAS unsigned char* vp[2];
; #pragma unroll
;     for (int ds = 0; ds < 2; ++ds) kp[ds] = shm + KOFF + kr0 * 128 + ((((ds << 2) | g4) ^ fk) << 4) + kg * 4096;
;     const LAS unsigned char* krp = shm + KOFF + 8192 + kr0 * 64 + ((g4 ^ (((kr0 >> 4) & 1) << 1)) << 4) + kg * 2048;
; #pragma unroll
;     for (int s_ = 0; s_ < 2; ++s_) vp[s_] = shm + VOFF + q16 * 128 + ((((s_ << 2) | g4) ^ ((q16 >> 1) & 7)) << 4);
;     const LAS unsigned char* vpk = kg ? vp[1] : vp[0];
;     ...
;     ATT_DMA_K(0, 0); ATT_DMA_V(0, 0); ATT_DMA_K(1, 1); ATT_DMA_K(2, 2);
;     bf16x8 qf[NQB * NDS];
;     {
;       const float c2 = (DQK == 64) ? C2_EVEN : C2_ODD; const bool lat = tq0 >= 0;
; #pragma unroll
;       for (int qb = 0; qb < NQB; ++qb) {
;           const bf16_t* qp = Q + (size_t)(qrow0 + qoff + qb * 16 + q16) * qpitch + g4 * 8;
;           bf16x8 raw[NDS];
; #pragma unroll
;           for (int ds = 0; ds < NDS; ++ds) raw[ds] = *(const bf16x8*)(qp + ds * 32);
;           float x[NDS][8];
; #pragma unroll
;           for (int ds = 0; ds < NDS; ++ds)
; #pragma unroll
;               for (int j = 0; j < 8; ++j) x[ds][j] = __uint_as_float(((unsigned)(unsigned short)raw[ds][j]) << 16);
.LBB0_641:
	s_bfe_u32 s24, s4, 0x40005
	s_ashr_i32 s5, s4, 9
	s_mul_i32 s6, s24, 0xc0
	s_add_u32 s46, s8, s6
	s_addc_u32 s47, s9, 0
	s_lshl_b32 s6, s24, 7
	s_add_u32 s50, s10, s6
	s_addc_u32 s51, s11, 0
	s_mul_i32 s6, s24, 0x840000
	s_add_u32 s52, s22, s6
	s_mov_b64 s[6:7], s[0:1]
	s_load_dwordx2 s[6:7], s[6:7], 0x98
	s_addc_u32 s53, s23, 0
	s_lshl_b32 s4, s4, 8
	s_mul_i32 s40, s5, 0x2100
	s_and_b32 s31, s4, 0x1f00
	s_add_i32 s25, s40, s31
	s_lshl_b64 s[4:5], s[20:21], 2
	s_waitcnt lgkmcnt(0)
	s_add_u32 s44, s6, s4
	s_addc_u32 s45, s7, s5
	v_readfirstlane_b32 s4, v0
	s_cmpk_gt_u32 s4, 0xff
	s_mov_b64 s[4:5], -1
	s_cbranch_scc0 .LBB0_648
	v_mov_b32_e32 v236, v0
	v_mov_b64_e32 v[6:7], s[52:53]
	v_readfirstlane_b32 s38, v236
	s_ashr_i32 s4, s38, 6
	v_bfe_u32 v2, v236, 3, 3
	v_lshl_or_b32 v8, s4, 3, v2
	v_ashrrev_i32_e32 v3, 1, v8
	v_and_b32_e32 v4, 1, v3
	s_lshl_b32 s5, s4, 1
	s_lshr_b32 s7, s38, 5
	v_and_b32_e32 v2, 7, v236
	s_and_b32 s6, s5, 2
	v_and_or_b32 v4, s7, 4, v4
	s_and_b32 s30, s4, 3
	v_bitop3_b32 v9, v4, v2, s6 bitop3:0x36
	v_bfe_u32 v4, v236, 2, 4
	v_add_u32_e32 v2, s40, v8
	v_lshl_or_b32 v4, s30, 4, v4
	v_xor_b32_e32 v10, v3, v236
	v_ashrrev_i32_e32 v3, 31, v2
	v_or_b32_e32 v4, s40, v4
	v_lshlrev_b64 v[2:3], 11, v[2:3]
	v_and_b32_e32 v12, 3, v236
	v_ashrrev_i32_e32 v5, 31, v4
	v_bitop3_b32 v11, s5, v12, 2 bitop3:0x6c
	v_lshlrev_b64 v[4:5], 6, v[4:5]
	s_lshl_b32 s42, s4, 10
	s_lshl_b32 s6, s30, 10
	v_lshl_add_u64 v[2:3], s[50:51], 0, v[2:3]
	v_lshlrev_b32_e32 v194, 4, v9
	s_ashr_i32 s41, s40, 31
	s_add_i32 s42, s42, 0
	v_lshl_add_u64 v[4:5], s[28:29], 0, v[4:5]
	v_mad_i64_i32 v[6:7], s[4:5], v8, s91, v[6:7]
	v_lshl_add_u64 v[192:193], v[2:3], 0, v[194:195]
	v_lshlrev_b32_e32 v194, 4, v11
	v_lshlrev_b32_e32 v2, 4, v10
	s_add_i32 s43, s6, 0
	s_mov_b32 s4, m0
	s_mov_b32 m0, s42
	s_nop 0
	global_load_lds_dwordx4 v[192:193], off
	s_mov_b32 m0, s4
	v_lshl_add_u64 v[6:7], s[40:41], 1, v[6:7]
	v_lshl_add_u64 v[204:205], v[4:5], 0, v[194:195]
	v_and_b32_e32 v194, 0x70, v2
	s_addk_i32 s43, 0x2000
	s_mov_b32 s4, m0
	s_mov_b32 m0, s43
	s_nop 0
	global_load_lds_dwordx4 v[204:205], off
	s_mov_b32 m0, s4
	s_add_i32 s41, s42, 0x9000
	v_lshl_add_u64 v[206:207], v[6:7], 0, v[194:195]
	s_mov_b32 s4, m0
	s_mov_b32 m0, s41
	s_nop 0
	global_load_lds_dwordx4 v[206:207], off
	s_mov_b32 m0, s4
	s_mov_b64 s[4:5], 0x20000
	v_lshl_add_u64 v[2:3], v[192:193], 0, s[4:5]
	s_add_i32 s4, s42, 0x3000
	s_mov_b32 s5, m0
	s_mov_b32 m0, s4
	s_nop 0
	global_load_lds_dwordx4 v[2:3], off
	s_mov_b32 m0, s5
	v_lshl_add_u64 v[2:3], v[204:205], 0, s[60:61]
	s_add_i32 s4, s43, 0x3000
	s_mov_b32 s5, m0
	s_mov_b32 m0, s4
	s_nop 0
	global_load_lds_dwordx4 v[2:3], off
	s_mov_b32 m0, s5
	s_mov_b64 s[4:5], 0x40000
	v_lshl_add_u64 v[2:3], v[192:193], 0, s[4:5]
	s_add_i32 s4, s42, 0x6000
	s_mov_b32 s5, m0
	s_mov_b32 m0, s4
	s_nop 0
	global_load_lds_dwordx4 v[2:3], off
	s_mov_b32 m0, s5
	s_mov_b64 s[4:5], 0x2000
	v_and_b32_e32 v237, 15, v236
	v_lshl_add_u64 v[2:3], v[204:205], 0, s[4:5]
	s_add_i32 s4, s43, 0x6000
	s_mov_b32 s5, m0
	s_mov_b32 m0, s4
	s_nop 0
	global_load_lds_dwordx4 v[2:3], off
	s_mov_b32 m0, s5
	v_lshl_or_b32 v2, s30, 6, v237
	v_and_b32_e32 v8, 48, v236
	v_or_b32_e32 v6, s25, v2
	v_mov_b32_e32 v9, v195
	v_lshl_add_u64 v[2:3], s[46:47], 0, v[8:9]
	v_or_b32_e32 v7, 16, v6
	v_mad_i64_i32 v[4:5], s[4:5], v6, s90, v[2:3]
	v_mad_i64_i32 v[10:11], s[4:5], v7, s90, v[2:3]
	v_or_b32_e32 v7, 32, v6
	v_or_b32_e32 v6, 48, v6
	v_mad_i64_i32 v[14:15], s[4:5], v7, s90, v[2:3]
	v_mad_i64_i32 v[16:17], s[4:5], v6, s90, v[2:3]
	global_load_dwordx4 v[54:57], v[4:5], off offset:64
	global_load_dwordx4 v[62:65], v[10:11], off offset:64
	global_load_dwordx4 v[84:87], v[14:15], off offset:64
	global_load_dwordx4 v[122:125], v[16:17], off offset:64
	global_load_dwordx4 v[138:141], v[4:5], off
	global_load_dwordx4 v[144:147], v[10:11], off
	global_load_dwordx4 v[80:83], v[14:15], off
	global_load_dwordx4 v[6:9], v[16:17], off
	s_lshr_b32 s4, s31, 6
	v_and_b32_e32 v194, 63, v236
	v_lshlrev_b32_e32 v2, 1, v236
	s_or_b32 s4, s4, s30
	v_and_or_b32 v239, v2, 24, v12
	v_bfe_u32 v241, v236, 3, 1
	v_mov_b32_e32 v18, s4
	v_cmp_gt_u32_e32 vcc, 32, v194
	v_or_b32_e32 v19, 16, v237
	v_bfe_u32 v238, v236, 4, 2
	s_ashr_i32 s16, s38, 8
	v_bfe_u32 v242, v236, 1, 2
	v_lshlrev_b32_e32 v243, 2, v241
	v_lshl_add_u32 v240, v239, 7, 0
	v_cndmask_b32_e32 v12, v237, v18, vcc
	v_cndmask_b32_e32 v19, v19, v18, vcc
	v_lshl_add_u32 v244, s16, 12, v240
	v_bitop3_b32 v2, v243, v238, v242 bitop3:0x36
	v_lshlrev_b32_e32 v12, 6, v12
	v_lshlrev_b32_e32 v19, 6, v19
	v_lshl_add_u32 v203, v2, 4, v244
	global_load_dwordx4 v[2:5], v[4:5], off offset:128
	s_nop 0
	global_load_dwordx4 v[112:115], v12, s[36:37] offset:48
	global_load_dwordx4 v[108:111], v12, s[36:37] offset:32
	global_load_dwordx4 v[104:107], v12, s[36:37] offset:16
	global_load_dwordx4 v[100:103], v12, s[36:37]
	s_nop 0
	global_load_dwordx4 v[10:13], v[10:11], off offset:128
	s_nop 0
	global_load_dwordx4 v[96:99], v19, s[36:37] offset:48
	global_load_dwordx4 v[92:95], v19, s[36:37] offset:32
	global_load_dwordx4 v[88:91], v19, s[36:37] offset:16
	global_load_dwordx4 v[58:61], v19, s[36:37]
	global_load_dwordx4 v[34:37], v[14:15], off offset:128
	v_or_b32_e32 v14, 32, v237
	v_cndmask_b32_e32 v14, v14, v18, vcc
	v_lshlrev_b32_e32 v14, 6, v14
	global_load_dwordx4 v[76:79], v14, s[36:37] offset:48
	global_load_dwordx4 v[70:73], v14, s[36:37] offset:32
	global_load_dwordx4 v[66:69], v14, s[36:37] offset:16
	global_load_dwordx4 v[50:53], v14, s[36:37]
	global_load_dwordx4 v[46:49], v[16:17], off offset:128
	v_or_b32_e32 v14, 48, v237
	v_cndmask_b32_e32 v14, v14, v18, vcc
	v_lshlrev_b32_e32 v18, 6, v14
	v_lshlrev_b32_e32 v162, 5, v238
	global_load_dwordx4 v[14:17], v18, s[36:37] offset:48
	global_load_dwordx4 v[20:23], v18, s[36:37] offset:32
	global_load_dwordx4 v[24:27], v18, s[36:37] offset:16
	global_load_dwordx4 v[30:33], v18, s[36:37]
	global_load_dwordx4 v[38:41], v162, s[44:45] offset:144
	global_load_dwordx4 v[42:45], v162, s[44:45] offset:128
	v_and_b32_e32 v160, 16, v236
	v_cmp_eq_u32_e32 vcc, 0, v160
	s_mov_b32 s6, 0x3d000000
	s_brev_b32 s7, 60
	s_mov_b32 s4, 0x358637bd
	s_mov_b32 s7, 0x3c800000
	v_mov_b64_e32 v[170:171], s[4:5]
	s_mov_b32 s48, 2
	s_waitcnt vmcnt(26)
; template <int DQK, int DV, bool LEAD> ...
;     ...
;           float x[NDS][8];
; #pragma unroll
;           for (int ds = 0; ds < NDS; ++ds)
; #pragma unroll
;               for (int j = 0; j < 8; ++j) x[ds][j] = __uint_as_float(((unsigned)(unsigned short)raw[ds][j]) << 16);
;           const int tq = tq0 + qoff + qb * 16 + q16, prow = (tq >> 6) & 127, pcol = tq & 63;
;           float sn = 0.f;
; #pragma unroll
;           for (int ds = 0; ds < 2; ++ds)
; #pragma unroll
;               for (int j = 0; j < 8; ++j) sn += x[ds][j] * x[ds][j];
;           sn = lanes4_sum(sn);
;     ...
;               float sr = 0.f;
; #pragma unroll
;               for (int j = 0; j < 8; ++j) sr += x[2][j] * x[2][j];
;               sr = lanes4_sum(sr);
	v_and_b32_e32 v117, 0xffff0000, v125
	s_waitcnt vmcnt(25)
	v_and_b32_e32 v191, 0xffff0000, v138
	v_lshlrev_b32_e32 v190, 16, v138
	v_lshlrev_b32_e32 v116, 16, v125
	s_waitcnt vmcnt(22)
	v_and_b32_e32 v127, 0xffff0000, v8
	v_lshlrev_b32_e32 v126, 16, v8
	v_mul_f32_e32 v8, v191, v191
	v_and_b32_e32 v119, 0xffff0000, v124
	v_lshlrev_b32_e32 v118, 16, v124
	v_and_b32_e32 v125, 0xffff0000, v9
	v_lshlrev_b32_e32 v124, 16, v9
	v_and_b32_e32 v211, 0xffff0000, v139
	v_lshlrev_b32_e32 v210, 16, v139
	v_pk_fma_f32 v[8:9], v[190:191], v[190:191], v[8:9] op_sel_hi:[1,1,0]
	v_and_b32_e32 v187, 0xffff0000, v141
	v_lshlrev_b32_e32 v186, 16, v141
	v_and_b32_e32 v189, 0xffff0000, v140
	v_lshlrev_b32_e32 v188, 16, v140
	v_and_b32_e32 v141, 0xffff0000, v82
	v_lshlrev_b32_e32 v140, 16, v82
	v_pk_fma_f32 v[8:9], v[210:211], v[210:211], v[8:9]
	v_mul_f32_e32 v82, v211, v211
	v_pk_add_f32 v[8:9], v[82:83], v[8:9] op_sel_hi:[0,1]
	v_pk_fma_f32 v[8:9], v[188:189], v[188:189], v[8:9]
	v_mul_f32_e32 v82, v189, v189
	v_pk_add_f32 v[8:9], v[82:83], v[8:9] op_sel_hi:[0,1]
	v_pk_fma_f32 v[8:9], v[186:187], v[186:187], v[8:9]
	v_mul_f32_e32 v82, v187, v187
	v_and_b32_e32 v185, 0xffff0000, v54
	v_lshlrev_b32_e32 v184, 16, v54
	v_pk_add_f32 v[8:9], v[82:83], v[8:9] op_sel_hi:[0,1]
	v_pk_fma_f32 v[8:9], v[184:185], v[184:185], v[8:9]
	v_mul_f32_e32 v82, v185, v185
	v_and_b32_e32 v179, 0xffff0000, v55
	v_lshlrev_b32_e32 v178, 16, v55
	v_pk_add_f32 v[8:9], v[82:83], v[8:9] op_sel_hi:[0,1]
	v_pk_fma_f32 v[8:9], v[178:179], v[178:179], v[8:9]
	v_mul_f32_e32 v82, v179, v179
	v_and_b32_e32 v177, 0xffff0000, v56
	v_lshlrev_b32_e32 v176, 16, v56
	v_pk_add_f32 v[8:9], v[82:83], v[8:9] op_sel_hi:[0,1]
	v_pk_fma_f32 v[8:9], v[176:177], v[176:177], v[8:9]
	v_mul_f32_e32 v82, v177, v177
	v_and_b32_e32 v175, 0xffff0000, v57
	v_lshlrev_b32_e32 v174, 16, v57
	v_pk_add_f32 v[8:9], v[82:83], v[8:9] op_sel_hi:[0,1]
	v_pk_fma_f32 v[8:9], v[174:175], v[174:175], v[8:9]
	v_mul_f32_e32 v82, v175, v175
	v_pk_add_f32 v[8:9], v[82:83], v[8:9] op_sel_hi:[0,1]
	v_and_b32_e32 v129, 0xffff0000, v7
	v_lshlrev_b32_e32 v128, 16, v7
	v_mov_b32_e32 v7, v8
	s_nop 1
	v_permlane16_swap_b32_e32 v8, v7
	v_add_f32_e32 v7, v8, v7
	v_mov_b32_e32 v9, v7
	v_and_b32_e32 v167, 0xffff0000, v144
	s_nop 0
	v_permlane32_swap_b32_e32 v7, v9
	v_lshlrev_b32_e32 v166, 16, v144
	v_mul_f32_e32 v8, v167, v167
	v_and_b32_e32 v137, 0xffff0000, v83
	v_lshlrev_b32_e32 v136, 16, v83
	v_and_b32_e32 v159, 0xffff0000, v145
	v_lshlrev_b32_e32 v158, 16, v145
	v_pk_fma_f32 v[82:83], v[166:167], v[166:167], v[8:9] op_sel_hi:[1,1,0]
	v_mul_f32_e32 v8, v159, v159
	v_pk_fma_f32 v[82:83], v[158:159], v[158:159], v[82:83]
	v_and_b32_e32 v157, 0xffff0000, v146
	v_lshlrev_b32_e32 v156, 16, v146
	v_pk_add_f32 v[82:83], v[8:9], v[82:83] op_sel_hi:[0,1]
	v_pk_fma_f32 v[82:83], v[156:157], v[156:157], v[82:83]
	v_mul_f32_e32 v8, v157, v157
	v_and_b32_e32 v155, 0xffff0000, v147
	v_lshlrev_b32_e32 v154, 16, v147
	v_pk_add_f32 v[82:83], v[8:9], v[82:83] op_sel_hi:[0,1]
	v_pk_fma_f32 v[82:83], v[154:155], v[154:155], v[82:83]
	v_mul_f32_e32 v8, v155, v155
	v_and_b32_e32 v153, 0xffff0000, v62
	v_lshlrev_b32_e32 v152, 16, v62
	v_pk_add_f32 v[82:83], v[8:9], v[82:83] op_sel_hi:[0,1]
	v_pk_fma_f32 v[82:83], v[152:153], v[152:153], v[82:83]
	v_mul_f32_e32 v8, v153, v153
	v_and_b32_e32 v151, 0xffff0000, v63
	v_lshlrev_b32_e32 v150, 16, v63
	v_pk_add_f32 v[82:83], v[8:9], v[82:83] op_sel_hi:[0,1]
	v_pk_fma_f32 v[82:83], v[150:151], v[150:151], v[82:83]
	v_mul_f32_e32 v8, v151, v151
	v_and_b32_e32 v29, 0xffff0000, v64
	v_lshlrev_b32_e32 v28, 16, v64
	v_pk_add_f32 v[82:83], v[8:9], v[82:83] op_sel_hi:[0,1]
	v_pk_fma_f32 v[82:83], v[28:29], v[28:29], v[82:83]
	v_mul_f32_e32 v8, v29, v29
	v_and_b32_e32 v19, 0xffff0000, v65
	v_lshlrev_b32_e32 v18, 16, v65
	v_pk_add_f32 v[82:83], v[8:9], v[82:83] op_sel_hi:[0,1]
	v_pk_fma_f32 v[82:83], v[18:19], v[18:19], v[82:83]
	v_mul_f32_e32 v8, v19, v19
	v_pk_add_f32 v[82:83], v[8:9], v[82:83] op_sel_hi:[0,1]
	v_mov_b32_e32 v8, v82
	s_nop 1
	v_permlane16_swap_b32_e32 v82, v8
	v_and_b32_e32 v149, 0xffff0000, v80
	v_add_f32_e32 v181, v82, v8
	v_lshlrev_b32_e32 v148, 16, v80
	v_mul_f32_e32 v8, v149, v149
	v_and_b32_e32 v143, 0xffff0000, v81
	v_lshlrev_b32_e32 v142, 16, v81
	v_pk_fma_f32 v[80:81], v[148:149], v[148:149], v[8:9] op_sel_hi:[1,1,0]
	v_mul_f32_e32 v8, v143, v143
	v_pk_fma_f32 v[80:81], v[142:143], v[142:143], v[80:81]
	v_and_b32_e32 v135, 0xffff0000, v84
	v_pk_add_f32 v[80:81], v[8:9], v[80:81] op_sel_hi:[0,1]
	v_pk_fma_f32 v[80:81], v[140:141], v[140:141], v[80:81]
	v_mul_f32_e32 v8, v141, v141
	v_pk_add_f32 v[80:81], v[8:9], v[80:81] op_sel_hi:[0,1]
	v_pk_fma_f32 v[80:81], v[136:137], v[136:137], v[80:81]
	v_mul_f32_e32 v8, v137, v137
	v_lshlrev_b32_e32 v134, 16, v84
	v_pk_add_f32 v[80:81], v[8:9], v[80:81] op_sel_hi:[0,1]
	v_pk_fma_f32 v[80:81], v[134:135], v[134:135], v[80:81]
	v_mul_f32_e32 v8, v135, v135
	v_and_b32_e32 v133, 0xffff0000, v85
	v_lshlrev_b32_e32 v132, 16, v85
	v_pk_add_f32 v[80:81], v[8:9], v[80:81] op_sel_hi:[0,1]
	v_pk_fma_f32 v[80:81], v[132:133], v[132:133], v[80:81]
	v_mul_f32_e32 v8, v133, v133
	v_and_b32_e32 v131, 0xffff0000, v86
	v_lshlrev_b32_e32 v130, 16, v86
	v_pk_add_f32 v[80:81], v[8:9], v[80:81] op_sel_hi:[0,1]
	v_pk_fma_f32 v[80:81], v[130:131], v[130:131], v[80:81]
	v_mul_f32_e32 v8, v131, v131
	v_and_b32_e32 v75, 0xffff0000, v87
	v_lshlrev_b32_e32 v74, 16, v87
	v_pk_add_f32 v[80:81], v[8:9], v[80:81] op_sel_hi:[0,1]
	v_pk_fma_f32 v[80:81], v[74:75], v[74:75], v[80:81]
	v_mul_f32_e32 v8, v75, v75
	v_pk_add_f32 v[80:81], v[8:9], v[80:81] op_sel_hi:[0,1]
	v_mov_b32_e32 v8, v80
; __device__ __forceinline__ unsigned cvtpk(float lo, float hi) { f32x2 v = {lo, hi}; bf16x2_t b = __builtin_convertvector(v, bf16x2_t); return __builtin_bit_cast(unsigned, b); }
; template <int DQK, int DV, bool LEAD> ...
;     ...
;               for (int j = 0; j < 8; ++j) sn += x[ds][j] * x[ds][j];
;           sn = lanes4_sum(sn);
;           const float rn = rsqrtf(sn * (1.f / 64.f) + EPS);
; #pragma unroll
;           for (int ds = 0; ds < 2; ++ds)
; #pragma unroll
;               for (int j = 0; j < 8; ++j) x[ds][j] *= rn * qgain[32 * ds + 8 * g4 + j];
;           if constexpr (DQK == 64) {
; #pragma unroll
;               for (int ds = 0; ds < 2; ++ds)
; #pragma unroll
;                   for (int j = 0; j < 8; ++j) {
;                       auto rr = __builtin_amdgcn_permlane32_swap(__float_as_uint(x[ds][j]), __float_as_uint(x[ds][j]), false, false);
;                       const float other = hi ? __uint_as_float(rr[0]) : __uint_as_float(rr[1]);
;                       float cc = 1.f, sg = 0.f;
;                       if (lat) { const f32x2 cs = rope[(ds ? pcol : prow) * 16 + 8 * (g4 & 1) + j]; cc = cs.x; sg = hi ? cs.y : -cs.y; }
;                       x[ds][j] = x[ds][j] * cc + other * sg; }
;           } else {
;               float sr = 0.f;
; #pragma unroll
;               for (int j = 0; j < 8; ++j) sr += x[2][j] * x[2][j];
;               sr = lanes4_sum(sr);
;               const float rq = rsqrtf(sr * (1.f / 32.f) + EPS);
; #pragma unroll
;               for (int j = 0; j < 8; ++j) { const float av = x[2][j] * rq * qgain[64 + 8 * g4 + j];
;                   auto rr = __builtin_amdgcn_permlane16_swap(__float_as_uint(av), __float_as_uint(av), false, false);
;                   const float other = (g4 & 1) ? __uint_as_float(rr[0]) : __uint_as_float(rr[1]);
;                   float cc = 1.f, sg = 0.f;
;                   if (lat) { const f32x2 cs = rope[((g4 & 2) ? pcol : prow) * 8 + j]; cc = cs.x; sg = (g4 & 1) ? cs.y : -cs.y; }
;                   x[2][j] = av * cc + other * sg; }
;           }
; #pragma unroll
;           for (int ds = 0; ds < NDS; ++ds) { u32x4 w;
; #pragma unroll
;               for (int i = 0; i < 4; ++i) w[i] = cvtpk(x[ds][2 * i] * c2, x[ds][2 * i + 1] * c2);
;               qf[qb * NDS + ds] = __builtin_bit_cast(bf16x8, w); }
	v_and_b32_e32 v139, 0xffff0000, v6
	s_nop 0
	v_permlane16_swap_b32_e32 v80, v8
	v_lshlrev_b32_e32 v138, 16, v6
	v_mul_f32_e32 v6, v139, v139
	v_add_f32_e32 v161, v80, v8
	v_pk_fma_f32 v[80:81], v[138:139], v[138:139], v[6:7] op_sel_hi:[1,1,0]
	v_mul_f32_e32 v6, v129, v129
	v_pk_fma_f32 v[80:81], v[128:129], v[128:129], v[80:81]
	global_load_dwordx4 v[54:57], v162, s[44:45] offset:16
	global_load_dwordx4 v[62:65], v162, s[44:45]
	v_pk_add_f32 v[80:81], v[6:7], v[80:81] op_sel_hi:[0,1]
	v_pk_fma_f32 v[80:81], v[126:127], v[126:127], v[80:81]
	v_mul_f32_e32 v6, v127, v127
	v_pk_add_f32 v[80:81], v[6:7], v[80:81] op_sel_hi:[0,1]
	v_pk_fma_f32 v[80:81], v[124:125], v[124:125], v[80:81]
	v_mul_f32_e32 v6, v125, v125
	v_and_b32_e32 v121, 0xffff0000, v123
	v_lshlrev_b32_e32 v120, 16, v123
	v_and_b32_e32 v123, 0xffff0000, v122
	v_lshlrev_b32_e32 v122, 16, v122
	v_pk_add_f32 v[80:81], v[6:7], v[80:81] op_sel_hi:[0,1]
	v_pk_fma_f32 v[80:81], v[122:123], v[122:123], v[80:81]
	v_mul_f32_e32 v6, v123, v123
	v_pk_add_f32 v[80:81], v[6:7], v[80:81] op_sel_hi:[0,1]
	v_pk_fma_f32 v[80:81], v[120:121], v[120:121], v[80:81]
	v_mul_f32_e32 v6, v121, v121
	v_pk_add_f32 v[80:81], v[6:7], v[80:81] op_sel_hi:[0,1]
	v_pk_fma_f32 v[80:81], v[118:119], v[118:119], v[80:81]
	v_mul_f32_e32 v6, v119, v119
	v_pk_add_f32 v[80:81], v[6:7], v[80:81] op_sel_hi:[0,1]
	v_pk_fma_f32 v[80:81], v[116:117], v[116:117], v[80:81]
	v_mul_f32_e32 v6, v117, v117
	v_pk_add_f32 v[80:81], v[6:7], v[80:81] op_sel_hi:[0,1]
	v_mov_b32_e32 v6, v80
	s_nop 1
	v_permlane16_swap_b32_e32 v80, v6
	v_add_f32_e32 v145, v80, v6
	global_load_dwordx4 v[80:83], v162, s[44:45] offset:272
	global_load_dwordx4 v[84:87], v162, s[44:45] offset:256
	s_waitcnt vmcnt(25)
	v_and_b32_e32 v201, 0xffff0000, v2
	v_lshlrev_b32_e32 v200, 16, v2
	v_mul_f32_e32 v2, v201, v201
	s_waitcnt vmcnt(20)
	v_and_b32_e32 v213, 0xffff0000, v13
	v_lshlrev_b32_e32 v212, 16, v13
	v_and_b32_e32 v217, 0xffff0000, v12
	v_lshlrev_b32_e32 v216, 16, v12
	v_and_b32_e32 v13, 0xffff0000, v3
	v_lshlrev_b32_e32 v12, 16, v3
	v_pk_fma_f32 v[2:3], v[200:201], v[200:201], v[2:3] op_sel_hi:[1,1,0]
	v_cndmask_b32_e64 v219, v115, -v115, vcc
	v_cndmask_b32_e64 v218, v113, -v113, vcc
	v_mov_b32_e32 v113, v114
	s_waitcnt vmcnt(14)
	v_cndmask_b32_e64 v115, v79, -v79, vcc
	v_cndmask_b32_e64 v114, v77, -v77, vcc
	v_mov_b32_e32 v77, v78
	s_waitcnt vmcnt(9)
	v_cndmask_b32_e64 v79, v17, -v17, vcc
	v_cndmask_b32_e64 v78, v15, -v15, vcc
	v_mov_b32_e32 v15, v16
	v_and_b32_e32 v17, 0xffff0000, v4
	v_lshlrev_b32_e32 v16, 16, v4
	v_pk_fma_f32 v[2:3], v[12:13], v[12:13], v[2:3]
	v_mul_f32_e32 v4, v13, v13
	v_pk_add_f32 v[2:3], v[4:5], v[2:3] op_sel_hi:[0,1]
	v_pk_fma_f32 v[2:3], v[16:17], v[16:17], v[2:3]
	v_mul_f32_e32 v4, v17, v17
	v_and_b32_e32 v221, 0xffff0000, v5
	v_lshlrev_b32_e32 v220, 16, v5
	v_pk_add_f32 v[2:3], v[4:5], v[2:3] op_sel_hi:[0,1]
	v_pk_fma_f32 v[2:3], v[220:221], v[220:221], v[2:3]
	v_mul_f32_e32 v4, v221, v221
	v_pk_add_f32 v[2:3], v[4:5], v[2:3] op_sel_hi:[0,1]
	v_mov_b32_e32 v3, v2
	s_nop 1
	v_permlane16_swap_b32_e32 v2, v3
	v_add_f32_e32 v6, v2, v3
	v_mov_b32_e32 v8, v6
	s_nop 1
	v_permlane32_swap_b32_e32 v6, v8
	v_pk_add_f32 v[2:3], v[6:7], v[8:9]
	v_mov_b32_e32 v147, v145
	v_pk_fma_f32 v[6:7], v[2:3], s[6:7], v[170:171] op_sel_hi:[1,1,0]
	s_nop 0
	v_permlane32_swap_b32_e32 v145, v147
	v_mul_f32_e32 v2, 0x4b800000, v7
	v_cmp_gt_f32_e64 s[4:5], s95, v7
	v_cndmask_b32_e64 v215, v95, -v95, vcc
	v_cndmask_b32_e64 v214, v93, -v93, vcc
	v_cndmask_b32_e64 v2, v7, v2, s[4:5]
	v_rsq_f32_e32 v2, v2
	v_mov_b32_e32 v93, v94
	s_waitcnt vmcnt(8)
	v_cndmask_b32_e64 v95, v23, -v23, vcc
	v_cndmask_b32_e64 v94, v21, -v21, vcc
	v_mul_f32_e32 v3, 0x45800000, v2
	v_cndmask_b32_e64 v144, v2, v3, s[4:5]
	s_waitcnt vmcnt(5)
	v_pk_mul_f32 v[2:3], v[144:145], v[40:41] op_sel_hi:[0,1]
	v_pk_mul_f32 v[2:3], v[2:3], v[174:175]
	v_pk_mul_f32 v[4:5], v[144:145], v[38:39] op_sel_hi:[0,1]
	v_pk_mul_f32 v[2:3], v[2:3], s[82:83] op_sel_hi:[1,0]
	v_pk_mul_f32 v[8:9], v[4:5], v[176:177]
	v_cvt_pk_bf16_f32 v5, v2, v3
	v_pk_mul_f32 v[2:3], v[8:9], s[82:83] op_sel_hi:[1,0]
	s_waitcnt vmcnt(4)
	v_pk_mul_f32 v[8:9], v[42:43], v[144:145] op_sel_hi:[1,0]
	v_cvt_pk_bf16_f32 v4, v2, v3
	v_pk_mul_f32 v[2:3], v[144:145], v[44:45] op_sel_hi:[0,1]
	v_pk_mul_f32 v[2:3], v[2:3], v[178:179]
	v_pk_mul_f32 v[8:9], v[8:9], v[184:185]
	v_pk_mul_f32 v[2:3], v[2:3], s[82:83] op_sel_hi:[1,0]
	v_pk_mul_f32 v[8:9], v[8:9], s[82:83] op_sel_hi:[1,0]
	v_mov_b32_e32 v21, v22
	v_cvt_pk_bf16_f32 v3, v2, v3
	v_cvt_pk_bf16_f32 v2, v8, v9
	s_waitcnt vmcnt(3)
	v_pk_mul_f32 v[8:9], v[56:57], v[144:145] op_sel_hi:[1,0]
	v_pk_mul_f32 v[22:23], v[54:55], v[144:145] op_sel_hi:[1,0]
	v_pk_mul_f32 v[8:9], v[8:9], v[186:187]
	v_pk_mul_f32 v[22:23], v[22:23], v[188:189]
	v_pk_mul_f32 v[8:9], v[8:9], s[82:83] op_sel_hi:[1,0]
	v_pk_mul_f32 v[22:23], v[22:23], s[82:83] op_sel_hi:[1,0]
	v_and_b32_e32 v165, 0xffff0000, v37
	v_lshlrev_b32_e32 v164, 16, v37
	v_and_b32_e32 v173, 0xffff0000, v36
	v_lshlrev_b32_e32 v172, 16, v36
	v_cndmask_b32_e64 v37, v107, -v107, vcc
	v_cndmask_b32_e64 v36, v105, -v105, vcc
	v_mov_b32_e32 v105, v106
	v_and_b32_e32 v107, 0xffff0000, v11
	v_lshlrev_b32_e32 v106, 16, v11
	v_cvt_pk_bf16_f32 v9, v8, v9
	v_cvt_pk_bf16_f32 v8, v22, v23
	s_waitcnt vmcnt(2)
; __device__ __forceinline__ unsigned cvtpk(float lo, float hi) { f32x2 v = {lo, hi}; bf16x2_t b = __builtin_convertvector(v, bf16x2_t); return __builtin_bit_cast(unsigned, b); }
; template <int DQK, int DV, bool LEAD> ...
;     ...
;               float sr = 0.f;
; #pragma unroll
;               for (int j = 0; j < 8; ++j) sr += x[2][j] * x[2][j];
;               sr = lanes4_sum(sr);
;               const float rq = rsqrtf(sr * (1.f / 32.f) + EPS);
; #pragma unroll
;               for (int j = 0; j < 8; ++j) { const float av = x[2][j] * rq * qgain[64 + 8 * g4 + j];
;                   auto rr = __builtin_amdgcn_permlane16_swap(__float_as_uint(av), __float_as_uint(av), false, false);
;                   const float other = (g4 & 1) ? __uint_as_float(rr[0]) : __uint_as_float(rr[1]);
;                   float cc = 1.f, sg = 0.f;
;                   if (lat) { const f32x2 cs = rope[((g4 & 2) ? pcol : prow) * 8 + j]; cc = cs.x; sg = (g4 & 1) ? cs.y : -cs.y; }
;                   x[2][j] = av * cc + other * sg; }
;           }
; #pragma unroll
;           for (int ds = 0; ds < NDS; ++ds) { u32x4 w;
; #pragma unroll
;               for (int i = 0; i < 4; ++i) w[i] = cvtpk(x[ds][2 * i] * c2, x[ds][2 * i + 1] * c2);
;               qf[qb * NDS + ds] = __builtin_bit_cast(bf16x8, w); }
	v_pk_mul_f32 v[22:23], v[64:65], v[144:145] op_sel_hi:[1,0]
	v_mul_f32_e32 v11, 0x4b800000, v6
	v_cmp_gt_f32_e64 s[4:5], s95, v6
	v_pk_mul_f32 v[22:23], v[22:23], v[210:211]
	v_cndmask_b32_e64 v209, v99, -v99, vcc
	v_cndmask_b32_e64 v6, v6, v11, s[4:5]
	v_pk_mul_f32 v[22:23], v[22:23], s[82:83] op_sel_hi:[1,0]
	v_rsq_f32_e32 v11, v6
	v_cvt_pk_bf16_f32 v7, v22, v23
	v_cndmask_b32_e64 v23, v27, -v27, vcc
	v_cndmask_b32_e64 v22, v25, -v25, vcc
	v_mov_b32_e32 v25, v26
	v_pk_mul_f32 v[26:27], v[62:63], v[144:145] op_sel_hi:[1,0]
	v_cndmask_b32_e64 v208, v97, -v97, vcc
	v_pk_mul_f32 v[26:27], v[26:27], v[190:191]
	v_mov_b32_e32 v97, v98
	v_pk_mul_f32 v[26:27], v[26:27], s[82:83] op_sel_hi:[1,0]
	v_and_b32_e32 v99, 0xffff0000, v49
	v_cvt_pk_bf16_f32 v6, v26, v27
	v_mul_f32_e32 v26, 0x45800000, v11
	v_cndmask_b32_e64 v26, v11, v26, s[4:5]
	v_pk_mul_f32 v[176:177], v[26:27], v[12:13] op_sel_hi:[0,1]
	v_pk_mul_f32 v[12:13], v[26:27], v[220:221] op_sel_hi:[0,1]
	s_waitcnt vmcnt(1)
	v_pk_mul_f32 v[12:13], v[12:13], v[82:83]
	v_lshlrev_b32_e32 v98, 16, v49
	v_cndmask_b32_e64 v199, v111, -v111, vcc
	v_cndmask_b32_e64 v198, v109, -v109, vcc
	v_mov_b32_e32 v109, v110
	v_and_b32_e32 v111, 0xffff0000, v48
	v_lshlrev_b32_e32 v110, 16, v48
	v_and_b32_e32 v49, 0xffff0000, v35
	v_lshlrev_b32_e32 v48, 16, v35
	v_pk_mul_f32 v[174:175], v[26:27], v[200:201] op_sel_hi:[0,1]
	v_pk_mul_f32 v[16:17], v[26:27], v[16:17] op_sel_hi:[0,1]
	v_mov_b32_e32 v11, v12
	v_mov_b32_e32 v26, v12
	v_mov_b32_e32 v27, v13
	v_mov_b32_e32 v35, v13
	v_permlane16_swap_b32_e32 v11, v26
	s_nop 0
	v_permlane16_swap_b32_e32 v27, v35
	v_cndmask_b32_e32 v27, v27, v35, vcc
	v_cndmask_b32_e32 v26, v11, v26, vcc
	v_pk_mul_f32 v[26:27], v[218:219], v[26:27]
	v_pk_mul_f32 v[16:17], v[16:17], v[80:81]
	v_pk_fma_f32 v[12:13], v[12:13], v[112:113], v[26:27]
	v_mov_b32_e32 v11, v16
	v_pk_mul_f32 v[12:13], v[12:13], s[82:83] op_sel_hi:[1,0]
	v_mov_b32_e32 v26, v17
	v_cvt_pk_bf16_f32 v13, v12, v13
	v_mov_b32_e32 v12, v16
	v_mov_b32_e32 v27, v17
	s_nop 0
	v_permlane16_swap_b32_e32 v11, v12
	v_permlane16_swap_b32_e32 v26, v27
	v_cndmask_b32_e32 v27, v26, v27, vcc
	v_cndmask_b32_e32 v26, v11, v12, vcc
	v_pk_mul_f32 v[26:27], v[198:199], v[26:27]
	v_cndmask_b32_e64 v178, v101, -v101, vcc
	v_pk_fma_f32 v[16:17], v[16:17], v[108:109], v[26:27]
	v_mov_b32_e32 v101, v102
	v_pk_mul_f32 v[16:17], v[16:17], s[82:83] op_sel_hi:[1,0]
	v_cndmask_b32_e64 v179, v103, -v103, vcc
	v_cvt_pk_bf16_f32 v12, v16, v17
	s_waitcnt vmcnt(0)
	v_pk_mul_f32 v[16:17], v[86:87], v[176:177]
	v_mov_b32_e32 v183, v181
	v_mov_b32_e32 v11, v16
	v_mov_b32_e32 v26, v16
	v_mov_b32_e32 v27, v17
	v_mov_b32_e32 v35, v17
	v_permlane16_swap_b32_e32 v11, v26
	s_nop 0
	v_permlane16_swap_b32_e32 v27, v35
	v_cndmask_b32_e32 v27, v27, v35, vcc
	v_cndmask_b32_e32 v26, v11, v26, vcc
	v_pk_mul_f32 v[26:27], v[36:37], v[26:27]
	v_and_b32_e32 v37, 0xffff0000, v10
	v_pk_fma_f32 v[16:17], v[104:105], v[16:17], v[26:27]
	v_permlane32_swap_b32_e32 v181, v183
	v_pk_mul_f32 v[16:17], v[16:17], s[82:83] op_sel_hi:[1,0]
	v_cndmask_b32_e64 v169, v73, -v73, vcc
	v_cvt_pk_bf16_f32 v11, v16, v17
	v_pk_mul_f32 v[16:17], v[84:85], v[174:175]
	v_cndmask_b32_e64 v168, v71, -v71, vcc
	v_mov_b32_e32 v26, v16
	v_mov_b32_e32 v35, v16
	v_mov_b32_e32 v27, v17
	v_mov_b32_e32 v36, v17
	v_permlane16_swap_b32_e32 v26, v35
	s_nop 0
	v_permlane16_swap_b32_e32 v27, v36
	v_cndmask_b32_e32 v27, v27, v36, vcc
	v_cndmask_b32_e32 v26, v26, v35, vcc
	v_pk_mul_f32 v[16:17], v[100:101], v[16:17]
	v_lshlrev_b32_e32 v36, 16, v10
	v_mul_f32_e32 v10, v37, v37
	v_pk_fma_f32 v[16:17], v[178:179], v[26:27], v[16:17]
	v_pk_fma_f32 v[26:27], v[36:37], v[36:37], v[10:11] op_sel_hi:[1,1,0]
	v_mul_f32_e32 v10, v107, v107
	v_pk_fma_f32 v[26:27], v[106:107], v[106:107], v[26:27]
	v_pk_mul_f32 v[16:17], v[16:17], s[82:83] op_sel_hi:[1,0]
	v_pk_add_f32 v[26:27], v[10:11], v[26:27] op_sel_hi:[0,1]
	v_pk_fma_f32 v[26:27], v[216:217], v[216:217], v[26:27]
	v_mul_f32_e32 v10, v217, v217
	v_pk_add_f32 v[26:27], v[10:11], v[26:27] op_sel_hi:[0,1]
	v_pk_fma_f32 v[26:27], v[212:213], v[212:213], v[26:27]
	v_mul_f32_e32 v10, v213, v213
	v_pk_add_f32 v[26:27], v[10:11], v[26:27] op_sel_hi:[0,1]
	v_mov_b32_e32 v10, v26
	s_nop 1
	v_permlane16_swap_b32_e32 v26, v10
	v_add_f32_e32 v180, v26, v10
	v_mov_b32_e32 v182, v180
	s_nop 1
	v_permlane32_swap_b32_e32 v180, v182
	v_pk_add_f32 v[26:27], v[180:181], v[182:183]
	v_mov_b32_e32 v71, v72
	v_pk_fma_f32 v[26:27], v[26:27], s[6:7], v[170:171] op_sel_hi:[1,1,0]
	v_cndmask_b32_e64 v73, v91, -v91, vcc
	v_mul_f32_e32 v10, 0x4b800000, v27
	v_cmp_gt_f32_e64 s[4:5], s95, v27
	v_mul_f32_e32 v35, 0x4b800000, v26
	v_cndmask_b32_e64 v72, v89, -v89, vcc
	v_cndmask_b32_e64 v10, v27, v10, s[4:5]
	v_rsq_f32_e32 v27, v10
	v_cvt_pk_bf16_f32 v10, v16, v17
	v_mov_b32_e32 v89, v90
	v_cndmask_b32_e64 v91, v69, -v69, vcc
	v_mul_f32_e32 v16, 0x45800000, v27
	v_cndmask_b32_e64 v102, v27, v16, s[4:5]
	v_pk_mul_f32 v[16:17], v[40:41], v[102:103] op_sel_hi:[1,0]
	v_cmp_gt_f32_e64 s[4:5], s95, v26
	v_pk_mul_f32 v[16:17], v[16:17], v[18:19]
	v_pk_mul_f32 v[104:105], v[54:55], v[102:103] op_sel_hi:[1,0]
	v_pk_mul_f32 v[16:17], v[16:17], s[82:83] op_sel_hi:[1,0]
	v_cndmask_b32_e64 v26, v26, v35, s[4:5]
	v_cvt_pk_bf16_f32 v19, v16, v17
	v_pk_mul_f32 v[16:17], v[38:39], v[102:103] op_sel_hi:[1,0]
	v_pk_mul_f32 v[104:105], v[104:105], v[156:157]
	v_pk_mul_f32 v[16:17], v[16:17], v[28:29]
	v_pk_mul_f32 v[28:29], v[42:43], v[102:103] op_sel_hi:[1,0]
	v_pk_mul_f32 v[16:17], v[16:17], s[82:83] op_sel_hi:[1,0]
	v_pk_mul_f32 v[28:29], v[28:29], v[152:153]
	v_cvt_pk_bf16_f32 v18, v16, v17
; template <int DQK, int DV, bool LEAD> ...
;     ...
;           float sn = 0.f;
; #pragma unroll
;           for (int ds = 0; ds < 2; ++ds)
; #pragma unroll
;               for (int j = 0; j < 8; ++j) sn += x[ds][j] * x[ds][j];
;           sn = lanes4_sum(sn);
;           const float rn = rsqrtf(sn * (1.f / 64.f) + EPS);
; #pragma unroll
;           for (int ds = 0; ds < 2; ++ds)
; #pragma unroll
;               for (int j = 0; j < 8; ++j) x[ds][j] *= rn * qgain[32 * ds + 8 * g4 + j];
;           if constexpr (DQK == 64) {
; #pragma unroll
;               for (int ds = 0; ds < 2; ++ds)
; #pragma unroll
;                   for (int j = 0; j < 8; ++j) {
;                       auto rr = __builtin_amdgcn_permlane32_swap(__float_as_uint(x[ds][j]), __float_as_uint(x[ds][j]), false, false);
;                       const float other = hi ? __uint_as_float(rr[0]) : __uint_as_float(rr[1]);
;                       float cc = 1.f, sg = 0.f;
;                       if (lat) { const f32x2 cs = rope[(ds ? pcol : prow) * 16 + 8 * (g4 & 1) + j]; cc = cs.x; sg = hi ? cs.y : -cs.y; }
;                       x[ds][j] = x[ds][j] * cc + other * sg; }
;           } else {
;               float sr = 0.f;
; #pragma unroll
;               for (int j = 0; j < 8; ++j) sr += x[2][j] * x[2][j];
;               sr = lanes4_sum(sr);
;               const float rq = rsqrtf(sr * (1.f / 32.f) + EPS);
; #pragma unroll
;               for (int j = 0; j < 8; ++j) { const float av = x[2][j] * rq * qgain[64 + 8 * g4 + j];
;                   auto rr = __builtin_amdgcn_permlane16_swap(__float_as_uint(av), __float_as_uint(av), false, false);
;                   const float other = (g4 & 1) ? __uint_as_float(rr[0]) : __uint_as_float(rr[1]);
;                   float cc = 1.f, sg = 0.f;
;                   if (lat) { const f32x2 cs = rope[((g4 & 2) ? pcol : prow) * 8 + j]; cc = cs.x; sg = (g4 & 1) ? cs.y : -cs.y; }
;                   x[2][j] = av * cc + other * sg; }
;           }
; #pragma unroll
;           for (int ds = 0; ds < NDS; ++ds) { u32x4 w;
; #pragma unroll
;               for (int i = 0; i < 4; ++i) w[i] = cvtpk(x[ds][2 * i] * c2, x[ds][2 * i + 1] * c2);
;               qf[qb * NDS + ds] = __builtin_bit_cast(bf16x8, w); }
	v_pk_mul_f32 v[16:17], v[44:45], v[102:103] op_sel_hi:[1,0]
	v_pk_mul_f32 v[28:29], v[28:29], s[82:83] op_sel_hi:[1,0]
	v_pk_mul_f32 v[16:17], v[16:17], v[150:151]
	v_rsq_f32_e32 v35, v26
	v_pk_mul_f32 v[16:17], v[16:17], s[82:83] op_sel_hi:[1,0]
	v_pk_mul_f32 v[104:105], v[104:105], s[82:83] op_sel_hi:[1,0]
	v_cvt_pk_bf16_f32 v17, v16, v17
	v_cvt_pk_bf16_f32 v16, v28, v29
	v_pk_mul_f32 v[28:29], v[56:57], v[102:103] op_sel_hi:[1,0]
	v_cndmask_b32_e64 v90, v67, -v67, vcc
	v_pk_mul_f32 v[28:29], v[28:29], v[154:155]
	v_mov_b32_e32 v67, v68
	v_pk_mul_f32 v[28:29], v[28:29], s[82:83] op_sel_hi:[1,0]
	v_and_b32_e32 v69, 0xffff0000, v47
	v_cvt_pk_bf16_f32 v29, v28, v29
	v_cvt_pk_bf16_f32 v28, v104, v105
	v_pk_mul_f32 v[104:105], v[64:65], v[102:103] op_sel_hi:[1,0]
	v_pk_mul_f32 v[102:103], v[62:63], v[102:103] op_sel_hi:[1,0]
	v_lshlrev_b32_e32 v68, 16, v47
	v_pk_mul_f32 v[102:103], v[102:103], v[166:167]
	v_pk_mul_f32 v[104:105], v[104:105], v[158:159]
	v_pk_mul_f32 v[102:103], v[102:103], s[82:83] op_sel_hi:[1,0]
	v_mul_f32_e32 v47, 0x45800000, v35
	v_pk_mul_f32 v[104:105], v[104:105], s[82:83] op_sel_hi:[1,0]
	v_cvt_pk_bf16_f32 v26, v102, v103
	v_cndmask_b32_e64 v102, v35, v47, s[4:5]
	v_cvt_pk_bf16_f32 v27, v104, v105
	v_pk_mul_f32 v[104:105], v[102:103], v[36:37] op_sel_hi:[0,1]
	v_pk_mul_f32 v[36:37], v[102:103], v[212:213] op_sel_hi:[0,1]
	v_pk_mul_f32 v[36:37], v[82:83], v[36:37]
	v_cndmask_b32_e64 v101, v61, -v61, vcc
	v_cndmask_b32_e64 v100, v59, -v59, vcc
	v_mov_b32_e32 v35, v36
	v_mov_b32_e32 v47, v36
	v_mov_b32_e32 v59, v37
	v_mov_b32_e32 v61, v37
	v_permlane16_swap_b32_e32 v35, v47
	s_nop 0
	v_permlane16_swap_b32_e32 v59, v61
	v_pk_mul_f32 v[106:107], v[102:103], v[106:107] op_sel_hi:[0,1]
	v_pk_mul_f32 v[108:109], v[102:103], v[216:217] op_sel_hi:[0,1]
	v_cndmask_b32_e32 v103, v59, v61, vcc
	v_cndmask_b32_e32 v102, v35, v47, vcc
	v_pk_mul_f32 v[102:103], v[208:209], v[102:103]
	v_mov_b32_e32 v163, v161
	v_pk_fma_f32 v[36:37], v[36:37], v[96:97], v[102:103]
	v_pk_mul_f32 v[96:97], v[80:81], v[108:109]
	v_pk_mul_f32 v[36:37], v[36:37], s[82:83] op_sel_hi:[1,0]
	v_mov_b32_e32 v35, v96
	v_cvt_pk_bf16_f32 v37, v36, v37
	v_mov_b32_e32 v36, v96
	v_mov_b32_e32 v47, v97
	v_mov_b32_e32 v59, v97
	v_permlane16_swap_b32_e32 v35, v36
	s_nop 0
	v_permlane16_swap_b32_e32 v47, v59
	v_cndmask_b32_e32 v103, v47, v59, vcc
	v_cndmask_b32_e32 v102, v35, v36, vcc
	v_pk_mul_f32 v[102:103], v[214:215], v[102:103]
	v_permlane32_swap_b32_e32 v161, v163
	v_pk_fma_f32 v[92:93], v[92:93], v[96:97], v[102:103]
	s_nop 0
	v_pk_mul_f32 v[92:93], v[92:93], s[82:83] op_sel_hi:[1,0]
	s_nop 0
	v_cvt_pk_bf16_f32 v36, v92, v93
	v_pk_mul_f32 v[92:93], v[86:87], v[106:107]
	s_nop 0
	v_mov_b32_e32 v35, v92
	v_mov_b32_e32 v47, v92
	v_mov_b32_e32 v59, v93
	v_mov_b32_e32 v61, v93
	v_permlane16_swap_b32_e32 v35, v47
	s_nop 0
	v_permlane16_swap_b32_e32 v59, v61
	v_cndmask_b32_e32 v97, v59, v61, vcc
	v_cndmask_b32_e32 v96, v35, v47, vcc
	v_pk_mul_f32 v[88:89], v[88:89], v[92:93]
	v_cndmask_b32_e64 v92, v51, -v51, vcc
	v_pk_fma_f32 v[72:73], v[72:73], v[96:97], v[88:89]
	v_cndmask_b32_e64 v93, v53, -v53, vcc
	v_pk_mul_f32 v[72:73], v[72:73], s[82:83] op_sel_hi:[1,0]
	s_nop 0
	v_cvt_pk_bf16_f32 v35, v72, v73
	v_pk_mul_f32 v[72:73], v[84:85], v[104:105]
	s_nop 0
	v_mov_b32_e32 v47, v72
	v_mov_b32_e32 v59, v72
	v_mov_b32_e32 v61, v73
	v_mov_b32_e32 v88, v73
	v_permlane16_swap_b32_e32 v47, v59
	s_nop 0
	v_permlane16_swap_b32_e32 v61, v88
	v_cndmask_b32_e32 v89, v61, v88, vcc
	v_cndmask_b32_e32 v88, v47, v59, vcc
	v_mov_b32_e32 v59, v60
	v_pk_mul_f32 v[58:59], v[58:59], v[72:73]
	s_nop 0
	v_pk_fma_f32 v[58:59], v[100:101], v[88:89], v[58:59]
	v_and_b32_e32 v89, 0xffff0000, v34
	v_lshlrev_b32_e32 v88, 16, v34
	v_mul_f32_e32 v34, v89, v89
	v_pk_fma_f32 v[60:61], v[88:89], v[88:89], v[34:35] op_sel_hi:[1,1,0]
	v_mul_f32_e32 v34, v49, v49
	v_pk_fma_f32 v[60:61], v[48:49], v[48:49], v[60:61]
	v_pk_mul_f32 v[58:59], v[58:59], s[82:83] op_sel_hi:[1,0]
	v_pk_add_f32 v[60:61], v[34:35], v[60:61] op_sel_hi:[0,1]
	v_pk_fma_f32 v[60:61], v[172:173], v[172:173], v[60:61]
	v_mul_f32_e32 v34, v173, v173
	v_pk_add_f32 v[60:61], v[34:35], v[60:61] op_sel_hi:[0,1]
	v_pk_fma_f32 v[60:61], v[164:165], v[164:165], v[60:61]
	v_mul_f32_e32 v34, v165, v165
	v_pk_add_f32 v[60:61], v[34:35], v[60:61] op_sel_hi:[0,1]
	v_mov_b32_e32 v34, v60
	s_nop 1
	v_permlane16_swap_b32_e32 v60, v34
	v_add_f32_e32 v160, v60, v34
	v_mov_b32_e32 v162, v160
	s_nop 1
	v_permlane32_swap_b32_e32 v160, v162
	v_pk_add_f32 v[60:61], v[160:161], v[162:163]
	s_nop 0
	v_pk_fma_f32 v[72:73], v[60:61], s[6:7], v[170:171] op_sel_hi:[1,1,0]
	s_nop 0
	v_mul_f32_e32 v34, 0x4b800000, v73
	v_cmp_gt_f32_e64 s[4:5], s95, v73
	s_nop 1
	v_cndmask_b32_e64 v34, v73, v34, s[4:5]
	v_rsq_f32_e32 v47, v34
	v_cvt_pk_bf16_f32 v34, v58, v59
	v_mul_f32_e32 v51, 0x45800000, v47
	v_cndmask_b32_e64 v96, v47, v51, s[4:5]
	v_pk_mul_f32 v[58:59], v[40:41], v[96:97] op_sel_hi:[1,0]
	v_mul_f32_e32 v47, 0x4b800000, v72
	v_pk_mul_f32 v[58:59], v[58:59], v[74:75]
	v_pk_mul_f32 v[74:75], v[42:43], v[96:97] op_sel_hi:[1,0]
	v_pk_mul_f32 v[58:59], v[58:59], s[82:83] op_sel_hi:[1,0]
	v_pk_mul_f32 v[74:75], v[74:75], v[134:135]
	v_cvt_pk_bf16_f32 v61, v58, v59
	v_pk_mul_f32 v[58:59], v[38:39], v[96:97] op_sel_hi:[1,0]
	v_pk_mul_f32 v[74:75], v[74:75], s[82:83] op_sel_hi:[1,0]
	v_pk_mul_f32 v[58:59], v[58:59], v[130:131]
	v_cmp_gt_f32_e64 s[4:5], s95, v72
	v_pk_mul_f32 v[58:59], v[58:59], s[82:83] op_sel_hi:[1,0]
	v_pk_mul_f32 v[100:101], v[54:55], v[96:97] op_sel_hi:[1,0]
	v_cvt_pk_bf16_f32 v60, v58, v59
	v_pk_mul_f32 v[58:59], v[44:45], v[96:97] op_sel_hi:[1,0]
; template <int DQK, int DV, bool LEAD> ...
;     ...
;           float sn = 0.f;
; #pragma unroll
;           for (int ds = 0; ds < 2; ++ds)
; #pragma unroll
;               for (int j = 0; j < 8; ++j) sn += x[ds][j] * x[ds][j];
;           sn = lanes4_sum(sn);
;           const float rn = rsqrtf(sn * (1.f / 64.f) + EPS);
; #pragma unroll
;           for (int ds = 0; ds < 2; ++ds)
; #pragma unroll
;               for (int j = 0; j < 8; ++j) x[ds][j] *= rn * qgain[32 * ds + 8 * g4 + j];
;           if constexpr (DQK == 64) {
; #pragma unroll
;               for (int ds = 0; ds < 2; ++ds)
; #pragma unroll
;                   for (int j = 0; j < 8; ++j) {
;                       auto rr = __builtin_amdgcn_permlane32_swap(__float_as_uint(x[ds][j]), __float_as_uint(x[ds][j]), false, false);
;                       const float other = hi ? __uint_as_float(rr[0]) : __uint_as_float(rr[1]);
;                       float cc = 1.f, sg = 0.f;
;                       if (lat) { const f32x2 cs = rope[(ds ? pcol : prow) * 16 + 8 * (g4 & 1) + j]; cc = cs.x; sg = hi ? cs.y : -cs.y; }
;                       x[ds][j] = x[ds][j] * cc + other * sg; }
;           } else {
;               float sr = 0.f;
; #pragma unroll
;               for (int j = 0; j < 8; ++j) sr += x[2][j] * x[2][j];
;               sr = lanes4_sum(sr);
;               const float rq = rsqrtf(sr * (1.f / 32.f) + EPS);
; #pragma unroll
;               for (int j = 0; j < 8; ++j) { const float av = x[2][j] * rq * qgain[64 + 8 * g4 + j];
;                   auto rr = __builtin_amdgcn_permlane16_swap(__float_as_uint(av), __float_as_uint(av), false, false);
;                   const float other = (g4 & 1) ? __uint_as_float(rr[0]) : __uint_as_float(rr[1]);
;                   float cc = 1.f, sg = 0.f;
;                   if (lat) { const f32x2 cs = rope[((g4 & 2) ? pcol : prow) * 8 + j]; cc = cs.x; sg = (g4 & 1) ? cs.y : -cs.y; }
;                   x[2][j] = av * cc + other * sg; }
;           }
; #pragma unroll
;           for (int ds = 0; ds < NDS; ++ds) { u32x4 w;
; #pragma unroll
;               for (int i = 0; i < 4; ++i) w[i] = cvtpk(x[ds][2 * i] * c2, x[ds][2 * i + 1] * c2);
;               qf[qb * NDS + ds] = __builtin_bit_cast(bf16x8, w); }
	v_cndmask_b32_e64 v47, v72, v47, s[4:5]
	v_pk_mul_f32 v[58:59], v[58:59], v[132:133]
	v_pk_mul_f32 v[100:101], v[100:101], v[140:141]
	v_pk_mul_f32 v[58:59], v[58:59], s[82:83] op_sel_hi:[1,0]
	v_rsq_f32_e32 v47, v47
	v_cvt_pk_bf16_f32 v59, v58, v59
	v_cvt_pk_bf16_f32 v58, v74, v75
	v_pk_mul_f32 v[74:75], v[56:57], v[96:97] op_sel_hi:[1,0]
	v_pk_mul_f32 v[100:101], v[100:101], s[82:83] op_sel_hi:[1,0]
	v_pk_mul_f32 v[74:75], v[74:75], v[136:137]
	v_mul_f32_e32 v51, 0x45800000, v47
	v_pk_mul_f32 v[74:75], v[74:75], s[82:83] op_sel_hi:[1,0]
	s_nop 0
	v_cvt_pk_bf16_f32 v75, v74, v75
	v_cvt_pk_bf16_f32 v74, v100, v101
	v_pk_mul_f32 v[100:101], v[64:65], v[96:97] op_sel_hi:[1,0]
	v_pk_mul_f32 v[96:97], v[62:63], v[96:97] op_sel_hi:[1,0]
	v_pk_mul_f32 v[100:101], v[100:101], v[142:143]
	v_pk_mul_f32 v[96:97], v[96:97], v[148:149]
	v_pk_mul_f32 v[100:101], v[100:101], s[82:83] op_sel_hi:[1,0]
	v_pk_mul_f32 v[96:97], v[96:97], s[82:83] op_sel_hi:[1,0]
	v_cvt_pk_bf16_f32 v73, v100, v101
	v_cvt_pk_bf16_f32 v72, v96, v97
	v_cndmask_b32_e64 v96, v47, v51, s[4:5]
	v_pk_mul_f32 v[100:101], v[96:97], v[48:49] op_sel_hi:[0,1]
	v_pk_mul_f32 v[48:49], v[96:97], v[164:165] op_sel_hi:[0,1]
	v_pk_mul_f32 v[48:49], v[82:83], v[48:49]
	v_pk_mul_f32 v[88:89], v[96:97], v[88:89] op_sel_hi:[0,1]
	v_pk_mul_f32 v[102:103], v[96:97], v[172:173] op_sel_hi:[0,1]
	v_mov_b32_e32 v47, v48
	v_mov_b32_e32 v51, v48
	v_mov_b32_e32 v53, v49
	v_mov_b32_e32 v96, v49
	v_permlane16_swap_b32_e32 v47, v51
	s_nop 0
	v_permlane16_swap_b32_e32 v53, v96
	v_cndmask_b32_e32 v97, v53, v96, vcc
	v_cndmask_b32_e32 v96, v47, v51, vcc
	v_pk_mul_f32 v[96:97], v[114:115], v[96:97]
	s_nop 0
	v_pk_fma_f32 v[48:49], v[48:49], v[76:77], v[96:97]
	v_pk_mul_f32 v[76:77], v[80:81], v[102:103]
	v_pk_mul_f32 v[48:49], v[48:49], s[82:83] op_sel_hi:[1,0]
	v_mov_b32_e32 v47, v76
	v_cvt_pk_bf16_f32 v49, v48, v49
	v_mov_b32_e32 v48, v76
	v_mov_b32_e32 v51, v77
	v_mov_b32_e32 v53, v77
	v_permlane16_swap_b32_e32 v47, v48
	s_nop 0
	v_permlane16_swap_b32_e32 v51, v53
	v_cndmask_b32_e32 v97, v51, v53, vcc
	v_cndmask_b32_e32 v96, v47, v48, vcc
	v_pk_mul_f32 v[96:97], v[168:169], v[96:97]
	s_nop 0
	v_pk_fma_f32 v[70:71], v[70:71], v[76:77], v[96:97]
	s_nop 0
	v_pk_mul_f32 v[70:71], v[70:71], s[82:83] op_sel_hi:[1,0]
	s_nop 0
	v_cvt_pk_bf16_f32 v48, v70, v71
	v_pk_mul_f32 v[70:71], v[86:87], v[100:101]
	s_nop 0
	v_mov_b32_e32 v47, v70
	v_mov_b32_e32 v51, v70
	v_mov_b32_e32 v53, v71
	v_mov_b32_e32 v76, v71
	v_permlane16_swap_b32_e32 v47, v51
	s_nop 0
	v_permlane16_swap_b32_e32 v53, v76
	v_cndmask_b32_e32 v77, v53, v76, vcc
	v_cndmask_b32_e32 v76, v47, v51, vcc
	v_pk_mul_f32 v[66:67], v[66:67], v[70:71]
	s_nop 0
	v_pk_fma_f32 v[66:67], v[90:91], v[76:77], v[66:67]
	s_nop 0
	v_pk_mul_f32 v[66:67], v[66:67], s[82:83] op_sel_hi:[1,0]
	s_nop 0
	v_cvt_pk_bf16_f32 v47, v66, v67
	v_pk_mul_f32 v[66:67], v[84:85], v[88:89]
	s_nop 0
	v_mov_b32_e32 v51, v66
	v_mov_b32_e32 v53, v66
	v_mov_b32_e32 v70, v67
	v_mov_b32_e32 v71, v67
	v_permlane16_swap_b32_e32 v51, v53
	s_nop 0
	v_permlane16_swap_b32_e32 v70, v71
	v_cndmask_b32_e32 v71, v70, v71, vcc
	v_cndmask_b32_e32 v70, v51, v53, vcc
	v_and_b32_e32 v53, 0xffff0000, v46
	v_mov_b32_e32 v51, v52
	v_lshlrev_b32_e32 v52, 16, v46
	v_mul_f32_e32 v46, v53, v53
	v_pk_mul_f32 v[50:51], v[50:51], v[66:67]
	v_pk_fma_f32 v[66:67], v[52:53], v[52:53], v[46:47] op_sel_hi:[1,1,0]
	v_mul_f32_e32 v46, v69, v69
	v_pk_fma_f32 v[66:67], v[68:69], v[68:69], v[66:67]
	v_pk_fma_f32 v[50:51], v[92:93], v[70:71], v[50:51]
	v_pk_add_f32 v[66:67], v[46:47], v[66:67] op_sel_hi:[0,1]
	v_pk_fma_f32 v[66:67], v[110:111], v[110:111], v[66:67]
	v_mul_f32_e32 v46, v111, v111
	v_pk_add_f32 v[66:67], v[46:47], v[66:67] op_sel_hi:[0,1]
	v_pk_fma_f32 v[66:67], v[98:99], v[98:99], v[66:67]
	v_mul_f32_e32 v46, v99, v99
	v_pk_add_f32 v[66:67], v[46:47], v[66:67] op_sel_hi:[0,1]
	v_mov_b32_e32 v46, v66
	s_nop 1
	v_permlane16_swap_b32_e32 v66, v46
	v_add_f32_e32 v144, v66, v46
	v_mov_b32_e32 v146, v144
	s_nop 1
	v_permlane32_swap_b32_e32 v144, v146
	v_pk_add_f32 v[66:67], v[144:145], v[146:147]
	v_pk_mul_f32 v[50:51], v[50:51], s[82:83] op_sel_hi:[1,0]
	v_pk_fma_f32 v[66:67], v[66:67], s[6:7], v[170:171] op_sel_hi:[1,1,0]
	s_mov_b64 s[6:7], 0x60000
	v_mul_f32_e32 v46, 0x4b800000, v67
	v_cmp_gt_f32_e64 s[4:5], s95, v67
	s_nop 1
	v_cndmask_b32_e64 v46, v67, v46, s[4:5]
	v_rsq_f32_e32 v67, v46
	v_cvt_pk_bf16_f32 v46, v50, v51
	v_cndmask_b32_e64 v50, v31, -v31, vcc
	v_cndmask_b32_e64 v51, v33, -v33, vcc
	v_mul_f32_e32 v31, 0x45800000, v67
	v_cndmask_b32_e64 v70, v67, v31, s[4:5]
	v_mul_f32_e32 v31, 0x4b800000, v66
	v_cmp_gt_f32_e64 s[4:5], s95, v66
	v_pk_mul_f32 v[62:63], v[62:63], v[70:71] op_sel_hi:[1,0]
	v_pk_mul_f32 v[64:65], v[64:65], v[70:71] op_sel_hi:[1,0]
	v_cndmask_b32_e64 v31, v66, v31, s[4:5]
	v_pk_mul_f32 v[38:39], v[38:39], v[70:71] op_sel_hi:[1,0]
	v_rsq_f32_e32 v31, v31
	v_pk_mul_f32 v[62:63], v[62:63], v[138:139]
	v_pk_mul_f32 v[64:65], v[64:65], v[128:129]
	v_pk_mul_f32 v[54:55], v[54:55], v[70:71] op_sel_hi:[1,0]
	v_pk_mul_f32 v[56:57], v[56:57], v[70:71] op_sel_hi:[1,0]
	v_pk_mul_f32 v[42:43], v[42:43], v[70:71] op_sel_hi:[1,0]
	v_pk_mul_f32 v[44:45], v[44:45], v[70:71] op_sel_hi:[1,0]
	v_pk_mul_f32 v[76:77], v[38:39], v[118:119]
	v_pk_mul_f32 v[38:39], v[40:41], v[70:71] op_sel_hi:[1,0]
	v_pk_mul_f32 v[54:55], v[54:55], v[126:127]
	v_pk_mul_f32 v[56:57], v[56:57], v[124:125]
	v_pk_mul_f32 v[42:43], v[42:43], v[122:123]
	v_pk_mul_f32 v[44:45], v[44:45], v[120:121]
	v_pk_mul_f32 v[70:71], v[38:39], v[116:117]
	v_pk_mul_f32 v[38:39], v[62:63], s[82:83] op_sel_hi:[1,0]
	v_pk_mul_f32 v[40:41], v[64:65], s[82:83] op_sel_hi:[1,0]
; __device__ __forceinline__ unsigned cvtpk(float lo, float hi) { f32x2 v = {lo, hi}; bf16x2_t b = __builtin_convertvector(v, bf16x2_t); return __builtin_bit_cast(unsigned, b); }
; #define ATT_KLOAD(sl) do { _Pragma("unroll") for (int kb_ = 0; kb_ < NKW; ++kb_) _Pragma("unroll") for (int ds_ = 0; ds_ < NDS; ++ds_) { \
;         if (ds_ < 2) kf[kb_ * NDS + ds_] = *(const LAS bf16x8*)(kp[ds_ & 1] + (sl) * KSLOT + (kb_ & 1) * 512 + (kb_ >> 1) * 4096); \
;         else kf[kb_ * NDS + ds_] = *(const LAS bf16x8*)(krp + (sl) * KSLOT + (kb_ & 1) * 256 + (kb_ >> 1) * 2048); } } while (0)
; template <int DQK, int DV, bool LEAD> ...
;     ...
;               for (int j = 0; j < 8; ++j) { const float av = x[2][j] * rq * qgain[64 + 8 * g4 + j];
;                   auto rr = __builtin_amdgcn_permlane16_swap(__float_as_uint(av), __float_as_uint(av), false, false);
;                   const float other = (g4 & 1) ? __uint_as_float(rr[0]) : __uint_as_float(rr[1]);
;                   float cc = 1.f, sg = 0.f;
;                   if (lat) { const f32x2 cs = rope[((g4 & 2) ? pcol : prow) * 8 + j]; cc = cs.x; sg = (g4 & 1) ? cs.y : -cs.y; }
;                   x[2][j] = av * cc + other * sg; }
;           }
; #pragma unroll
;           for (int ds = 0; ds < NDS; ++ds) { u32x4 w;
; #pragma unroll
;               for (int i = 0; i < 4; ++i) w[i] = cvtpk(x[ds][2 * i] * c2, x[ds][2 * i + 1] * c2);
;               qf[qb * NDS + ds] = __builtin_bit_cast(bf16x8, w); }
;       }
; #pragma unroll
;       for (int d0 = 0; d0 < NQB * NDS; ++d0) asm volatile("" : "+v"(qf[d0])); }
;     wait_bar<0>();
;     bf16x8 kf[NKW * NDS], vf[NVF];
;     ATT_KLOAD(0);
;     asm volatile("s_waitcnt lgkmcnt(0)\n\ts_barrier" ::: "memory");
	v_cvt_pk_bf16_f32 v38, v38, v39
	v_cvt_pk_bf16_f32 v39, v40, v41
	v_pk_mul_f32 v[40:41], v[54:55], s[82:83] op_sel_hi:[1,0]
	v_pk_mul_f32 v[54:55], v[56:57], s[82:83] op_sel_hi:[1,0]
	v_pk_mul_f32 v[42:43], v[42:43], s[82:83] op_sel_hi:[1,0]
	v_pk_mul_f32 v[44:45], v[44:45], s[82:83] op_sel_hi:[1,0]
	v_cvt_pk_bf16_f32 v40, v40, v41
	v_cvt_pk_bf16_f32 v41, v54, v55
	v_cvt_pk_bf16_f32 v42, v42, v43
	v_cvt_pk_bf16_f32 v43, v44, v45
	v_pk_mul_f32 v[44:45], v[76:77], s[82:83] op_sel_hi:[1,0]
	v_pk_mul_f32 v[54:55], v[70:71], s[82:83] op_sel_hi:[1,0]
	v_mul_f32_e32 v33, 0x45800000, v31
	v_cvt_pk_bf16_f32 v44, v44, v45
	v_cvt_pk_bf16_f32 v45, v54, v55
	v_cndmask_b32_e64 v54, v31, v33, s[4:5]
	v_pk_mul_f32 v[52:53], v[54:55], v[52:53] op_sel_hi:[0,1]
	v_pk_mul_f32 v[52:53], v[84:85], v[52:53]
	s_lshl_b32 s4, s16, 11
	v_mov_b32_e32 v31, v52
	v_mov_b32_e32 v33, v52
	v_mov_b32_e32 v55, v53
	v_mov_b32_e32 v56, v53
	v_permlane16_swap_b32_e32 v31, v33
	s_nop 0
	v_permlane16_swap_b32_e32 v55, v56
	v_cndmask_b32_e32 v57, v55, v56, vcc
	v_cndmask_b32_e32 v56, v31, v33, vcc
	v_mov_b32_e32 v31, v32
	v_pk_mul_f32 v[32:33], v[54:55], v[68:69] op_sel_hi:[0,1]
	v_pk_mul_f32 v[30:31], v[30:31], v[52:53]
	v_pk_mul_f32 v[32:33], v[86:87], v[32:33]
	v_pk_fma_f32 v[30:31], v[50:51], v[56:57], v[30:31]
	v_mov_b32_e32 v50, v32
	v_mov_b32_e32 v52, v32
	v_mov_b32_e32 v51, v33
	v_mov_b32_e32 v53, v33
	v_permlane16_swap_b32_e32 v50, v52
	s_nop 0
	v_permlane16_swap_b32_e32 v51, v53
	v_cndmask_b32_e32 v51, v51, v53, vcc
	v_cndmask_b32_e32 v50, v50, v52, vcc
	v_pk_mul_f32 v[24:25], v[24:25], v[32:33]
	s_cmpk_lt_u32 s38, 0x100
	v_pk_fma_f32 v[22:23], v[22:23], v[50:51], v[24:25]
	v_pk_mul_f32 v[24:25], v[54:55], v[110:111] op_sel_hi:[0,1]
	v_pk_mul_f32 v[24:25], v[80:81], v[24:25]
	v_pk_mul_f32 v[22:23], v[22:23], s[82:83] op_sel_hi:[1,0]
	v_mov_b32_e32 v32, v24
	v_mov_b32_e32 v50, v24
	v_mov_b32_e32 v33, v25
	v_mov_b32_e32 v51, v25
	v_permlane16_swap_b32_e32 v32, v50
	s_nop 0
	v_permlane16_swap_b32_e32 v33, v51
	v_cndmask_b32_e32 v33, v33, v51, vcc
	v_cndmask_b32_e32 v32, v32, v50, vcc
	v_pk_mul_f32 v[32:33], v[94:95], v[32:33]
	s_mov_b32 s16, 1
	v_pk_fma_f32 v[20:21], v[20:21], v[24:25], v[32:33]
	v_pk_mul_f32 v[24:25], v[54:55], v[98:99] op_sel_hi:[0,1]
	v_pk_mul_f32 v[24:25], v[82:83], v[24:25]
	v_pk_mul_f32 v[20:21], v[20:21], s[82:83] op_sel_hi:[1,0]
	v_mov_b32_e32 v32, v24
	v_mov_b32_e32 v50, v24
	v_mov_b32_e32 v33, v25
	v_mov_b32_e32 v51, v25
	v_permlane16_swap_b32_e32 v32, v50
	s_nop 0
	v_permlane16_swap_b32_e32 v33, v51
	v_cndmask_b32_e32 v33, v33, v51, vcc
	v_cndmask_b32_e32 v32, v32, v50, vcc
	v_pk_mul_f32 v[32:33], v[78:79], v[32:33]
	v_cvt_pk_bf16_f32 v55, v22, v23
	v_pk_fma_f32 v[14:15], v[24:25], v[14:15], v[32:33]
	v_pk_mul_f32 v[24:25], v[30:31], s[82:83] op_sel_hi:[1,0]
	v_pk_mul_f32 v[14:15], v[14:15], s[82:83] op_sel_hi:[1,0]
	v_cvt_pk_bf16_f32 v54, v24, v25
	v_cvt_pk_bf16_f32 v56, v20, v21
	v_cvt_pk_bf16_f32 v57, v14, v15
	s_waitcnt vmcnt(0) lgkmcnt(0)
	s_barrier
	ds_read_b128 v[20:23], v203
	ds_read_b128 v[30:33], v203 offset:512
	v_or_b32_e32 v24, 4, v238
	v_bitop3_b32 v14, v243, v24, v242 bitop3:0x36
	v_lshl_add_u32 v211, v14, 4, v244
	s_waitcnt lgkmcnt(1)
	v_mfma_f32_16x16x32_bf16 v[50:53], v[20:23], v[6:9], 0
	ds_read_b128 v[76:79], v211
	ds_read_b128 v[80:83], v211 offset:512
	v_lshlrev_b32_e32 v14, 5, v241
	v_lshlrev_b32_e32 v15, 6, v239
	v_mfma_f32_16x16x32_bf16 v[62:65], v[20:23], v[26:29], 0
	v_bitop3_b32 v14, v14, v236, 48 bitop3:0x78
	v_sub_u32_e32 v15, v240, v15
	v_add3_u32 v212, v15, v14, s4
	v_mfma_f32_16x16x32_bf16 v[66:69], v[20:23], v[72:75], 0
	v_lshl_add_u64 v[14:15], v[192:193], 0, s[6:7]
	s_mov_b64 s[6:7], 0x3000
	s_mov_b32 s4, 0
	v_mfma_f32_16x16x32_bf16 v[20:23], v[20:23], v[38:41], 0
	s_cselect_b64 vcc, -1, 0
	v_lshrrev_b32_e32 v25, 1, v236
	s_waitcnt lgkmcnt(1)
	v_mfma_f32_16x16x32_bf16 v[50:53], v[76:79], v[2:5], v[50:53]
	v_mfma_f32_16x16x32_bf16 v[62:65], v[76:79], v[16:19], v[62:65]
	v_mfma_f32_16x16x32_bf16 v[66:69], v[76:79], v[58:61], v[66:69]
	v_mfma_f32_16x16x32_bf16 v[20:23], v[76:79], v[42:45], v[20:23]
	ds_read_b128 v[76:79], v212 offset:8192
	ds_read_b128 v[84:87], v212 offset:8448
	s_waitcnt lgkmcnt(0)
	s_barrier
; #define ATT_SB() __builtin_amdgcn_sched_barrier(0)
; #define ATT_DMA_K(t, sl) do { glds16(ksrc + (size_t)(t) * 64 * kpitch, (unsigned)__builtin_amdgcn_readfirstlane(kdst + (sl) * KSLOT)); \
;         if constexpr (DQK == 96) glds16(krsrc + (size_t)(t) * 64 * 32, (unsigned)__builtin_amdgcn_readfirstlane(krdst + (sl) * KSLOT)); } while (0)
; #define ATT_DMA_V(t, sl) do { glds16(vsrc + (size_t)(t) * 64, (unsigned)__builtin_amdgcn_readfirstlane(vdst + (sl) * VSLOT)); \
;         if constexpr (DV == 128) glds16(vsrc + (size_t)64 * NR + (size_t)(t) * 64, (unsigned)__builtin_amdgcn_readfirstlane(vdst + (sl) * VSLOT + 8192)); } while (0)
; #define ATT_KLOAD(sl) do { _Pragma("unroll") for (int kb_ = 0; kb_ < NKW; ++kb_) _Pragma("unroll") for (int ds_ = 0; ds_ < NDS; ++ds_) { \
;         if (ds_ < 2) kf[kb_ * NDS + ds_] = *(const LAS bf16x8*)(kp[ds_ & 1] + (sl) * KSLOT + (kb_ & 1) * 512 + (kb_ >> 1) * 4096); \
;         else kf[kb_ * NDS + ds_] = *(const LAS bf16x8*)(krp + (sl) * KSLOT + (kb_ & 1) * 256 + (kb_ >> 1) * 2048); } } while (0)
; #define ATT_QK() do { _Pragma("unroll") for (int kb_ = 0; kb_ < NKW; ++kb_) _Pragma("unroll") for (int ds_ = 0; ds_ < NDS; ++ds_) _Pragma("unroll") for (int qb_ = 0; qb_ < NQB; ++qb_) \
;         c[kb_][qb_] = __builtin_amdgcn_mfma_f32_16x16x32_bf16(kf[kb_ * NDS + ds_], qf[qb_ * NDS + ds_], ds_ == 0 ? zero4 : c[kb_][qb_], 0, 0, 0); } while (0)
; #define ATT_EXP() do { _Pragma("unroll") for (int kb_ = 0; kb_ < NKW; ++kb_) _Pragma("unroll") for (int qb_ = 0; qb_ < NQB; ++qb_) _Pragma("unroll") for (int i_ = 0; i_ < 4; ++i_) \
;         c[kb_][qb_][i_] = __builtin_amdgcn_exp2f(c[kb_][qb_][i_]); } while (0)
; template <int DQK, int DV, bool LEAD> ...
;     ...
;     asm volatile("s_waitcnt lgkmcnt(0)\n\ts_barrier" ::: "memory");
;     float lsum[NQB];
; #pragma unroll
;     for (int qb = 0; qb < NQB; ++qb) lsum[qb] = 0.f;
;     const f32x4 zero4 = {0.f, 0.f, 0.f, 0.f};
;     f32x4 o[NDB][NQB], c[NKW][NQB]; u32x4 pw[4];
; #pragma unroll
;     for (int i = 0; i < NDB; ++i)
; #pragma unroll
;         for (int qb = 0; qb < NQB; ++qb) o[i][qb] = zero4;
;     ATT_DMA_K(3, 0); ATT_DMA_V(1, 1);
;     ATT_QK(); ATT_SB();
;     ATT_KLOAD(1); ATT_SB();
;     if constexpr (LEAD) { ATT_EXP(); ATT_SUMPACK(); }
;     wait_bar<NDMA>();
;     int s_prev = 0, s_cur = 1, s_next = 2;
;     int one_ = 1; asm volatile("" : "+s"(one_));
	s_mov_b32 s5, m0
	s_mov_b32 m0, s42
	s_nop 0
	global_load_lds_dwordx4 v[14:15], off
	s_mov_b32 m0, s5
	s_waitcnt lgkmcnt(1)
	v_mfma_f32_16x16x32_bf16 v[164:167], v[76:79], v[10:13], v[50:53]
	v_lshl_add_u64 v[14:15], v[204:205], 0, s[6:7]
	s_mov_b32 s5, m0
	s_mov_b32 m0, s43
	s_nop 0
	global_load_lds_dwordx4 v[14:15], off
	s_mov_b32 m0, s5
	v_lshl_add_u64 v[14:15], v[206:207], 0, s[66:67]
	v_mfma_f32_16x16x32_bf16 v[152:155], v[76:79], v[34:37], v[62:65]
	s_add_i32 s5, s41, 0x2000
	s_mov_b32 s6, m0
	s_mov_b32 m0, s5
	s_nop 0
	global_load_lds_dwordx4 v[14:15], off
	s_mov_b32 m0, s6
	s_mov_b32 s6, s4
	v_mfma_f32_16x16x32_bf16 v[136:139], v[76:79], v[54:57], v[20:23]
	s_mov_b32 s7, s4
	s_mov_b32 s5, s4
	v_mfma_f32_16x16x32_bf16 v[20:23], v[30:33], v[6:9], 0
	v_mfma_f32_16x16x32_bf16 v[50:53], v[30:33], v[26:29], 0
	v_mfma_f32_16x16x32_bf16 v[62:65], v[30:33], v[72:75], 0
	v_mfma_f32_16x16x32_bf16 v[30:33], v[30:33], v[38:41], 0
	v_mfma_f32_16x16x32_bf16 v[20:23], v[80:83], v[2:5], v[20:23]
	v_mfma_f32_16x16x32_bf16 v[50:53], v[80:83], v[16:19], v[50:53]
	v_mfma_f32_16x16x32_bf16 v[62:65], v[80:83], v[58:61], v[62:65]
	v_mfma_f32_16x16x32_bf16 v[30:33], v[80:83], v[42:45], v[30:33]
	v_mfma_f32_16x16x32_bf16 v[144:147], v[76:79], v[46:49], v[66:69]
	s_waitcnt lgkmcnt(0)
	v_mfma_f32_16x16x32_bf16 v[172:175], v[84:87], v[10:13], v[20:23]
	s_nop 0
	v_lshlrev_b32_e32 v66, 7, v237
	v_mfma_f32_16x16x32_bf16 v[168:171], v[84:87], v[34:37], v[50:53]
	v_mov_b64_e32 v[22:23], s[6:7]
	v_mov_b64_e32 v[20:21], s[4:5]
	v_mfma_f32_16x16x32_bf16 v[160:163], v[84:87], v[46:49], v[62:65]
	v_mfma_f32_16x16x32_bf16 v[156:159], v[84:87], v[54:57], v[30:33]
	ds_read_b128 v[120:123], v203 offset:12288
	ds_read_b128 v[132:135], v203 offset:12800
	ds_read_b128 v[124:127], v211 offset:12288
	ds_read_b128 v[140:143], v211 offset:12800
	ds_read_b128 v[128:131], v212 offset:20480
	ds_read_b128 v[148:151], v212 offset:20736
	v_cndmask_b32_e32 v14, v24, v238, vcc
	v_bitop3_b32 v14, v14, v25, 7 bitop3:0x78
	v_lshlrev_b32_e32 v14, 4, v14
	v_add3_u32 v210, 0, v66, v14
	s_waitcnt vmcnt(3) lgkmcnt(0)
	s_barrier
	s_mov_b32 s5, 1
	v_mov_b32_e32 v14, 0
	s_cmp_lg_u32 s5, 0
	v_mov_b64_e32 v[32:33], v[22:23]
	v_mov_b64_e32 v[52:53], v[22:23]
	v_mov_b64_e32 v[64:65], v[22:23]
	v_mov_b64_e32 v[68:69], v[22:23]
	v_mov_b64_e32 v[78:79], v[22:23]
	v_mov_b64_e32 v[82:83], v[22:23]
	v_mov_b64_e32 v[86:87], v[22:23]
	v_mov_b64_e32 v[90:91], v[22:23]
	v_mov_b64_e32 v[94:95], v[22:23]
	v_mov_b64_e32 v[98:99], v[22:23]
	v_mov_b64_e32 v[102:103], v[22:23]
	v_mov_b64_e32 v[106:107], v[22:23]
	v_mov_b64_e32 v[110:111], v[22:23]
	v_mov_b64_e32 v[114:115], v[22:23]
	v_mov_b64_e32 v[118:119], v[22:23]
	s_cselect_b64 s[6:7], -1, 0
	v_mov_b64_e32 v[30:31], v[20:21]
	v_mov_b64_e32 v[50:51], v[20:21]
	v_mov_b64_e32 v[62:63], v[20:21]
	v_mov_b64_e32 v[66:67], v[20:21]
	v_mov_b64_e32 v[76:77], v[20:21]
	v_mov_b64_e32 v[80:81], v[20:21]
	v_mov_b64_e32 v[84:85], v[20:21]
	v_mov_b64_e32 v[88:89], v[20:21]
	v_mov_b64_e32 v[92:93], v[20:21]
	v_mov_b64_e32 v[96:97], v[20:21]
	v_mov_b64_e32 v[100:101], v[20:21]
	v_mov_b64_e32 v[104:105], v[20:21]
	v_mov_b64_e32 v[108:109], v[20:21]
	v_mov_b64_e32 v[112:113], v[20:21]
	v_mov_b64_e32 v[116:117], v[20:21]
	s_mov_b32 s38, 2
	v_mov_b32_e32 v15, v14
	v_mov_b32_e32 v24, v14
	v_mov_b32_e32 v25, v14
	s_branch .LBB0_643
.Lx_rot0_head:
	s_barrier

; #define ATT_SB() __builtin_amdgcn_sched_barrier(0)
; template <int DQK, int DV, bool LEAD> ...
;     ...
;         ATT_SB();
;         wait_bar<NDMA>();
;         const int tmp = s_prev; s_prev = s_cur; s_cur = s_next; s_next = tmp;
.LBB0_645:
	v_add_f32_e32 v24, v24, v208
	v_add_f32_e32 v25, v25, v209
	v_add_f32_e32 v14, v14, v70
	v_add_f32_e32 v15, v15, v71
	s_setprio 0
	s_waitcnt vmcnt(3) lgkmcnt(0)
	s_add_i32 s48, s48, 1
	s_cmpk_lg_i32 s48, 0x85
	s_cbranch_scc0 .Lx_rot0_exit
	s_mov_b32 s38, s4
	s_mov_b32 s4, s5
	s_branch .Lx_rot0_head
.Lx_rot0_exit:
	s_barrier
	s_branch .LBB0_647

; template <int DQK, int DV, bool LEAD> ...
;     ...
;     const int tid = tid_, lane = tid & 63, q16 = lane & 15, g4 = lane >> 4, hi = lane >> 5; const int wid = __builtin_amdgcn_readfirstlane(tid >> 6);
;     const int kg = KS ? (wid >> 2) : 0, qoff = KS ? (wid & 3) * 64 : wid * 32;
;     const unsigned lds0 = (unsigned)(uintptr_t)shm;
;     const int krow_l = wid * 8 + (lane >> 3);
;     const int kc_l = (lane & 7) ^ (((krow_l >> 1) & 1) | (((krow_l >> 3) & 1) << 1) | (((krow_l >> 4) & 1) << 2));
;     const int vc_l = (lane & 7) ^ ((krow_l >> 1) & 7);
;     const bf16_t* ksrc = K + (size_t)(krow0 + krow_l) * kpitch + kc_l * 8;
;     const int rrow_l = (wid & 3) * 16 + (lane >> 2), rc_l = (lane & 3) ^ (((rrow_l >> 4) & 1) << 1);
;     const bf16_t* krsrc = (DQK == 96) ? KR + (size_t)(krow0 + rrow_l) * 32 + rc_l * 8 : nullptr;
;     const bf16_t* vsrc = Vt + (size_t)krow_l * NR + krow0 + vc_l * 8;
;     const unsigned kdst = lds0 + KOFF + wid * 1024, krdst = lds0 + KOFF + 8192 + (wid & 3) * 1024, vdst = lds0 + VOFF + wid * 1024;
;     ...
;     const int kr0 = 8 * (q16 >> 2) + (q16 & 3);
;     const int fk = ((kr0 >> 1) & 1) | (((kr0 >> 3) & 1) << 1) | (((kr0 >> 4) & 1) << 2);
;     const LAS unsigned char* kp[2]; const LAS unsigned char* vp[2];
; #pragma unroll
;     for (int ds = 0; ds < 2; ++ds) kp[ds] = shm + KOFF + kr0 * 128 + ((((ds << 2) | g4) ^ fk) << 4) + kg * 4096;
;     const LAS unsigned char* krp = shm + KOFF + 8192 + kr0 * 64 + ((g4 ^ (((kr0 >> 4) & 1) << 1)) << 4) + kg * 2048;
; #pragma unroll
;     for (int s_ = 0; s_ < 2; ++s_) vp[s_] = shm + VOFF + q16 * 128 + ((((s_ << 2) | g4) ^ ((q16 >> 1) & 7)) << 4);
;     const LAS unsigned char* vpk = kg ? vp[1] : vp[0];
;     ...
;     ATT_DMA_K(0, 0); ATT_DMA_V(0, 0); ATT_DMA_K(1, 1); ATT_DMA_K(2, 2);
;     bf16x8 qf[NQB * NDS];
;     {
;       const float c2 = (DQK == 64) ? C2_EVEN : C2_ODD; const bool lat = tq0 >= 0;
; #pragma unroll
;       for (int qb = 0; qb < NQB; ++qb) {
;           const bf16_t* qp = Q + (size_t)(qrow0 + qoff + qb * 16 + q16) * qpitch + g4 * 8;
;           bf16x8 raw[NDS];
; #pragma unroll
;           for (int ds = 0; ds < NDS; ++ds) raw[ds] = *(const bf16x8*)(qp + ds * 32);
;           float x[NDS][8];
; #pragma unroll
;           for (int ds = 0; ds < NDS; ++ds)
; #pragma unroll
;               for (int j = 0; j < 8; ++j) x[ds][j] = __uint_as_float(((unsigned)(unsigned short)raw[ds][j]) << 16);
.LBB0_648:
	s_and_b64 vcc, exec, s[4:5]
	s_cbranch_vccz .LBB0_640
	v_mov_b32_e32 v220, v0
	v_mov_b64_e32 v[6:7], s[52:53]
	v_readfirstlane_b32 s38, v220
	s_ashr_i32 s4, s38, 6
	v_bfe_u32 v203, v220, 3, 3
	v_lshl_or_b32 v8, s4, 3, v203
	v_ashrrev_i32_e32 v2, 1, v8
	s_and_b32 s30, s4, 3
	v_and_b32_e32 v3, 1, v2
	s_lshl_b32 s5, s4, 1
	s_lshr_b32 s7, s38, 5
	v_bfe_u32 v4, v220, 2, 4
	v_and_b32_e32 v216, 7, v220
	s_and_b32 s6, s5, 2
	v_and_or_b32 v3, s7, 4, v3
	v_xor_b32_e32 v10, v2, v220
	v_add_u32_e32 v2, s40, v8
	v_lshl_or_b32 v4, s30, 4, v4
	v_bitop3_b32 v9, v3, v216, s6 bitop3:0x36
	v_ashrrev_i32_e32 v3, 31, v2
	v_and_b32_e32 v12, 3, v220
	v_or_b32_e32 v4, s40, v4
	s_lshl_b32 s4, s4, 10
	v_lshlrev_b64 v[2:3], 11, v[2:3]
	v_bitop3_b32 v11, s5, v12, 2 bitop3:0x6c
	v_ashrrev_i32_e32 v5, 31, v4
	s_add_i32 s42, s4, 0
	s_lshl_b32 s6, s30, 10
	v_mad_i64_i32 v[6:7], s[4:5], v8, s91, v[6:7]
	v_lshlrev_b64 v[4:5], 6, v[4:5]
	s_ashr_i32 s41, s40, 31
	v_lshl_add_u64 v[2:3], s[50:51], 0, v[2:3]
	v_lshlrev_b32_e32 v194, 4, v9
	s_add_i32 s5, s6, 0
	v_lshl_add_u64 v[4:5], s[28:29], 0, v[4:5]
	v_lshl_add_u64 v[6:7], s[40:41], 1, v[6:7]
	v_lshl_add_u64 v[186:187], v[2:3], 0, v[194:195]
	v_lshlrev_b32_e32 v194, 4, v11
	v_lshlrev_b32_e32 v2, 4, v10
	s_add_i32 s41, s5, 0x2000
	s_mov_b32 s5, m0
	s_mov_b32 m0, s42
	s_nop 0
	global_load_lds_dwordx4 v[186:187], off
	s_mov_b32 m0, s5
	v_lshl_add_u64 v[188:189], v[4:5], 0, v[194:195]
	v_and_b32_e32 v194, 0x70, v2
	s_mov_b32 s5, m0
	s_mov_b32 m0, s41
	s_nop 0
	global_load_lds_dwordx4 v[188:189], off
	s_mov_b32 m0, s5
	s_add_i32 s40, s42, 0x9000
	v_lshl_add_u64 v[190:191], v[6:7], 0, v[194:195]
	s_mov_b32 s5, m0
	s_mov_b32 m0, s40
	s_nop 0
	global_load_lds_dwordx4 v[190:191], off
	s_mov_b32 m0, s5
	s_mov_b64 s[6:7], 0x20000
	v_lshl_add_u64 v[2:3], v[186:187], 0, s[6:7]
	s_add_i32 s5, s42, 0x3000
	s_mov_b32 s6, m0
	s_mov_b32 m0, s5
	s_nop 0
	global_load_lds_dwordx4 v[2:3], off
	s_mov_b32 m0, s6
	v_lshl_add_u64 v[2:3], v[188:189], 0, s[60:61]
	s_add_i32 s5, s41, 0x3000
	s_mov_b32 s6, m0
	s_mov_b32 m0, s5
	s_nop 0
	global_load_lds_dwordx4 v[2:3], off
	s_mov_b32 m0, s6
	s_mov_b64 s[6:7], 0x40000
	s_lshl_b32 s4, s30, 6
	v_lshl_add_u64 v[2:3], v[186:187], 0, s[6:7]
	s_add_i32 s5, s42, 0x6000
	s_mov_b32 s6, m0
	s_mov_b32 m0, s5
	s_nop 0
	global_load_lds_dwordx4 v[2:3], off
	s_mov_b32 m0, s6
	v_and_b32_e32 v221, 15, v220
	s_mov_b64 s[6:7], 0x2000
	s_or_b32 s25, s4, s25
	v_and_b32_e32 v8, 48, v220
	v_lshl_add_u64 v[2:3], v[188:189], 0, s[6:7]
	v_or_b32_e32 v6, s25, v221
	v_mov_b32_e32 v9, v195
	s_add_i32 s5, s41, 0x6000
	s_mov_b32 s6, m0
	s_mov_b32 m0, s5
	s_nop 0
	global_load_lds_dwordx4 v[2:3], off
	s_mov_b32 m0, s6
	v_lshl_add_u64 v[2:3], s[46:47], 0, v[8:9]
	v_or_b32_e32 v7, 16, v6
	v_mad_i64_i32 v[4:5], s[4:5], v6, s90, v[2:3]
	v_mad_i64_i32 v[10:11], s[4:5], v7, s90, v[2:3]
	v_or_b32_e32 v7, 32, v6
	v_or_b32_e32 v6, 48, v6
	v_mad_i64_i32 v[22:23], s[4:5], v7, s90, v[2:3]
	v_mad_i64_i32 v[34:35], s[4:5], v6, s90, v[2:3]
	global_load_dwordx4 v[66:69], v[4:5], off offset:64
	global_load_dwordx4 v[70:73], v[10:11], off offset:64
	global_load_dwordx4 v[90:93], v[22:23], off offset:64
	global_load_dwordx4 v[116:119], v[34:35], off offset:64
	global_load_dwordx4 v[134:137], v[4:5], off
	global_load_dwordx4 v[140:143], v[10:11], off
	global_load_dwordx4 v[86:89], v[22:23], off
	global_load_dwordx4 v[6:9], v[34:35], off
	s_lshr_b32 s4, s31, 6
	v_and_b32_e32 v218, 63, v220
	v_lshlrev_b32_e32 v217, 1, v220
	s_or_b32 s4, s4, s30
	v_and_or_b32 v236, v217, 24, v12
	v_bfe_u32 v238, v220, 3, 1
	v_mov_b32_e32 v38, s4
	v_cmp_gt_u32_e32 vcc, 32, v218
	v_or_b32_e32 v24, 16, v221
	v_bfe_u32 v194, v220, 4, 2
	s_ashr_i32 s16, s38, 8
	v_bfe_u32 v239, v220, 1, 2
	v_lshlrev_b32_e32 v240, 2, v238
	v_lshl_add_u32 v237, v236, 7, 0
	v_cndmask_b32_e32 v12, v221, v38, vcc
	v_cndmask_b32_e32 v24, v24, v38, vcc
	v_lshl_add_u32 v241, s16, 12, v237
	v_bitop3_b32 v2, v240, v194, v239 bitop3:0x36
	v_lshlrev_b32_e32 v12, 6, v12
	v_lshlrev_b32_e32 v24, 6, v24
	v_lshl_add_u32 v219, v2, 4, v241
	global_load_dwordx4 v[2:5], v[4:5], off offset:128
	s_nop 0
	global_load_dwordx4 v[106:109], v12, s[36:37] offset:48
	global_load_dwordx4 v[102:105], v12, s[36:37] offset:32
	global_load_dwordx4 v[18:21], v12, s[36:37] offset:16
	global_load_dwordx4 v[14:17], v12, s[36:37]
	s_nop 0
	global_load_dwordx4 v[10:13], v[10:11], off offset:128
	s_nop 0
	global_load_dwordx4 v[98:101], v24, s[36:37] offset:48
	global_load_dwordx4 v[94:97], v24, s[36:37] offset:32
	global_load_dwordx4 v[30:33], v24, s[36:37] offset:16
	global_load_dwordx4 v[26:29], v24, s[36:37]
	s_nop 0
	global_load_dwordx4 v[22:25], v[22:23], off offset:128
	v_or_b32_e32 v36, 32, v221
	v_or_b32_e32 v39, 48, v221
	v_cndmask_b32_e32 v36, v36, v38, vcc
	v_cndmask_b32_e32 v38, v39, v38, vcc
	v_lshlrev_b32_e32 v36, 6, v36
	v_lshlrev_b32_e32 v50, 6, v38
	v_lshlrev_b32_e32 v162, 5, v194
	global_load_dwordx4 v[82:85], v36, s[36:37] offset:48
	global_load_dwordx4 v[78:81], v36, s[36:37] offset:32
	global_load_dwordx4 v[74:77], v36, s[36:37] offset:16
	global_load_dwordx4 v[62:65], v36, s[36:37]
	s_nop 0
	global_load_dwordx4 v[34:37], v[34:35], off offset:128
	s_nop 0
	global_load_dwordx4 v[38:41], v50, s[36:37] offset:48
	global_load_dwordx4 v[42:45], v50, s[36:37] offset:32
	global_load_dwordx4 v[46:49], v50, s[36:37] offset:16
	s_nop 0
	global_load_dwordx4 v[50:53], v50, s[36:37]
	s_nop 0
	global_load_dwordx4 v[54:57], v162, s[44:45] offset:144
	global_load_dwordx4 v[58:61], v162, s[44:45] offset:128
	v_and_b32_e32 v160, 16, v220
	v_cmp_eq_u32_e32 vcc, 0, v160
	s_mov_b32 s6, 0x3d000000
	s_brev_b32 s7, 60
	s_mov_b32 s4, 0x358637bd
	s_mov_b32 s7, 0x3c800000
	s_waitcnt vmcnt(26)
; template <int DQK, int DV, bool LEAD> ...
;     ...
;           const bf16_t* qp = Q + (size_t)(qrow0 + qoff + qb * 16 + q16) * qpitch + g4 * 8;
;           bf16x8 raw[NDS];
; #pragma unroll
;           for (int ds = 0; ds < NDS; ++ds) raw[ds] = *(const bf16x8*)(qp + ds * 32);
;           float x[NDS][8];
; #pragma unroll
;           for (int ds = 0; ds < NDS; ++ds)
; #pragma unroll
;               for (int j = 0; j < 8; ++j) x[ds][j] = __uint_as_float(((unsigned)(unsigned short)raw[ds][j]) << 16);
;           const int tq = tq0 + qoff + qb * 16 + q16, prow = (tq >> 6) & 127, pcol = tq & 63;
;           float sn = 0.f;
; #pragma unroll
;           for (int ds = 0; ds < 2; ++ds)
; #pragma unroll
;               for (int j = 0; j < 8; ++j) sn += x[ds][j] * x[ds][j];
;           sn = lanes4_sum(sn);
	v_and_b32_e32 v111, 0xffff0000, v119
	s_waitcnt vmcnt(25)
	v_and_b32_e32 v193, 0xffff0000, v134
	v_lshlrev_b32_e32 v192, 16, v134
	v_lshlrev_b32_e32 v110, 16, v119
	s_waitcnt vmcnt(22)
	v_and_b32_e32 v121, 0xffff0000, v8
	v_lshlrev_b32_e32 v120, 16, v8
	v_mul_f32_e32 v8, v193, v193
	v_and_b32_e32 v113, 0xffff0000, v118
	v_lshlrev_b32_e32 v112, 16, v118
	v_and_b32_e32 v119, 0xffff0000, v9
	v_lshlrev_b32_e32 v118, 16, v9
	v_and_b32_e32 v207, 0xffff0000, v135
	v_lshlrev_b32_e32 v206, 16, v135
	v_pk_fma_f32 v[8:9], v[192:193], v[192:193], v[8:9] op_sel_hi:[1,1,0]
	v_and_b32_e32 v181, 0xffff0000, v137
	v_lshlrev_b32_e32 v180, 16, v137
	v_and_b32_e32 v185, 0xffff0000, v136
	v_lshlrev_b32_e32 v184, 16, v136
	v_and_b32_e32 v137, 0xffff0000, v88
	v_lshlrev_b32_e32 v136, 16, v88
	v_pk_fma_f32 v[8:9], v[206:207], v[206:207], v[8:9]
	v_mul_f32_e32 v88, v207, v207
	v_pk_add_f32 v[8:9], v[88:89], v[8:9] op_sel_hi:[0,1]
	v_pk_fma_f32 v[8:9], v[184:185], v[184:185], v[8:9]
	v_mul_f32_e32 v88, v185, v185
	v_pk_add_f32 v[8:9], v[88:89], v[8:9] op_sel_hi:[0,1]
	v_pk_fma_f32 v[8:9], v[180:181], v[180:181], v[8:9]
	v_mul_f32_e32 v88, v181, v181
	v_and_b32_e32 v179, 0xffff0000, v66
	v_lshlrev_b32_e32 v178, 16, v66
	v_pk_add_f32 v[8:9], v[88:89], v[8:9] op_sel_hi:[0,1]
	v_pk_fma_f32 v[8:9], v[178:179], v[178:179], v[8:9]
	v_mul_f32_e32 v88, v179, v179
	v_and_b32_e32 v177, 0xffff0000, v67
	v_lshlrev_b32_e32 v176, 16, v67
	v_pk_add_f32 v[8:9], v[88:89], v[8:9] op_sel_hi:[0,1]
	v_pk_fma_f32 v[8:9], v[176:177], v[176:177], v[8:9]
	v_mul_f32_e32 v88, v177, v177
	v_and_b32_e32 v171, 0xffff0000, v68
	v_lshlrev_b32_e32 v170, 16, v68
	v_pk_add_f32 v[8:9], v[88:89], v[8:9] op_sel_hi:[0,1]
	v_pk_fma_f32 v[8:9], v[170:171], v[170:171], v[8:9]
	v_mul_f32_e32 v88, v171, v171
	v_and_b32_e32 v169, 0xffff0000, v69
	v_lshlrev_b32_e32 v168, 16, v69
	v_pk_add_f32 v[8:9], v[88:89], v[8:9] op_sel_hi:[0,1]
	v_pk_fma_f32 v[8:9], v[168:169], v[168:169], v[8:9]
	v_mul_f32_e32 v88, v169, v169
	v_pk_add_f32 v[8:9], v[88:89], v[8:9] op_sel_hi:[0,1]
	v_and_b32_e32 v123, 0xffff0000, v7
	v_lshlrev_b32_e32 v122, 16, v7
	v_mov_b32_e32 v7, v8
	s_nop 1
	v_permlane16_swap_b32_e32 v8, v7
	v_add_f32_e32 v7, v8, v7
	v_mov_b32_e32 v9, v7
	v_and_b32_e32 v167, 0xffff0000, v140
	s_nop 0
	v_permlane32_swap_b32_e32 v7, v9
	v_lshlrev_b32_e32 v166, 16, v140
	v_mul_f32_e32 v8, v167, v167
	v_and_b32_e32 v133, 0xffff0000, v89
	v_lshlrev_b32_e32 v132, 16, v89
	v_and_b32_e32 v159, 0xffff0000, v141
	v_lshlrev_b32_e32 v158, 16, v141
	v_pk_fma_f32 v[88:89], v[166:167], v[166:167], v[8:9] op_sel_hi:[1,1,0]
	v_mul_f32_e32 v8, v159, v159
	v_pk_fma_f32 v[88:89], v[158:159], v[158:159], v[88:89]
	v_and_b32_e32 v157, 0xffff0000, v142
	v_lshlrev_b32_e32 v156, 16, v142
	v_pk_add_f32 v[88:89], v[8:9], v[88:89] op_sel_hi:[0,1]
	v_pk_fma_f32 v[88:89], v[156:157], v[156:157], v[88:89]
	v_mul_f32_e32 v8, v157, v157
	v_and_b32_e32 v155, 0xffff0000, v143
	v_lshlrev_b32_e32 v154, 16, v143
	v_pk_add_f32 v[88:89], v[8:9], v[88:89] op_sel_hi:[0,1]
	v_pk_fma_f32 v[88:89], v[154:155], v[154:155], v[88:89]
	v_mul_f32_e32 v8, v155, v155
	v_and_b32_e32 v153, 0xffff0000, v70
	v_lshlrev_b32_e32 v152, 16, v70
	v_pk_add_f32 v[88:89], v[8:9], v[88:89] op_sel_hi:[0,1]
	v_pk_fma_f32 v[88:89], v[152:153], v[152:153], v[88:89]
	v_mul_f32_e32 v8, v153, v153
	v_and_b32_e32 v151, 0xffff0000, v71
	v_lshlrev_b32_e32 v150, 16, v71
	v_pk_add_f32 v[88:89], v[8:9], v[88:89] op_sel_hi:[0,1]
	v_pk_fma_f32 v[88:89], v[150:151], v[150:151], v[88:89]
	v_mul_f32_e32 v8, v151, v151
	v_and_b32_e32 v149, 0xffff0000, v72
	v_lshlrev_b32_e32 v148, 16, v72
	v_pk_add_f32 v[88:89], v[8:9], v[88:89] op_sel_hi:[0,1]
	v_pk_fma_f32 v[88:89], v[148:149], v[148:149], v[88:89]
	v_mul_f32_e32 v8, v149, v149
	v_and_b32_e32 v147, 0xffff0000, v73
	v_lshlrev_b32_e32 v146, 16, v73
	v_pk_add_f32 v[88:89], v[8:9], v[88:89] op_sel_hi:[0,1]
	v_pk_fma_f32 v[88:89], v[146:147], v[146:147], v[88:89]
	v_mul_f32_e32 v8, v147, v147
	v_pk_add_f32 v[88:89], v[8:9], v[88:89] op_sel_hi:[0,1]
	v_mov_b32_e32 v8, v88
	s_nop 1
	v_permlane16_swap_b32_e32 v88, v8
	v_and_b32_e32 v145, 0xffff0000, v86
	v_add_f32_e32 v173, v88, v8
	v_lshlrev_b32_e32 v144, 16, v86
	v_mul_f32_e32 v8, v145, v145
	v_and_b32_e32 v139, 0xffff0000, v87
	v_lshlrev_b32_e32 v138, 16, v87
	v_pk_fma_f32 v[86:87], v[144:145], v[144:145], v[8:9] op_sel_hi:[1,1,0]
	v_mul_f32_e32 v8, v139, v139
	v_pk_fma_f32 v[86:87], v[138:139], v[138:139], v[86:87]
	v_and_b32_e32 v131, 0xffff0000, v90
	v_pk_add_f32 v[86:87], v[8:9], v[86:87] op_sel_hi:[0,1]
	v_pk_fma_f32 v[86:87], v[136:137], v[136:137], v[86:87]
	v_mul_f32_e32 v8, v137, v137
	v_pk_add_f32 v[86:87], v[8:9], v[86:87] op_sel_hi:[0,1]
	v_pk_fma_f32 v[86:87], v[132:133], v[132:133], v[86:87]
	v_mul_f32_e32 v8, v133, v133
	v_lshlrev_b32_e32 v130, 16, v90
	v_pk_add_f32 v[86:87], v[8:9], v[86:87] op_sel_hi:[0,1]
	v_pk_fma_f32 v[86:87], v[130:131], v[130:131], v[86:87]
	v_mul_f32_e32 v8, v131, v131
	v_and_b32_e32 v129, 0xffff0000, v91
	v_lshlrev_b32_e32 v128, 16, v91
	v_pk_add_f32 v[86:87], v[8:9], v[86:87] op_sel_hi:[0,1]
	v_pk_fma_f32 v[86:87], v[128:129], v[128:129], v[86:87]
	v_mul_f32_e32 v8, v129, v129
	v_and_b32_e32 v127, 0xffff0000, v92
	v_lshlrev_b32_e32 v126, 16, v92
	v_pk_add_f32 v[86:87], v[8:9], v[86:87] op_sel_hi:[0,1]
	v_pk_fma_f32 v[86:87], v[126:127], v[126:127], v[86:87]
	v_mul_f32_e32 v8, v127, v127
	v_and_b32_e32 v125, 0xffff0000, v93
	v_lshlrev_b32_e32 v124, 16, v93
	v_pk_add_f32 v[86:87], v[8:9], v[86:87] op_sel_hi:[0,1]
	v_pk_fma_f32 v[86:87], v[124:125], v[124:125], v[86:87]
	v_mul_f32_e32 v8, v125, v125
	v_pk_add_f32 v[86:87], v[8:9], v[86:87] op_sel_hi:[0,1]
; template <int DQK, int DV, bool LEAD> ...
;     ...
;               for (int j = 0; j < 8; ++j) x[ds][j] = __uint_as_float(((unsigned)(unsigned short)raw[ds][j]) << 16);
;           const int tq = tq0 + qoff + qb * 16 + q16, prow = (tq >> 6) & 127, pcol = tq & 63;
;           float sn = 0.f;
; #pragma unroll
;           for (int ds = 0; ds < 2; ++ds)
; #pragma unroll
;               for (int j = 0; j < 8; ++j) sn += x[ds][j] * x[ds][j];
;           sn = lanes4_sum(sn);
;           const float rn = rsqrtf(sn * (1.f / 64.f) + EPS);
; #pragma unroll
;           for (int ds = 0; ds < 2; ++ds)
; #pragma unroll
;               for (int j = 0; j < 8; ++j) x[ds][j] *= rn * qgain[32 * ds + 8 * g4 + j];
;           if constexpr (DQK == 64) {
; #pragma unroll
;               for (int ds = 0; ds < 2; ++ds)
; #pragma unroll
;                   for (int j = 0; j < 8; ++j) {
;                       auto rr = __builtin_amdgcn_permlane32_swap(__float_as_uint(x[ds][j]), __float_as_uint(x[ds][j]), false, false);
;                       const float other = hi ? __uint_as_float(rr[0]) : __uint_as_float(rr[1]);
;                       float cc = 1.f, sg = 0.f;
;                       if (lat) { const f32x2 cs = rope[(ds ? pcol : prow) * 16 + 8 * (g4 & 1) + j]; cc = cs.x; sg = hi ? cs.y : -cs.y; }
;                       x[ds][j] = x[ds][j] * cc + other * sg; }
;           } else {
;               float sr = 0.f;
; #pragma unroll
;               for (int j = 0; j < 8; ++j) sr += x[2][j] * x[2][j];
;               sr = lanes4_sum(sr);
;               const float rq = rsqrtf(sr * (1.f / 32.f) + EPS);
; #pragma unroll
;               for (int j = 0; j < 8; ++j) { const float av = x[2][j] * rq * qgain[64 + 8 * g4 + j];
;                   auto rr = __builtin_amdgcn_permlane16_swap(__float_as_uint(av), __float_as_uint(av), false, false);
;                   const float other = (g4 & 1) ? __uint_as_float(rr[0]) : __uint_as_float(rr[1]);
;                   float cc = 1.f, sg = 0.f;
;                   if (lat) { const f32x2 cs = rope[((g4 & 2) ? pcol : prow) * 8 + j]; cc = cs.x; sg = (g4 & 1) ? cs.y : -cs.y; }
;                   x[2][j] = av * cc + other * sg; }
	v_mov_b32_e32 v8, v86
	v_and_b32_e32 v135, 0xffff0000, v6
	s_nop 0
	v_permlane16_swap_b32_e32 v86, v8
	v_lshlrev_b32_e32 v134, 16, v6
	v_mul_f32_e32 v6, v135, v135
	v_add_f32_e32 v161, v86, v8
	v_pk_fma_f32 v[86:87], v[134:135], v[134:135], v[6:7] op_sel_hi:[1,1,0]
	v_mul_f32_e32 v6, v123, v123
	v_pk_fma_f32 v[86:87], v[122:123], v[122:123], v[86:87]
	v_and_b32_e32 v115, 0xffff0000, v117
	v_pk_add_f32 v[86:87], v[6:7], v[86:87] op_sel_hi:[0,1]
	v_pk_fma_f32 v[86:87], v[120:121], v[120:121], v[86:87]
	v_mul_f32_e32 v6, v121, v121
	v_pk_add_f32 v[86:87], v[6:7], v[86:87] op_sel_hi:[0,1]
	v_pk_fma_f32 v[86:87], v[118:119], v[118:119], v[86:87]
	v_mul_f32_e32 v6, v119, v119
	v_lshlrev_b32_e32 v114, 16, v117
	v_and_b32_e32 v117, 0xffff0000, v116
	v_lshlrev_b32_e32 v116, 16, v116
	v_pk_add_f32 v[86:87], v[6:7], v[86:87] op_sel_hi:[0,1]
	v_pk_fma_f32 v[86:87], v[116:117], v[116:117], v[86:87]
	v_mul_f32_e32 v6, v117, v117
	global_load_dwordx4 v[66:69], v162, s[44:45] offset:16
	global_load_dwordx4 v[70:73], v162, s[44:45]
	v_pk_add_f32 v[86:87], v[6:7], v[86:87] op_sel_hi:[0,1]
	v_pk_fma_f32 v[86:87], v[114:115], v[114:115], v[86:87]
	v_mul_f32_e32 v6, v115, v115
	v_pk_add_f32 v[86:87], v[6:7], v[86:87] op_sel_hi:[0,1]
	v_pk_fma_f32 v[86:87], v[112:113], v[112:113], v[86:87]
	v_mul_f32_e32 v6, v113, v113
	v_pk_add_f32 v[86:87], v[6:7], v[86:87] op_sel_hi:[0,1]
	v_pk_fma_f32 v[86:87], v[110:111], v[110:111], v[86:87]
	v_mul_f32_e32 v6, v111, v111
	v_pk_add_f32 v[86:87], v[6:7], v[86:87] op_sel_hi:[0,1]
	v_mov_b32_e32 v6, v86
	s_nop 1
	v_permlane16_swap_b32_e32 v86, v6
	v_add_f32_e32 v141, v86, v6
	global_load_dwordx4 v[86:89], v162, s[44:45] offset:272
	global_load_dwordx4 v[90:93], v162, s[44:45] offset:256
	s_waitcnt vmcnt(15)
	v_and_b32_e32 v165, 0xffff0000, v25
	v_lshlrev_b32_e32 v164, 16, v25
	v_and_b32_e32 v25, 0xffff0000, v2
	v_cndmask_b32_e64 v201, v105, -v105, vcc
	v_cndmask_b32_e64 v200, v103, -v103, vcc
	v_mov_b32_e32 v103, v104
	v_and_b32_e32 v105, 0xffff0000, v24
	v_lshlrev_b32_e32 v104, 16, v24
	v_lshlrev_b32_e32 v24, 16, v2
	v_mul_f32_e32 v2, v25, v25
	v_and_b32_e32 v205, 0xffff0000, v13
	v_lshlrev_b32_e32 v204, 16, v13
	v_and_b32_e32 v211, 0xffff0000, v12
	v_lshlrev_b32_e32 v210, 16, v12
	v_and_b32_e32 v13, 0xffff0000, v3
	v_lshlrev_b32_e32 v12, 16, v3
	v_pk_fma_f32 v[2:3], v[24:25], v[24:25], v[2:3] op_sel_hi:[1,1,0]
	v_and_b32_e32 v199, 0xffff0000, v4
	v_lshlrev_b32_e32 v198, 16, v4
	v_pk_fma_f32 v[2:3], v[12:13], v[12:13], v[2:3]
	v_mul_f32_e32 v4, v13, v13
	v_pk_add_f32 v[2:3], v[4:5], v[2:3] op_sel_hi:[0,1]
	v_pk_fma_f32 v[2:3], v[198:199], v[198:199], v[2:3]
	v_mul_f32_e32 v4, v199, v199
	v_and_b32_e32 v215, 0xffff0000, v5
	v_lshlrev_b32_e32 v214, 16, v5
	v_pk_add_f32 v[2:3], v[4:5], v[2:3] op_sel_hi:[0,1]
	v_pk_fma_f32 v[2:3], v[214:215], v[214:215], v[2:3]
	v_mul_f32_e32 v4, v215, v215
	v_pk_add_f32 v[2:3], v[4:5], v[2:3] op_sel_hi:[0,1]
	v_mov_b32_e32 v3, v2
	s_nop 1
	v_permlane16_swap_b32_e32 v2, v3
	v_add_f32_e32 v6, v2, v3
	v_mov_b32_e32 v8, v6
	s_nop 1
	v_permlane32_swap_b32_e32 v6, v8
	v_cndmask_b32_e64 v213, v109, -v109, vcc
	v_cndmask_b32_e64 v212, v107, -v107, vcc
	v_mov_b32_e32 v107, v108
	s_waitcnt vmcnt(14)
	v_cndmask_b32_e64 v109, v85, -v85, vcc
	v_cndmask_b32_e64 v108, v83, -v83, vcc
	v_mov_b32_e32 v83, v84
	s_waitcnt vmcnt(9)
	v_cndmask_b32_e64 v85, v41, -v41, vcc
	v_cndmask_b32_e64 v84, v39, -v39, vcc
	v_mov_b32_e32 v39, v40
	s_waitcnt vmcnt(8)
	v_cndmask_b32_e64 v41, v45, -v45, vcc
	v_cndmask_b32_e64 v40, v43, -v43, vcc
	v_mov_b32_e32 v43, v44
	v_pk_add_f32 v[2:3], v[6:7], v[8:9]
	v_mov_b64_e32 v[44:45], s[4:5]
	v_pk_fma_f32 v[6:7], v[2:3], s[6:7], v[44:45] op_sel_hi:[1,1,0]
	v_cndmask_b32_e64 v222, v19, -v19, vcc
	v_mul_f32_e32 v2, 0x4b800000, v7
	v_cmp_gt_f32_e64 s[4:5], s95, v7
	v_mov_b32_e32 v19, v20
	v_and_b32_e32 v229, 0xffff0000, v11
	v_cndmask_b32_e64 v2, v7, v2, s[4:5]
	v_rsq_f32_e32 v2, v2
	v_lshlrev_b32_e32 v228, 16, v11
	v_mul_f32_e32 v11, 0x4b800000, v6
	v_cndmask_b32_e64 v223, v21, -v21, vcc
	v_mul_f32_e32 v3, 0x45800000, v2
	v_cndmask_b32_e64 v20, v2, v3, s[4:5]
	s_waitcnt vmcnt(5)
	v_pk_mul_f32 v[2:3], v[20:21], v[56:57] op_sel_hi:[0,1]
	v_pk_mul_f32 v[2:3], v[2:3], v[168:169]
	v_pk_mul_f32 v[4:5], v[20:21], v[54:55] op_sel_hi:[0,1]
	v_pk_mul_f32 v[2:3], v[2:3], s[82:83] op_sel_hi:[1,0]
	v_pk_mul_f32 v[8:9], v[4:5], v[170:171]
	v_cvt_pk_bf16_f32 v5, v2, v3
	v_pk_mul_f32 v[2:3], v[8:9], s[82:83] op_sel_hi:[1,0]
	s_waitcnt vmcnt(4)
	v_pk_mul_f32 v[8:9], v[58:59], v[20:21] op_sel_hi:[1,0]
	v_cvt_pk_bf16_f32 v4, v2, v3
	v_pk_mul_f32 v[2:3], v[20:21], v[60:61] op_sel_hi:[0,1]
	v_pk_mul_f32 v[2:3], v[2:3], v[176:177]
	v_pk_mul_f32 v[8:9], v[8:9], v[178:179]
	v_pk_mul_f32 v[2:3], v[2:3], s[82:83] op_sel_hi:[1,0]
	v_pk_mul_f32 v[8:9], v[8:9], s[82:83] op_sel_hi:[1,0]
	v_cvt_pk_bf16_f32 v3, v2, v3
	v_cndmask_b32_e64 v177, v33, -v33, vcc
	v_cndmask_b32_e64 v176, v31, -v31, vcc
	v_mov_b32_e32 v31, v32
	v_cvt_pk_bf16_f32 v2, v8, v9
	s_waitcnt vmcnt(3)
	v_pk_mul_f32 v[8:9], v[68:69], v[20:21] op_sel_hi:[1,0]
	v_pk_mul_f32 v[32:33], v[66:67], v[20:21] op_sel_hi:[1,0]
	v_cmp_gt_f32_e64 s[4:5], s95, v6
	v_pk_mul_f32 v[8:9], v[8:9], v[180:181]
	v_pk_mul_f32 v[32:33], v[32:33], v[184:185]
	v_cndmask_b32_e64 v6, v6, v11, s[4:5]
	v_pk_mul_f32 v[8:9], v[8:9], s[82:83] op_sel_hi:[1,0]
	v_pk_mul_f32 v[32:33], v[32:33], s[82:83] op_sel_hi:[1,0]
	v_rsq_f32_e32 v11, v6
	v_cvt_pk_bf16_f32 v9, v8, v9
	v_cvt_pk_bf16_f32 v8, v32, v33
	s_waitcnt vmcnt(2)
; __device__ __forceinline__ unsigned cvtpk(float lo, float hi) { f32x2 v = {lo, hi}; bf16x2_t b = __builtin_convertvector(v, bf16x2_t); return __builtin_bit_cast(unsigned, b); }
; template <int DQK, int DV, bool LEAD> ...
;     ...
;               float sr = 0.f;
; #pragma unroll
;               for (int j = 0; j < 8; ++j) sr += x[2][j] * x[2][j];
;               sr = lanes4_sum(sr);
;               const float rq = rsqrtf(sr * (1.f / 32.f) + EPS);
; #pragma unroll
;               for (int j = 0; j < 8; ++j) { const float av = x[2][j] * rq * qgain[64 + 8 * g4 + j];
;                   auto rr = __builtin_amdgcn_permlane16_swap(__float_as_uint(av), __float_as_uint(av), false, false);
;                   const float other = (g4 & 1) ? __uint_as_float(rr[0]) : __uint_as_float(rr[1]);
;                   float cc = 1.f, sg = 0.f;
;                   if (lat) { const f32x2 cs = rope[((g4 & 2) ? pcol : prow) * 8 + j]; cc = cs.x; sg = (g4 & 1) ? cs.y : -cs.y; }
;                   x[2][j] = av * cc + other * sg; }
;           }
; #pragma unroll
;           for (int ds = 0; ds < NDS; ++ds) { u32x4 w;
; #pragma unroll
;               for (int i = 0; i < 4; ++i) w[i] = cvtpk(x[ds][2 * i] * c2, x[ds][2 * i + 1] * c2);
;               qf[qb * NDS + ds] = __builtin_bit_cast(bf16x8, w); }
	v_pk_mul_f32 v[32:33], v[72:73], v[20:21] op_sel_hi:[1,0]
	v_pk_mul_f32 v[20:21], v[70:71], v[20:21] op_sel_hi:[1,0]
	v_pk_mul_f32 v[32:33], v[32:33], v[206:207]
	v_pk_mul_f32 v[20:21], v[20:21], v[192:193]
	v_pk_mul_f32 v[32:33], v[32:33], s[82:83] op_sel_hi:[1,0]
	v_pk_mul_f32 v[20:21], v[20:21], s[82:83] op_sel_hi:[1,0]
	v_cvt_pk_bf16_f32 v7, v32, v33
	v_cvt_pk_bf16_f32 v6, v20, v21
	v_mul_f32_e32 v20, 0x45800000, v11
	v_cndmask_b32_e64 v20, v11, v20, s[4:5]
	v_pk_mul_f32 v[32:33], v[20:21], v[12:13] op_sel_hi:[0,1]
	v_pk_mul_f32 v[12:13], v[20:21], v[214:215] op_sel_hi:[0,1]
	s_waitcnt vmcnt(1)
	v_pk_mul_f32 v[12:13], v[12:13], v[88:89]
	v_cndmask_b32_e64 v183, v101, -v101, vcc
	v_cndmask_b32_e64 v182, v99, -v99, vcc
	v_mov_b32_e32 v99, v100
	v_and_b32_e32 v101, 0xffff0000, v37
	v_lshlrev_b32_e32 v100, 16, v37
	v_cndmask_b32_e64 v209, v97, -v97, vcc
	v_cndmask_b32_e64 v208, v95, -v95, vcc
	v_mov_b32_e32 v95, v96
	v_cndmask_b32_e64 v97, v81, -v81, vcc
	v_cndmask_b32_e64 v96, v79, -v79, vcc
	v_mov_b32_e32 v79, v80
	v_and_b32_e32 v81, 0xffff0000, v36
	v_lshlrev_b32_e32 v80, 16, v36
	v_and_b32_e32 v37, 0xffff0000, v23
	v_lshlrev_b32_e32 v36, 16, v23
	v_pk_mul_f32 v[24:25], v[20:21], v[24:25] op_sel_hi:[0,1]
	v_pk_mul_f32 v[178:179], v[20:21], v[198:199] op_sel_hi:[0,1]
	v_mov_b32_e32 v11, v12
	v_mov_b32_e32 v20, v12
	v_mov_b32_e32 v21, v13
	v_mov_b32_e32 v23, v13
	v_permlane16_swap_b32_e32 v11, v20
	s_nop 0
	v_permlane16_swap_b32_e32 v21, v23
	v_cndmask_b32_e32 v21, v21, v23, vcc
	v_cndmask_b32_e32 v20, v11, v20, vcc
	v_pk_mul_f32 v[20:21], v[212:213], v[20:21]
	v_cndmask_b32_e64 v169, v49, -v49, vcc
	v_pk_fma_f32 v[12:13], v[12:13], v[106:107], v[20:21]
	v_pk_mul_f32 v[20:21], v[178:179], v[86:87]
	v_pk_mul_f32 v[12:13], v[12:13], s[82:83] op_sel_hi:[1,0]
	v_cndmask_b32_e64 v168, v47, -v47, vcc
	v_mov_b32_e32 v47, v48
	v_cndmask_b32_e64 v49, v17, -v17, vcc
	v_cndmask_b32_e64 v48, v15, -v15, vcc
	v_cvt_pk_bf16_f32 v13, v12, v13
	v_mov_b32_e32 v11, v20
	v_mov_b32_e32 v12, v20
	v_mov_b32_e32 v15, v21
	v_mov_b32_e32 v17, v21
	v_permlane16_swap_b32_e32 v11, v12
	s_nop 0
	v_permlane16_swap_b32_e32 v15, v17
	v_cndmask_b32_e32 v107, v15, v17, vcc
	v_cndmask_b32_e32 v106, v11, v12, vcc
	v_pk_mul_f32 v[106:107], v[200:201], v[106:107]
	v_mov_b32_e32 v175, v173
	v_pk_fma_f32 v[20:21], v[20:21], v[102:103], v[106:107]
	s_nop 0
	v_permlane32_swap_b32_e32 v173, v175
	v_pk_mul_f32 v[20:21], v[20:21], s[82:83] op_sel_hi:[1,0]
	v_cndmask_b32_e64 v171, v77, -v77, vcc
	v_cvt_pk_bf16_f32 v12, v20, v21
	s_waitcnt vmcnt(0)
	v_pk_mul_f32 v[20:21], v[92:93], v[32:33]
	v_cndmask_b32_e64 v170, v75, -v75, vcc
	v_mov_b32_e32 v11, v20
	v_mov_b32_e32 v15, v20
	v_mov_b32_e32 v17, v21
	v_mov_b32_e32 v23, v21
	v_permlane16_swap_b32_e32 v11, v15
	s_nop 0
	v_permlane16_swap_b32_e32 v17, v23
	v_cndmask_b32_e32 v33, v17, v23, vcc
	v_cndmask_b32_e32 v32, v11, v15, vcc
	v_pk_mul_f32 v[32:33], v[222:223], v[32:33]
	v_mov_b32_e32 v75, v76
	v_pk_fma_f32 v[18:19], v[18:19], v[20:21], v[32:33]
	v_cndmask_b32_e64 v32, v27, -v27, vcc
	v_pk_mul_f32 v[18:19], v[18:19], s[82:83] op_sel_hi:[1,0]
	v_and_b32_e32 v77, 0xffff0000, v35
	v_cvt_pk_bf16_f32 v11, v18, v19
	v_pk_mul_f32 v[18:19], v[90:91], v[24:25]
	v_and_b32_e32 v25, 0xffff0000, v10
	v_mov_b32_e32 v15, v18
	v_mov_b32_e32 v17, v18
	v_mov_b32_e32 v20, v19
	v_mov_b32_e32 v21, v19
	v_permlane16_swap_b32_e32 v15, v17
	s_nop 0
	v_permlane16_swap_b32_e32 v20, v21
	v_lshlrev_b32_e32 v24, 16, v10
	v_mul_f32_e32 v10, v25, v25
	v_cndmask_b32_e32 v21, v20, v21, vcc
	v_cndmask_b32_e32 v20, v15, v17, vcc
	v_mov_b32_e32 v15, v16
	v_pk_fma_f32 v[16:17], v[24:25], v[24:25], v[10:11] op_sel_hi:[1,1,0]
	v_mul_f32_e32 v10, v229, v229
	v_pk_fma_f32 v[16:17], v[228:229], v[228:229], v[16:17]
	v_pk_mul_f32 v[14:15], v[14:15], v[18:19]
	v_pk_add_f32 v[16:17], v[10:11], v[16:17] op_sel_hi:[0,1]
	v_pk_fma_f32 v[16:17], v[210:211], v[210:211], v[16:17]
	v_mul_f32_e32 v10, v211, v211
	v_pk_add_f32 v[16:17], v[10:11], v[16:17] op_sel_hi:[0,1]
	v_pk_fma_f32 v[16:17], v[204:205], v[204:205], v[16:17]
	v_mul_f32_e32 v10, v205, v205
	v_pk_add_f32 v[16:17], v[10:11], v[16:17] op_sel_hi:[0,1]
	v_mov_b32_e32 v10, v16
	s_nop 1
	v_permlane16_swap_b32_e32 v16, v10
	v_add_f32_e32 v172, v16, v10
	v_mov_b32_e32 v174, v172
	s_nop 1
	v_permlane32_swap_b32_e32 v172, v174
	v_pk_add_f32 v[16:17], v[172:173], v[174:175]
	v_pk_fma_f32 v[14:15], v[48:49], v[20:21], v[14:15]
	v_pk_fma_f32 v[18:19], v[16:17], s[6:7], v[44:45] op_sel_hi:[1,1,0]
	v_pk_mul_f32 v[14:15], v[14:15], s[82:83] op_sel_hi:[1,0]
	v_mul_f32_e32 v10, 0x4b800000, v19
	v_cmp_gt_f32_e64 s[4:5], s95, v19
	v_mul_f32_e32 v23, 0x4b800000, v18
	v_lshlrev_b32_e32 v76, 16, v35
	v_cndmask_b32_e64 v10, v19, v10, s[4:5]
	v_rsq_f32_e32 v16, v10
	v_cvt_pk_bf16_f32 v10, v14, v15
	v_cndmask_b32_e64 v33, v29, -v29, vcc
	v_mov_b32_e32 v163, v161
	v_mul_f32_e32 v14, 0x45800000, v16
	v_cndmask_b32_e64 v48, v16, v14, s[4:5]
	v_pk_mul_f32 v[14:15], v[56:57], v[48:49] op_sel_hi:[1,0]
	v_pk_mul_f32 v[20:21], v[58:59], v[48:49] op_sel_hi:[1,0]
	v_pk_mul_f32 v[14:15], v[14:15], v[146:147]
	v_pk_mul_f32 v[20:21], v[20:21], v[152:153]
	v_pk_mul_f32 v[14:15], v[14:15], s[82:83] op_sel_hi:[1,0]
	v_pk_mul_f32 v[20:21], v[20:21], s[82:83] op_sel_hi:[1,0]
	v_cvt_pk_bf16_f32 v17, v14, v15
	v_pk_mul_f32 v[14:15], v[54:55], v[48:49] op_sel_hi:[1,0]
	v_cmp_gt_f32_e64 s[4:5], s95, v18
	v_pk_mul_f32 v[14:15], v[14:15], v[148:149]
	v_pk_mul_f32 v[102:103], v[66:67], v[48:49] op_sel_hi:[1,0]
	v_pk_mul_f32 v[14:15], v[14:15], s[82:83] op_sel_hi:[1,0]
	v_cndmask_b32_e64 v18, v18, v23, s[4:5]
	v_cvt_pk_bf16_f32 v16, v14, v15
; __device__ __forceinline__ unsigned cvtpk(float lo, float hi) { f32x2 v = {lo, hi}; bf16x2_t b = __builtin_convertvector(v, bf16x2_t); return __builtin_bit_cast(unsigned, b); }
; template <int DQK, int DV, bool LEAD> ...
;     ...
;           const float rn = rsqrtf(sn * (1.f / 64.f) + EPS);
; #pragma unroll
;           for (int ds = 0; ds < 2; ++ds)
; #pragma unroll
;               for (int j = 0; j < 8; ++j) x[ds][j] *= rn * qgain[32 * ds + 8 * g4 + j];
;           if constexpr (DQK == 64) {
; #pragma unroll
;               for (int ds = 0; ds < 2; ++ds)
; #pragma unroll
;                   for (int j = 0; j < 8; ++j) {
;                       auto rr = __builtin_amdgcn_permlane32_swap(__float_as_uint(x[ds][j]), __float_as_uint(x[ds][j]), false, false);
;                       const float other = hi ? __uint_as_float(rr[0]) : __uint_as_float(rr[1]);
;                       float cc = 1.f, sg = 0.f;
;                       if (lat) { const f32x2 cs = rope[(ds ? pcol : prow) * 16 + 8 * (g4 & 1) + j]; cc = cs.x; sg = hi ? cs.y : -cs.y; }
;                       x[ds][j] = x[ds][j] * cc + other * sg; }
;           } else {
;               float sr = 0.f;
; #pragma unroll
;               for (int j = 0; j < 8; ++j) sr += x[2][j] * x[2][j];
;               sr = lanes4_sum(sr);
;               const float rq = rsqrtf(sr * (1.f / 32.f) + EPS);
; #pragma unroll
;               for (int j = 0; j < 8; ++j) { const float av = x[2][j] * rq * qgain[64 + 8 * g4 + j];
;                   auto rr = __builtin_amdgcn_permlane16_swap(__float_as_uint(av), __float_as_uint(av), false, false);
;                   const float other = (g4 & 1) ? __uint_as_float(rr[0]) : __uint_as_float(rr[1]);
;                   float cc = 1.f, sg = 0.f;
;                   if (lat) { const f32x2 cs = rope[((g4 & 2) ? pcol : prow) * 8 + j]; cc = cs.x; sg = (g4 & 1) ? cs.y : -cs.y; }
;                   x[2][j] = av * cc + other * sg; }
;           }
; #pragma unroll
;           for (int ds = 0; ds < NDS; ++ds) { u32x4 w;
; #pragma unroll
;               for (int i = 0; i < 4; ++i) w[i] = cvtpk(x[ds][2 * i] * c2, x[ds][2 * i + 1] * c2);
;               qf[qb * NDS + ds] = __builtin_bit_cast(bf16x8, w); }
	v_pk_mul_f32 v[14:15], v[60:61], v[48:49] op_sel_hi:[1,0]
	v_pk_mul_f32 v[102:103], v[102:103], v[156:157]
	v_pk_mul_f32 v[14:15], v[14:15], v[150:151]
	v_rsq_f32_e32 v23, v18
	v_pk_mul_f32 v[14:15], v[14:15], s[82:83] op_sel_hi:[1,0]
	v_pk_mul_f32 v[102:103], v[102:103], s[82:83] op_sel_hi:[1,0]
	v_cvt_pk_bf16_f32 v15, v14, v15
	v_cvt_pk_bf16_f32 v14, v20, v21
	v_pk_mul_f32 v[20:21], v[68:69], v[48:49] op_sel_hi:[1,0]
	v_mul_f32_e32 v27, 0x45800000, v23
	v_pk_mul_f32 v[20:21], v[20:21], v[154:155]
	v_permlane32_swap_b32_e32 v161, v163
	v_pk_mul_f32 v[20:21], v[20:21], s[82:83] op_sel_hi:[1,0]
	v_mov_b32_e32 v143, v141
	v_cvt_pk_bf16_f32 v21, v20, v21
	v_cvt_pk_bf16_f32 v20, v102, v103
	v_pk_mul_f32 v[102:103], v[72:73], v[48:49] op_sel_hi:[1,0]
	v_pk_mul_f32 v[48:49], v[70:71], v[48:49] op_sel_hi:[1,0]
	v_pk_mul_f32 v[102:103], v[102:103], v[158:159]
	v_pk_mul_f32 v[48:49], v[48:49], v[166:167]
	v_pk_mul_f32 v[102:103], v[102:103], s[82:83] op_sel_hi:[1,0]
	v_pk_mul_f32 v[48:49], v[48:49], s[82:83] op_sel_hi:[1,0]
	v_cvt_pk_bf16_f32 v19, v102, v103
	v_cvt_pk_bf16_f32 v18, v48, v49
	v_cndmask_b32_e64 v48, v23, v27, s[4:5]
	v_pk_mul_f32 v[102:103], v[48:49], v[24:25] op_sel_hi:[0,1]
	v_pk_mul_f32 v[24:25], v[48:49], v[204:205] op_sel_hi:[0,1]
	v_pk_mul_f32 v[24:25], v[88:89], v[24:25]
	v_pk_mul_f32 v[106:107], v[48:49], v[228:229] op_sel_hi:[0,1]
	v_mov_b32_e32 v23, v24
	v_mov_b32_e32 v27, v24
	v_mov_b32_e32 v29, v25
	v_mov_b32_e32 v35, v25
	v_permlane16_swap_b32_e32 v23, v27
	s_nop 0
	v_permlane16_swap_b32_e32 v29, v35
	v_pk_mul_f32 v[146:147], v[48:49], v[210:211] op_sel_hi:[0,1]
	v_cndmask_b32_e32 v49, v29, v35, vcc
	v_cndmask_b32_e32 v48, v23, v27, vcc
	v_pk_mul_f32 v[48:49], v[182:183], v[48:49]
	v_permlane32_swap_b32_e32 v141, v143
	v_pk_fma_f32 v[24:25], v[24:25], v[98:99], v[48:49]
	v_pk_mul_f32 v[48:49], v[86:87], v[146:147]
	v_pk_mul_f32 v[24:25], v[24:25], s[82:83] op_sel_hi:[1,0]
	v_mov_b32_e32 v23, v48
	v_cvt_pk_bf16_f32 v25, v24, v25
	v_mov_b32_e32 v24, v48
	v_mov_b32_e32 v27, v49
	v_mov_b32_e32 v29, v49
	v_permlane16_swap_b32_e32 v23, v24
	s_nop 0
	v_permlane16_swap_b32_e32 v27, v29
	v_cndmask_b32_e32 v99, v27, v29, vcc
	v_cndmask_b32_e32 v98, v23, v24, vcc
	v_pk_mul_f32 v[98:99], v[208:209], v[98:99]
	s_nop 0
	v_pk_fma_f32 v[48:49], v[94:95], v[48:49], v[98:99]
	v_or_b32_e32 v206, 4, v194
	v_pk_mul_f32 v[48:49], v[48:49], s[82:83] op_sel_hi:[1,0]
	v_lshlrev_b32_e32 v207, 7, v221
	v_cvt_pk_bf16_f32 v24, v48, v49
	v_pk_mul_f32 v[48:49], v[92:93], v[106:107]
	v_lshrrev_b32_e32 v106, 1, v220
	v_mov_b32_e32 v23, v48
	v_mov_b32_e32 v27, v48
	v_mov_b32_e32 v29, v49
	v_mov_b32_e32 v35, v49
	v_permlane16_swap_b32_e32 v23, v27
	s_nop 0
	v_permlane16_swap_b32_e32 v29, v35
	v_cndmask_b32_e32 v95, v29, v35, vcc
	v_cndmask_b32_e32 v94, v23, v27, vcc
	v_pk_mul_f32 v[30:31], v[30:31], v[48:49]
	s_nop 0
	v_pk_fma_f32 v[30:31], v[176:177], v[94:95], v[30:31]
	v_cndmask_b32_e64 v94, v63, -v63, vcc
	v_pk_mul_f32 v[30:31], v[30:31], s[82:83] op_sel_hi:[1,0]
	v_cndmask_b32_e64 v95, v65, -v65, vcc
	v_cvt_pk_bf16_f32 v23, v30, v31
	v_pk_mul_f32 v[30:31], v[90:91], v[102:103]
	s_nop 0
	v_mov_b32_e32 v27, v30
	v_mov_b32_e32 v29, v30
	v_mov_b32_e32 v35, v31
	v_mov_b32_e32 v48, v31
	v_permlane16_swap_b32_e32 v27, v29
	s_nop 0
	v_permlane16_swap_b32_e32 v35, v48
	v_cndmask_b32_e32 v49, v35, v48, vcc
	v_cndmask_b32_e32 v48, v27, v29, vcc
	v_mov_b32_e32 v27, v28
	v_pk_mul_f32 v[26:27], v[26:27], v[30:31]
	s_nop 0
	v_pk_fma_f32 v[26:27], v[32:33], v[48:49], v[26:27]
	v_and_b32_e32 v49, 0xffff0000, v22
	v_lshlrev_b32_e32 v48, 16, v22
	v_mul_f32_e32 v22, v49, v49
	v_pk_fma_f32 v[28:29], v[48:49], v[48:49], v[22:23] op_sel_hi:[1,1,0]
	v_mul_f32_e32 v22, v37, v37
	v_pk_fma_f32 v[28:29], v[36:37], v[36:37], v[28:29]
	v_pk_mul_f32 v[26:27], v[26:27], s[82:83] op_sel_hi:[1,0]
	v_pk_add_f32 v[28:29], v[22:23], v[28:29] op_sel_hi:[0,1]
	v_pk_fma_f32 v[28:29], v[104:105], v[104:105], v[28:29]
	v_mul_f32_e32 v22, v105, v105
	v_pk_add_f32 v[28:29], v[22:23], v[28:29] op_sel_hi:[0,1]
	v_pk_fma_f32 v[28:29], v[164:165], v[164:165], v[28:29]
	v_mul_f32_e32 v22, v165, v165
	v_pk_add_f32 v[28:29], v[22:23], v[28:29] op_sel_hi:[0,1]
	v_mov_b32_e32 v22, v28
	s_nop 1
	v_permlane16_swap_b32_e32 v28, v22
	v_add_f32_e32 v160, v28, v22
	v_mov_b32_e32 v162, v160
	s_nop 1
	v_permlane32_swap_b32_e32 v160, v162
	v_pk_add_f32 v[28:29], v[160:161], v[162:163]
	s_nop 0
	v_pk_fma_f32 v[30:31], v[28:29], s[6:7], v[44:45] op_sel_hi:[1,1,0]
	s_nop 0
	v_mul_f32_e32 v22, 0x4b800000, v31
	v_cmp_gt_f32_e64 s[4:5], s95, v31
	v_mul_f32_e32 v35, 0x4b800000, v30
	s_nop 0
	v_cndmask_b32_e64 v22, v31, v22, s[4:5]
	v_rsq_f32_e32 v28, v22
	v_cvt_pk_bf16_f32 v22, v26, v27
	v_mul_f32_e32 v26, 0x45800000, v28
	v_cndmask_b32_e64 v98, v28, v26, s[4:5]
	v_pk_mul_f32 v[26:27], v[56:57], v[98:99] op_sel_hi:[1,0]
	v_pk_mul_f32 v[32:33], v[58:59], v[98:99] op_sel_hi:[1,0]
	v_pk_mul_f32 v[26:27], v[26:27], v[124:125]
	v_pk_mul_f32 v[32:33], v[32:33], v[130:131]
	v_pk_mul_f32 v[26:27], v[26:27], s[82:83] op_sel_hi:[1,0]
	v_pk_mul_f32 v[32:33], v[32:33], s[82:83] op_sel_hi:[1,0]
	v_cvt_pk_bf16_f32 v29, v26, v27
	v_pk_mul_f32 v[26:27], v[54:55], v[98:99] op_sel_hi:[1,0]
	v_cmp_gt_f32_e64 s[4:5], s95, v30
	v_pk_mul_f32 v[26:27], v[26:27], v[126:127]
	v_pk_mul_f32 v[102:103], v[66:67], v[98:99] op_sel_hi:[1,0]
	v_pk_mul_f32 v[26:27], v[26:27], s[82:83] op_sel_hi:[1,0]
	v_cndmask_b32_e64 v30, v30, v35, s[4:5]
	v_cvt_pk_bf16_f32 v28, v26, v27
	v_pk_mul_f32 v[26:27], v[60:61], v[98:99] op_sel_hi:[1,0]
	v_pk_mul_f32 v[102:103], v[102:103], v[136:137]
	v_pk_mul_f32 v[26:27], v[26:27], v[128:129]
	v_rsq_f32_e32 v35, v30
; __device__ __forceinline__ unsigned cvtpk(float lo, float hi) { f32x2 v = {lo, hi}; bf16x2_t b = __builtin_convertvector(v, bf16x2_t); return __builtin_bit_cast(unsigned, b); }
; template <int DQK, int DV, bool LEAD> ...
;     ...
;           const float rn = rsqrtf(sn * (1.f / 64.f) + EPS);
; #pragma unroll
;           for (int ds = 0; ds < 2; ++ds)
; #pragma unroll
;               for (int j = 0; j < 8; ++j) x[ds][j] *= rn * qgain[32 * ds + 8 * g4 + j];
;           if constexpr (DQK == 64) {
; #pragma unroll
;               for (int ds = 0; ds < 2; ++ds)
; #pragma unroll
;                   for (int j = 0; j < 8; ++j) {
;                       auto rr = __builtin_amdgcn_permlane32_swap(__float_as_uint(x[ds][j]), __float_as_uint(x[ds][j]), false, false);
;                       const float other = hi ? __uint_as_float(rr[0]) : __uint_as_float(rr[1]);
;                       float cc = 1.f, sg = 0.f;
;                       if (lat) { const f32x2 cs = rope[(ds ? pcol : prow) * 16 + 8 * (g4 & 1) + j]; cc = cs.x; sg = hi ? cs.y : -cs.y; }
;                       x[ds][j] = x[ds][j] * cc + other * sg; }
;           } else {
;               float sr = 0.f;
; #pragma unroll
;               for (int j = 0; j < 8; ++j) sr += x[2][j] * x[2][j];
;               sr = lanes4_sum(sr);
;               const float rq = rsqrtf(sr * (1.f / 32.f) + EPS);
; #pragma unroll
;               for (int j = 0; j < 8; ++j) { const float av = x[2][j] * rq * qgain[64 + 8 * g4 + j];
;                   auto rr = __builtin_amdgcn_permlane16_swap(__float_as_uint(av), __float_as_uint(av), false, false);
;                   const float other = (g4 & 1) ? __uint_as_float(rr[0]) : __uint_as_float(rr[1]);
;                   float cc = 1.f, sg = 0.f;
;                   if (lat) { const f32x2 cs = rope[((g4 & 2) ? pcol : prow) * 8 + j]; cc = cs.x; sg = (g4 & 1) ? cs.y : -cs.y; }
;                   x[2][j] = av * cc + other * sg; }
;           }
; #pragma unroll
;           for (int ds = 0; ds < NDS; ++ds) { u32x4 w;
; #pragma unroll
;               for (int i = 0; i < 4; ++i) w[i] = cvtpk(x[ds][2 * i] * c2, x[ds][2 * i + 1] * c2);
;               qf[qb * NDS + ds] = __builtin_bit_cast(bf16x8, w); }
	v_pk_mul_f32 v[26:27], v[26:27], s[82:83] op_sel_hi:[1,0]
	v_pk_mul_f32 v[102:103], v[102:103], s[82:83] op_sel_hi:[1,0]
	v_cvt_pk_bf16_f32 v27, v26, v27
	v_cvt_pk_bf16_f32 v26, v32, v33
	v_pk_mul_f32 v[32:33], v[68:69], v[98:99] op_sel_hi:[1,0]
	v_mul_f32_e32 v63, 0x45800000, v35
	v_pk_mul_f32 v[32:33], v[32:33], v[132:133]
	s_nop 0
	v_pk_mul_f32 v[32:33], v[32:33], s[82:83] op_sel_hi:[1,0]
	s_nop 0
	v_cvt_pk_bf16_f32 v33, v32, v33
	v_cvt_pk_bf16_f32 v32, v102, v103
	v_pk_mul_f32 v[102:103], v[72:73], v[98:99] op_sel_hi:[1,0]
	v_pk_mul_f32 v[98:99], v[70:71], v[98:99] op_sel_hi:[1,0]
	v_pk_mul_f32 v[102:103], v[102:103], v[138:139]
	v_pk_mul_f32 v[98:99], v[98:99], v[144:145]
	v_pk_mul_f32 v[102:103], v[102:103], s[82:83] op_sel_hi:[1,0]
	v_pk_mul_f32 v[98:99], v[98:99], s[82:83] op_sel_hi:[1,0]
	v_cvt_pk_bf16_f32 v31, v102, v103
	v_cvt_pk_bf16_f32 v30, v98, v99
	v_cndmask_b32_e64 v98, v35, v63, s[4:5]
	v_pk_mul_f32 v[102:103], v[98:99], v[36:37] op_sel_hi:[0,1]
	v_pk_mul_f32 v[36:37], v[98:99], v[164:165] op_sel_hi:[0,1]
	v_pk_mul_f32 v[36:37], v[88:89], v[36:37]
	v_pk_mul_f32 v[48:49], v[98:99], v[48:49] op_sel_hi:[0,1]
	v_pk_mul_f32 v[104:105], v[98:99], v[104:105] op_sel_hi:[0,1]
	v_mov_b32_e32 v35, v36
	v_mov_b32_e32 v63, v36
	v_mov_b32_e32 v65, v37
	v_mov_b32_e32 v98, v37
	v_permlane16_swap_b32_e32 v35, v63
	s_nop 0
	v_permlane16_swap_b32_e32 v65, v98
	v_cndmask_b32_e32 v99, v65, v98, vcc
	v_cndmask_b32_e32 v98, v35, v63, vcc
	v_pk_mul_f32 v[98:99], v[108:109], v[98:99]
	v_pk_mul_f32 v[48:49], v[90:91], v[48:49]
	v_pk_fma_f32 v[36:37], v[36:37], v[82:83], v[98:99]
	v_pk_mul_f32 v[82:83], v[86:87], v[104:105]
	v_pk_mul_f32 v[36:37], v[36:37], s[82:83] op_sel_hi:[1,0]
	v_mov_b32_e32 v35, v82
	v_cvt_pk_bf16_f32 v37, v36, v37
	v_mov_b32_e32 v36, v82
	v_mov_b32_e32 v63, v83
	v_mov_b32_e32 v65, v83
	v_permlane16_swap_b32_e32 v35, v36
	s_nop 0
	v_permlane16_swap_b32_e32 v63, v65
	v_cndmask_b32_e32 v99, v63, v65, vcc
	v_cndmask_b32_e32 v98, v35, v36, vcc
	v_pk_mul_f32 v[96:97], v[96:97], v[98:99]
	s_nop 0
	v_pk_fma_f32 v[78:79], v[78:79], v[82:83], v[96:97]
	s_nop 0
	v_pk_mul_f32 v[78:79], v[78:79], s[82:83] op_sel_hi:[1,0]
	s_nop 0
	v_cvt_pk_bf16_f32 v36, v78, v79
	v_pk_mul_f32 v[78:79], v[92:93], v[102:103]
	s_nop 0
	v_mov_b32_e32 v35, v78
	v_mov_b32_e32 v63, v78
	v_mov_b32_e32 v65, v79
	v_mov_b32_e32 v82, v79
	v_permlane16_swap_b32_e32 v35, v63
	s_nop 0
	v_permlane16_swap_b32_e32 v65, v82
	v_cndmask_b32_e32 v83, v65, v82, vcc
	v_cndmask_b32_e32 v82, v35, v63, vcc
	v_pk_mul_f32 v[74:75], v[74:75], v[78:79]
	v_mov_b32_e32 v63, v48
	v_pk_fma_f32 v[74:75], v[170:171], v[82:83], v[74:75]
	v_mov_b32_e32 v65, v48
	v_pk_mul_f32 v[74:75], v[74:75], s[82:83] op_sel_hi:[1,0]
	s_nop 0
	v_permlane16_swap_b32_e32 v63, v65
	v_cvt_pk_bf16_f32 v35, v74, v75
	v_mov_b32_e32 v74, v49
	v_mov_b32_e32 v75, v49
	s_nop 1
	v_permlane16_swap_b32_e32 v74, v75
	v_cndmask_b32_e32 v75, v74, v75, vcc
	v_cndmask_b32_e32 v74, v63, v65, vcc
	v_mov_b32_e32 v63, v64
	v_pk_mul_f32 v[48:49], v[62:63], v[48:49]
	v_and_b32_e32 v63, 0xffff0000, v34
	v_lshlrev_b32_e32 v62, 16, v34
	v_mul_f32_e32 v34, v63, v63
	v_pk_fma_f32 v[64:65], v[62:63], v[62:63], v[34:35] op_sel_hi:[1,1,0]
	v_mul_f32_e32 v34, v77, v77
	v_pk_fma_f32 v[64:65], v[76:77], v[76:77], v[64:65]
	v_pk_fma_f32 v[48:49], v[94:95], v[74:75], v[48:49]
	v_pk_add_f32 v[64:65], v[34:35], v[64:65] op_sel_hi:[0,1]
	v_pk_fma_f32 v[64:65], v[80:81], v[80:81], v[64:65]
	v_mul_f32_e32 v34, v81, v81
	v_pk_add_f32 v[64:65], v[34:35], v[64:65] op_sel_hi:[0,1]
	v_pk_fma_f32 v[64:65], v[100:101], v[100:101], v[64:65]
	v_mul_f32_e32 v34, v101, v101
	v_pk_add_f32 v[64:65], v[34:35], v[64:65] op_sel_hi:[0,1]
	v_mov_b32_e32 v34, v64
	s_nop 1
	v_permlane16_swap_b32_e32 v64, v34
	v_add_f32_e32 v140, v64, v34
	v_mov_b32_e32 v142, v140
	s_nop 1
	v_permlane32_swap_b32_e32 v140, v142
	v_pk_add_f32 v[64:65], v[140:141], v[142:143]
	v_pk_mul_f32 v[48:49], v[48:49], s[82:83] op_sel_hi:[1,0]
	v_pk_fma_f32 v[44:45], v[64:65], s[6:7], v[44:45] op_sel_hi:[1,1,0]
	v_lshlrev_b32_e32 v78, 5, v238
	v_mul_f32_e32 v34, 0x4b800000, v45
	v_cmp_gt_f32_e64 s[4:5], s95, v45
	v_lshlrev_b32_e32 v79, 6, v236
	v_bitop3_b32 v78, v78, v220, 48 bitop3:0x78
	v_cndmask_b32_e64 v34, v45, v34, s[4:5]
	v_rsq_f32_e32 v45, v34
	v_cvt_pk_bf16_f32 v34, v48, v49
	v_cndmask_b32_e64 v48, v51, -v51, vcc
	v_cndmask_b32_e64 v49, v53, -v53, vcc
	v_mul_f32_e32 v51, 0x45800000, v45
	v_cndmask_b32_e64 v64, v45, v51, s[4:5]
	v_mul_f32_e32 v45, 0x4b800000, v44
	v_cmp_gt_f32_e64 s[4:5], s95, v44
	v_pk_mul_f32 v[58:59], v[58:59], v[64:65] op_sel_hi:[1,0]
	v_pk_mul_f32 v[60:61], v[60:61], v[64:65] op_sel_hi:[1,0]
	v_cndmask_b32_e64 v44, v44, v45, s[4:5]
	v_pk_mul_f32 v[54:55], v[54:55], v[64:65] op_sel_hi:[1,0]
	v_rsq_f32_e32 v51, v44
	v_pk_mul_f32 v[58:59], v[58:59], v[116:117]
	v_pk_mul_f32 v[60:61], v[60:61], v[114:115]
	v_pk_mul_f32 v[74:75], v[54:55], v[112:113]
	v_pk_mul_f32 v[54:55], v[56:57], v[64:65] op_sel_hi:[1,0]
	v_pk_mul_f32 v[70:71], v[70:71], v[64:65] op_sel_hi:[1,0]
	v_pk_mul_f32 v[72:73], v[72:73], v[64:65] op_sel_hi:[1,0]
	v_pk_mul_f32 v[66:67], v[66:67], v[64:65] op_sel_hi:[1,0]
	v_pk_mul_f32 v[68:69], v[68:69], v[64:65] op_sel_hi:[1,0]
	v_pk_mul_f32 v[64:65], v[54:55], v[110:111]
	v_pk_mul_f32 v[58:59], v[58:59], s[82:83] op_sel_hi:[1,0]
	v_pk_mul_f32 v[60:61], v[60:61], s[82:83] op_sel_hi:[1,0]
	v_cvt_pk_bf16_f32 v58, v58, v59
	v_cvt_pk_bf16_f32 v59, v60, v61
	v_pk_mul_f32 v[60:61], v[74:75], s[82:83] op_sel_hi:[1,0]
	v_pk_mul_f32 v[44:45], v[64:65], s[82:83] op_sel_hi:[1,0]
	v_cvt_pk_bf16_f32 v60, v60, v61
	v_cvt_pk_bf16_f32 v61, v44, v45
	v_mul_f32_e32 v44, 0x45800000, v51
; __device__ __forceinline__ unsigned cvtpk(float lo, float hi) { f32x2 v = {lo, hi}; bf16x2_t b = __builtin_convertvector(v, bf16x2_t); return __builtin_bit_cast(unsigned, b); }
; #define ATT_SB() __builtin_amdgcn_sched_barrier(0)
; #define ATT_DMA_K(t, sl) do { glds16(ksrc + (size_t)(t) * 64 * kpitch, (unsigned)__builtin_amdgcn_readfirstlane(kdst + (sl) * KSLOT)); \
;         if constexpr (DQK == 96) glds16(krsrc + (size_t)(t) * 64 * 32, (unsigned)__builtin_amdgcn_readfirstlane(krdst + (sl) * KSLOT)); } while (0)
; #define ATT_DMA_V(t, sl) do { glds16(vsrc + (size_t)(t) * 64, (unsigned)__builtin_amdgcn_readfirstlane(vdst + (sl) * VSLOT)); \
;         if constexpr (DV == 128) glds16(vsrc + (size_t)64 * NR + (size_t)(t) * 64, (unsigned)__builtin_amdgcn_readfirstlane(vdst + (sl) * VSLOT + 8192)); } while (0)
; #define ATT_KLOAD(sl) do { _Pragma("unroll") for (int kb_ = 0; kb_ < NKW; ++kb_) _Pragma("unroll") for (int ds_ = 0; ds_ < NDS; ++ds_) { \
;         if (ds_ < 2) kf[kb_ * NDS + ds_] = *(const LAS bf16x8*)(kp[ds_ & 1] + (sl) * KSLOT + (kb_ & 1) * 512 + (kb_ >> 1) * 4096); \
;         else kf[kb_ * NDS + ds_] = *(const LAS bf16x8*)(krp + (sl) * KSLOT + (kb_ & 1) * 256 + (kb_ >> 1) * 2048); } } while (0)
; template <int DQK, int DV, bool LEAD> ...
;     ...
;           for (int ds = 0; ds < NDS; ++ds) { u32x4 w;
; #pragma unroll
;               for (int i = 0; i < 4; ++i) w[i] = cvtpk(x[ds][2 * i] * c2, x[ds][2 * i + 1] * c2);
;               qf[qb * NDS + ds] = __builtin_bit_cast(bf16x8, w); }
;       }
; #pragma unroll
;       for (int d0 = 0; d0 < NQB * NDS; ++d0) asm volatile("" : "+v"(qf[d0])); }
;     wait_bar<0>();
;     bf16x8 kf[NKW * NDS], vf[NVF];
;     ATT_KLOAD(0);
;     asm volatile("s_waitcnt lgkmcnt(0)\n\ts_barrier" ::: "memory");
;     float lsum[NQB];
; #pragma unroll
;     for (int qb = 0; qb < NQB; ++qb) lsum[qb] = 0.f;
;     const f32x4 zero4 = {0.f, 0.f, 0.f, 0.f};
;     f32x4 o[NDB][NQB], c[NKW][NQB]; u32x4 pw[4];
; #pragma unroll
;     for (int i = 0; i < NDB; ++i)
; #pragma unroll
;         for (int qb = 0; qb < NQB; ++qb) o[i][qb] = zero4;
;     ATT_DMA_K(3, 0); ATT_DMA_V(1, 1);
;     ATT_QK(); ATT_SB();
;     ATT_KLOAD(1); ATT_SB();
	v_cndmask_b32_e64 v44, v51, v44, s[4:5]
	v_pk_mul_f32 v[62:63], v[44:45], v[62:63] op_sel_hi:[0,1]
	v_pk_mul_f32 v[62:63], v[90:91], v[62:63]
	v_pk_mul_f32 v[70:71], v[70:71], v[134:135]
	v_mov_b32_e32 v45, v62
	v_mov_b32_e32 v51, v62
	v_mov_b32_e32 v53, v63
	v_mov_b32_e32 v64, v63
	v_permlane16_swap_b32_e32 v45, v51
	s_nop 0
	v_permlane16_swap_b32_e32 v53, v64
	v_cndmask_b32_e32 v65, v53, v64, vcc
	v_cndmask_b32_e32 v64, v45, v51, vcc
	v_mov_b32_e32 v51, v52
	v_pk_mul_f32 v[50:51], v[50:51], v[62:63]
	v_pk_mul_f32 v[72:73], v[72:73], v[122:123]
	v_pk_fma_f32 v[48:49], v[48:49], v[64:65], v[50:51]
	v_pk_mul_f32 v[50:51], v[44:45], v[76:77] op_sel_hi:[0,1]
	v_pk_mul_f32 v[50:51], v[92:93], v[50:51]
	v_pk_mul_f32 v[66:67], v[66:67], v[120:121]
	v_mov_b32_e32 v45, v50
	v_mov_b32_e32 v52, v50
	s_nop 1
	v_permlane16_swap_b32_e32 v45, v52
	v_mov_b32_e32 v53, v51
	v_mov_b32_e32 v62, v51
	s_nop 1
	v_permlane16_swap_b32_e32 v53, v62
	v_pk_mul_f32 v[46:47], v[46:47], v[50:51]
	v_pk_mul_f32 v[50:51], v[44:45], v[80:81] op_sel_hi:[0,1]
	v_cndmask_b32_e32 v53, v53, v62, vcc
	v_cndmask_b32_e32 v52, v45, v52, vcc
	v_pk_mul_f32 v[50:51], v[86:87], v[50:51]
	v_pk_fma_f32 v[46:47], v[168:169], v[52:53], v[46:47]
	v_mov_b32_e32 v45, v50
	v_mov_b32_e32 v52, v50
	v_mov_b32_e32 v53, v51
	v_mov_b32_e32 v62, v51
	v_permlane16_swap_b32_e32 v45, v52
	s_nop 0
	v_permlane16_swap_b32_e32 v53, v62
	v_cndmask_b32_e32 v53, v53, v62, vcc
	v_cndmask_b32_e32 v52, v45, v52, vcc
	v_pk_mul_f32 v[40:41], v[40:41], v[52:53]
	v_pk_mul_f32 v[68:69], v[68:69], v[118:119]
	v_pk_fma_f32 v[40:41], v[42:43], v[50:51], v[40:41]
	v_pk_mul_f32 v[42:43], v[44:45], v[100:101] op_sel_hi:[0,1]
	v_pk_mul_f32 v[42:43], v[88:89], v[42:43]
	v_pk_mul_f32 v[54:55], v[70:71], s[82:83] op_sel_hi:[1,0]
	v_mov_b32_e32 v44, v42
	v_mov_b32_e32 v50, v42
	v_mov_b32_e32 v45, v43
	v_mov_b32_e32 v51, v43
	v_permlane16_swap_b32_e32 v44, v50
	s_nop 0
	v_permlane16_swap_b32_e32 v45, v51
	v_cndmask_b32_e32 v45, v45, v51, vcc
	v_cndmask_b32_e32 v44, v44, v50, vcc
	v_pk_mul_f32 v[44:45], v[84:85], v[44:45]
	v_pk_mul_f32 v[56:57], v[72:73], s[82:83] op_sel_hi:[1,0]
	v_pk_fma_f32 v[42:43], v[42:43], v[38:39], v[44:45]
	v_cvt_pk_bf16_f32 v54, v54, v55
	v_cvt_pk_bf16_f32 v55, v56, v57
	v_pk_mul_f32 v[56:57], v[66:67], s[82:83] op_sel_hi:[1,0]
	v_pk_mul_f32 v[66:67], v[68:69], s[82:83] op_sel_hi:[1,0]
	v_pk_mul_f32 v[38:39], v[48:49], s[82:83] op_sel_hi:[1,0]
	v_pk_mul_f32 v[44:45], v[46:47], s[82:83] op_sel_hi:[1,0]
	v_pk_mul_f32 v[40:41], v[40:41], s[82:83] op_sel_hi:[1,0]
	v_pk_mul_f32 v[42:43], v[42:43], s[82:83] op_sel_hi:[1,0]
	v_cvt_pk_bf16_f32 v56, v56, v57
	v_cvt_pk_bf16_f32 v57, v66, v67
	v_cvt_pk_bf16_f32 v38, v38, v39
	v_cvt_pk_bf16_f32 v39, v44, v45
	v_cvt_pk_bf16_f32 v40, v40, v41
	v_cvt_pk_bf16_f32 v41, v42, v43
	s_waitcnt vmcnt(0) lgkmcnt(0)
	s_barrier
	ds_read_b128 v[42:45], v219
	ds_read_b128 v[46:49], v219 offset:512
	v_bitop3_b32 v70, v240, v206, v239 bitop3:0x36
	v_lshl_add_u32 v208, v70, 4, v241
	s_waitcnt lgkmcnt(1)
	v_mfma_f32_16x16x32_bf16 v[50:53], v[42:45], v[6:9], 0
	ds_read_b128 v[70:73], v208
	ds_read_b128 v[74:77], v208 offset:512
	s_lshl_b32 s4, s16, 11
	v_sub_u32_e32 v79, v237, v79
	v_mfma_f32_16x16x32_bf16 v[62:65], v[42:45], v[18:21], 0
	v_add3_u32 v209, v79, v78, s4
	s_mov_b64 s[4:5], 0x60000
	s_lshl_b32 s6, s24, 6
	v_mfma_f32_16x16x32_bf16 v[66:69], v[42:45], v[30:33], 0
	s_cmpk_lt_u32 s38, 0x100
	s_cselect_b64 vcc, -1, 0
	s_mov_b32 s16, 1
	v_mfma_f32_16x16x32_bf16 v[42:45], v[42:45], v[54:57], 0
	s_mov_b32 s7, 2
	s_mov_b32 s24, 0
	s_waitcnt lgkmcnt(1)
	v_mfma_f32_16x16x32_bf16 v[50:53], v[70:73], v[2:5], v[50:53]
	v_mfma_f32_16x16x32_bf16 v[62:65], v[70:73], v[14:17], v[62:65]
	v_mfma_f32_16x16x32_bf16 v[66:69], v[70:73], v[26:29], v[66:69]
	v_mfma_f32_16x16x32_bf16 v[42:45], v[70:73], v[58:61], v[42:45]
	ds_read_b128 v[70:73], v209 offset:8192
	ds_read_b128 v[78:81], v209 offset:8448
	s_waitcnt lgkmcnt(0)
	s_barrier
; #define LAS __attribute__((address_space(3)))
; #define ATT_SB() __builtin_amdgcn_sched_barrier(0)
; #define ATT_DMA_K(t, sl) do { glds16(ksrc + (size_t)(t) * 64 * kpitch, (unsigned)__builtin_amdgcn_readfirstlane(kdst + (sl) * KSLOT)); \
;         if constexpr (DQK == 96) glds16(krsrc + (size_t)(t) * 64 * 32, (unsigned)__builtin_amdgcn_readfirstlane(krdst + (sl) * KSLOT)); } while (0)
; #define ATT_DMA_V(t, sl) do { glds16(vsrc + (size_t)(t) * 64, (unsigned)__builtin_amdgcn_readfirstlane(vdst + (sl) * VSLOT)); \
;         if constexpr (DV == 128) glds16(vsrc + (size_t)64 * NR + (size_t)(t) * 64, (unsigned)__builtin_amdgcn_readfirstlane(vdst + (sl) * VSLOT + 8192)); } while (0)
; #define ATT_KLOAD(sl) do { _Pragma("unroll") for (int kb_ = 0; kb_ < NKW; ++kb_) _Pragma("unroll") for (int ds_ = 0; ds_ < NDS; ++ds_) { \
;         if (ds_ < 2) kf[kb_ * NDS + ds_] = *(const LAS bf16x8*)(kp[ds_ & 1] + (sl) * KSLOT + (kb_ & 1) * 512 + (kb_ >> 1) * 4096); \
;         else kf[kb_ * NDS + ds_] = *(const LAS bf16x8*)(krp + (sl) * KSLOT + (kb_ & 1) * 256 + (kb_ >> 1) * 2048); } } while (0)
; template <int DQK, int DV, bool LEAD> ...
;     ...
;     const int kr0 = 8 * (q16 >> 2) + (q16 & 3);
;     const int fk = ((kr0 >> 1) & 1) | (((kr0 >> 3) & 1) << 1) | (((kr0 >> 4) & 1) << 2);
;     const LAS unsigned char* kp[2]; const LAS unsigned char* vp[2];
; #pragma unroll
;     for (int ds = 0; ds < 2; ++ds) kp[ds] = shm + KOFF + kr0 * 128 + ((((ds << 2) | g4) ^ fk) << 4) + kg * 4096;
;     const LAS unsigned char* krp = shm + KOFF + 8192 + kr0 * 64 + ((g4 ^ (((kr0 >> 4) & 1) << 1)) << 4) + kg * 2048;
; #pragma unroll
;     for (int s_ = 0; s_ < 2; ++s_) vp[s_] = shm + VOFF + q16 * 128 + ((((s_ << 2) | g4) ^ ((q16 >> 1) & 7)) << 4);
;     const LAS unsigned char* vpk = kg ? vp[1] : vp[0];
;     ...
; #pragma unroll
;     for (int qb = 0; qb < NQB; ++qb) lsum[qb] = 0.f;
;     const f32x4 zero4 = {0.f, 0.f, 0.f, 0.f};
;     f32x4 o[NDB][NQB], c[NKW][NQB]; u32x4 pw[4];
; #pragma unroll
;     for (int i = 0; i < NDB; ++i)
; #pragma unroll
;         for (int qb = 0; qb < NQB; ++qb) o[i][qb] = zero4;
;     ATT_DMA_K(3, 0); ATT_DMA_V(1, 1);
;     ATT_QK(); ATT_SB();
;     ATT_KLOAD(1); ATT_SB();
;     if constexpr (LEAD) { ATT_EXP(); ATT_SUMPACK(); }
;     wait_bar<NDMA>();
;     int s_prev = 0, s_cur = 1, s_next = 2;
;     int one_ = 1; asm volatile("" : "+s"(one_));
	s_waitcnt lgkmcnt(1)
	v_mfma_f32_16x16x32_bf16 v[94:97], v[70:73], v[38:41], v[42:45]
	v_mfma_f32_16x16x32_bf16 v[42:45], v[46:49], v[6:9], 0
	v_mfma_f32_16x16x32_bf16 v[82:85], v[70:73], v[10:13], v[50:53]
	v_mfma_f32_16x16x32_bf16 v[86:89], v[70:73], v[22:25], v[62:65]
	v_mfma_f32_16x16x32_bf16 v[50:53], v[46:49], v[18:21], 0
	v_mfma_f32_16x16x32_bf16 v[62:65], v[46:49], v[30:33], 0
	v_mfma_f32_16x16x32_bf16 v[46:49], v[46:49], v[54:57], 0
	v_mfma_f32_16x16x32_bf16 v[42:45], v[74:77], v[2:5], v[42:45]
	v_mfma_f32_16x16x32_bf16 v[50:53], v[74:77], v[14:17], v[50:53]
	v_mfma_f32_16x16x32_bf16 v[62:65], v[74:77], v[26:29], v[62:65]
	v_mfma_f32_16x16x32_bf16 v[46:49], v[74:77], v[58:61], v[46:49]
	s_waitcnt lgkmcnt(0)
	v_mfma_f32_16x16x32_bf16 v[74:77], v[78:81], v[10:13], v[42:45]
	s_nop 2
	v_lshl_add_u64 v[42:43], v[186:187], 0, s[4:5]
	s_mov_b32 s4, m0
	s_mov_b32 m0, s42
	s_nop 0
	global_load_lds_dwordx4 v[42:43], off
	s_mov_b32 m0, s4
	s_mov_b64 s[4:5], 0x3000
	v_mfma_f32_16x16x32_bf16 v[90:93], v[70:73], v[34:37], v[66:69]
	v_lshl_add_u64 v[42:43], v[188:189], 0, s[4:5]
	s_mov_b32 s4, m0
	s_mov_b32 m0, s41
	s_nop 0
	global_load_lds_dwordx4 v[42:43], off
	s_mov_b32 m0, s4
	v_lshl_add_u64 v[42:43], v[190:191], 0, s[66:67]
	v_mfma_f32_16x16x32_bf16 v[98:101], v[78:81], v[22:25], v[50:53]
	s_add_i32 s4, s40, 0x2000
	s_mov_b32 s5, m0
	s_mov_b32 m0, s4
	s_nop 0
	global_load_lds_dwordx4 v[42:43], off
	s_mov_b32 m0, s5
	v_mfma_f32_16x16x32_bf16 v[102:105], v[78:81], v[34:37], v[62:65]
	v_mfma_f32_16x16x32_bf16 v[78:81], v[78:81], v[38:41], v[46:49]
	ds_read_b128 v[42:45], v219 offset:12288
	s_nop 1
	ds_read_b128 v[46:49], v219 offset:12800
	ds_read_b128 v[50:53], v208 offset:12288
	ds_read_b128 v[62:65], v208 offset:12800
	ds_read_b128 v[66:69], v209 offset:20480
	ds_read_b128 v[70:73], v209 offset:20736
	v_exp_f32_e32 v82, v82
	v_exp_f32_e32 v83, v83
	v_exp_f32_e32 v84, v84
	v_exp_f32_e32 v85, v85
	v_exp_f32_e32 v86, v86
	v_exp_f32_e32 v87, v87
	v_exp_f32_e32 v88, v88
	v_exp_f32_e32 v89, v89
	v_exp_f32_e32 v90, v90
	v_exp_f32_e32 v91, v91
	v_exp_f32_e32 v92, v92
	v_exp_f32_e32 v93, v93
	v_exp_f32_e32 v94, v94
	v_exp_f32_e32 v95, v95
	v_exp_f32_e32 v96, v96
	v_exp_f32_e32 v97, v97
	v_exp_f32_e32 v107, v74
	v_exp_f32_e32 v108, v75
	v_add_f32_e32 v74, v82, v83
	v_add_f32_e32 v75, v84, v85
	v_exp_f32_e32 v109, v76
	v_exp_f32_e32 v98, v98
	v_exp_f32_e32 v102, v102
	v_exp_f32_e32 v78, v78
	v_add_f32_e32 v74, v74, v75
	v_add_f32_e32 v75, v86, v87
	v_add_f32_e32 v76, v88, v89
	v_exp_f32_e32 v110, v77
	v_add_f32_e32 v75, v75, v76
	v_add_f32_e32 v76, v90, v91
	v_add_f32_e32 v77, v92, v93
	v_exp_f32_e32 v99, v99
	v_exp_f32_e32 v103, v103
	v_exp_f32_e32 v79, v79
	v_add_f32_e32 v76, v76, v77
	v_add_f32_e32 v77, v94, v95
	v_add_f32_e32 v111, v96, v97
	v_add_f32_e32 v77, v77, v111
	v_exp_f32_e32 v100, v100
	v_exp_f32_e32 v104, v104
	v_exp_f32_e32 v80, v80
	v_add_f32_e32 v74, v74, v107
	v_add_f32_e32 v75, v75, v98
	v_add_f32_e32 v76, v76, v102
	v_add_f32_e32 v77, v77, v78
	v_exp_f32_e32 v101, v101
	v_exp_f32_e32 v105, v105
	v_exp_f32_e32 v81, v81
	v_add_f32_e32 v74, v108, v74
	v_add_f32_e32 v75, v99, v75
	v_add_f32_e32 v76, v103, v76
	v_add_f32_e32 v77, v79, v77
	s_mov_b32 s4, 1
	v_add_f32_e32 v74, v109, v74
	v_add_f32_e32 v111, v100, v75
	v_add_f32_e32 v76, v104, v76
	v_add_f32_e32 v112, v80, v77
	v_cvt_pk_bf16_f32 v138, v82, v83
	v_add_f32_e32 v75, v110, v74
	v_add_f32_e32 v74, v101, v111
	v_add_f32_e32 v77, v105, v76
	v_add_f32_e32 v76, v81, v112
	s_waitcnt vmcnt(3) lgkmcnt(0)
	s_barrier
	s_cmp_lg_u32 s4, 0
	v_pk_add_f32 v[204:205], v[74:75], 0 op_sel_hi:[1,0]
	v_cndmask_b32_e32 v74, v206, v194, vcc
	v_bitop3_b32 v74, v74, v106, 7 bitop3:0x78
	v_lshlrev_b32_e32 v74, 4, v74
	v_add3_u32 v210, 0, v207, v74
	v_mov_b32_e32 v74, 0
	v_pk_add_f32 v[192:193], v[76:77], 0 op_sel_hi:[1,0]
	v_cvt_pk_bf16_f32 v139, v84, v85
	v_cvt_pk_bf16_f32 v140, v107, v108
	v_cvt_pk_bf16_f32 v141, v109, v110
	v_cvt_pk_bf16_f32 v142, v86, v87
	v_cvt_pk_bf16_f32 v143, v88, v89
	v_cvt_pk_bf16_f32 v144, v98, v99
	v_cvt_pk_bf16_f32 v145, v100, v101
	v_cvt_pk_bf16_f32 v146, v90, v91
	v_cvt_pk_bf16_f32 v147, v92, v93
	v_cvt_pk_bf16_f32 v148, v102, v103
	v_cvt_pk_bf16_f32 v149, v104, v105
	v_cvt_pk_bf16_f32 v150, v94, v95
	v_cvt_pk_bf16_f32 v151, v96, v97
	v_cvt_pk_bf16_f32 v152, v78, v79
	v_cvt_pk_bf16_f32 v153, v80, v81
	s_cselect_b64 s[4:5], -1, 0
	s_mov_b32 s38, 2
	v_mov_b32_e32 v75, v74
	v_mov_b32_e32 v76, v74
	v_mov_b32_e32 v77, v74
	v_mov_b32_e32 v78, v74
	v_mov_b32_e32 v79, v74
	v_mov_b32_e32 v80, v74
	v_mov_b32_e32 v81, v74
	v_mov_b32_e32 v82, v74
	v_mov_b32_e32 v83, v74
	v_mov_b32_e32 v84, v74
	v_mov_b32_e32 v85, v74
	v_mov_b32_e32 v86, v74
	v_mov_b32_e32 v87, v74
	v_mov_b32_e32 v88, v74
	v_mov_b32_e32 v89, v74
	v_mov_b32_e32 v90, v74
	v_mov_b32_e32 v91, v74
	v_mov_b32_e32 v92, v74
	v_mov_b32_e32 v93, v74
	v_mov_b32_e32 v94, v74
	v_mov_b32_e32 v95, v74
	v_mov_b32_e32 v96, v74
	v_mov_b32_e32 v97, v74
	v_mov_b32_e32 v98, v74
	v_mov_b32_e32 v99, v74
	v_mov_b32_e32 v100, v74
	v_mov_b32_e32 v101, v74
	v_mov_b32_e32 v102, v74
	v_mov_b32_e32 v103, v74
	v_mov_b32_e32 v104, v74
	v_mov_b32_e32 v105, v74
	v_mov_b32_e32 v106, v74
	v_mov_b32_e32 v107, v74
	v_mov_b32_e32 v108, v74
	v_mov_b32_e32 v109, v74
	v_mov_b32_e32 v110, v74
	v_mov_b32_e32 v111, v74
	v_mov_b32_e32 v112, v74
	v_mov_b32_e32 v113, v74
	v_mov_b32_e32 v114, v74
	v_mov_b32_e32 v115, v74
	v_mov_b32_e32 v116, v74
	v_mov_b32_e32 v117, v74
	v_mov_b32_e32 v118, v74
	v_mov_b32_e32 v119, v74
	v_mov_b32_e32 v120, v74
	v_mov_b32_e32 v121, v74
	v_mov_b32_e32 v122, v74
	v_mov_b32_e32 v123, v74
	v_mov_b32_e32 v124, v74
	v_mov_b32_e32 v125, v74
	v_mov_b32_e32 v126, v74
	v_mov_b32_e32 v127, v74
	v_mov_b32_e32 v128, v74
	v_mov_b32_e32 v129, v74
	v_mov_b32_e32 v130, v74
	v_mov_b32_e32 v131, v74
	v_mov_b32_e32 v132, v74
	v_mov_b32_e32 v133, v74
	v_mov_b32_e32 v134, v74
	v_mov_b32_e32 v135, v74
	v_mov_b32_e32 v136, v74
	v_mov_b32_e32 v137, v74
	s_branch .LBB0_650

; #define ATT_SB() __builtin_amdgcn_sched_barrier(0)
; #define ATT_KLOAD(sl) do { _Pragma("unroll") for (int kb_ = 0; kb_ < NKW; ++kb_) _Pragma("unroll") for (int ds_ = 0; ds_ < NDS; ++ds_) { \
;         if (ds_ < 2) kf[kb_ * NDS + ds_] = *(const LAS bf16x8*)(kp[ds_ & 1] + (sl) * KSLOT + (kb_ & 1) * 512 + (kb_ >> 1) * 4096); \
;         else kf[kb_ * NDS + ds_] = *(const LAS bf16x8*)(krp + (sl) * KSLOT + (kb_ & 1) * 256 + (kb_ >> 1) * 2048); } } while (0)
; #define ATT_QK() do { _Pragma("unroll") for (int kb_ = 0; kb_ < NKW; ++kb_) _Pragma("unroll") for (int ds_ = 0; ds_ < NDS; ++ds_) _Pragma("unroll") for (int qb_ = 0; qb_ < NQB; ++qb_) \
;         c[kb_][qb_] = __builtin_amdgcn_mfma_f32_16x16x32_bf16(kf[kb_ * NDS + ds_], qf[qb_ * NDS + ds_], ds_ == 0 ? zero4 : c[kb_][qb_], 0, 0, 0); } while (0)
; #define ATT_VLOAD(sl, h_) do { _Pragma("unroll") for (int g_ = 0; g_ < NVF; ++g_) { \
;         if constexpr (KS) vf[g_] = *(const LAS bf16x8*)(vpk + (sl) * VSLOT + g_ * 2048); \
;         else vf[g_] = *(const LAS bf16x8*)(vp[g_ & 1] + (sl) * VSLOT + ((h_) * 4 + (g_ >> 1)) * 2048); } } while (0)
; template <int DQK, int DV, bool LEAD> ...
;     ...
;             if (one_) ATT_KLOAD(s_next);
;             ATT_SB();
;             if constexpr (DV == 64) ATT_EXP();
;             ATT_SUMPACK();
;             asm volatile("" : "+v"(pw[0]), "+v"(pw[1]), "+v"(pw[2]), "+v"(pw[3]));
; #pragma unroll
;             for (int qb = 0; qb < NQB; ++qb) asm volatile("" : "+v"(lsum[qb]));
;         } else {
;             if constexpr (DV == 128) {
;                 ATT_PVP(0); ATT_SB();
;                 ATT_VLOAD(s_prev, 1); ATT_SB();
;                 ATT_QK(); ATT_SB();
;                 if (one_) { ATT_KLOAD(s_next); ATT_SB(); ATT_PVP(1); }
;                 ATT_SB();
;             } else {
;                 __builtin_amdgcn_s_setprio(1);
;                 ATT_QK(); ATT_SB();
;                 if (one_) { ATT_KLOAD(s_next); ATT_SB(); ATT_PVP(0); }
;                 ATT_SB();
;                 __builtin_amdgcn_s_setprio(0);
;             }
; #pragma unroll
;             for (int kb = 0; kb < NKW; ++kb)
; #pragma unroll
;                 for (int qb = 0; qb < NQB; ++qb) asm volatile("" : "+v"(c[kb][qb]));
;         }
;         ATT_SB();
;         wait_bar<NDMA>();
;         const int tmp = s_prev; s_prev = s_cur; s_cur = s_next; s_next = tmp;
.LBB0_652:
	v_exp_f32_e32 v138, v182
	v_exp_f32_e32 v139, v183
	v_exp_f32_e32 v140, v184
	v_exp_f32_e32 v141, v185
	v_exp_f32_e32 v142, v178
	v_exp_f32_e32 v143, v179
	v_exp_f32_e32 v144, v180
	v_exp_f32_e32 v145, v181
	v_exp_f32_e32 v146, v170
	v_exp_f32_e32 v147, v171
	v_exp_f32_e32 v148, v172
	v_exp_f32_e32 v149, v173
	v_exp_f32_e32 v150, v162
	v_exp_f32_e32 v151, v163
	v_exp_f32_e32 v152, v164
	v_exp_f32_e32 v153, v165
	v_add_f32_e32 v170, v138, v139
	v_add_f32_e32 v171, v140, v141
	v_exp_f32_e32 v162, v174
	v_exp_f32_e32 v166, v166
	v_exp_f32_e32 v158, v158
	v_exp_f32_e32 v154, v154
	v_add_f32_e32 v170, v170, v171
	v_add_f32_e32 v171, v142, v143
	v_add_f32_e32 v172, v144, v145
	v_add_f32_e32 v171, v171, v172
	v_add_f32_e32 v172, v146, v147
	v_add_f32_e32 v173, v148, v149
	v_exp_f32_e32 v163, v175
	v_exp_f32_e32 v167, v167
	v_exp_f32_e32 v159, v159
	v_exp_f32_e32 v155, v155
	v_add_f32_e32 v172, v172, v173
	v_add_f32_e32 v173, v150, v151
	v_add_f32_e32 v174, v152, v153
	v_add_f32_e32 v173, v173, v174
	v_exp_f32_e32 v164, v176
	v_exp_f32_e32 v168, v168
	v_exp_f32_e32 v160, v160
	v_exp_f32_e32 v156, v156
	v_add_f32_e32 v170, v170, v162
	v_add_f32_e32 v171, v171, v166
	v_add_f32_e32 v172, v172, v158
	v_add_f32_e32 v173, v173, v154
	v_exp_f32_e32 v165, v177
	v_exp_f32_e32 v169, v169
	v_exp_f32_e32 v161, v161
	v_exp_f32_e32 v157, v157
	v_add_f32_e32 v170, v163, v170
	v_add_f32_e32 v171, v167, v171
	v_add_f32_e32 v172, v159, v172
	v_add_f32_e32 v173, v155, v173
	v_cvt_pk_bf16_f32 v138, v138, v139
	v_add_f32_e32 v170, v164, v170
	v_add_f32_e32 v171, v168, v171
	v_add_f32_e32 v172, v160, v172
	v_add_f32_e32 v173, v156, v173
	v_cvt_pk_bf16_f32 v139, v140, v141
	v_add_f32_e32 v170, v165, v170
	v_add_f32_e32 v171, v169, v171
	v_add_f32_e32 v172, v161, v172
	v_add_f32_e32 v173, v157, v173
	v_cvt_pk_bf16_f32 v140, v162, v163
	v_add_f32_e32 v205, v205, v170
	v_add_f32_e32 v204, v204, v171
	v_add_f32_e32 v193, v193, v172
	v_add_f32_e32 v192, v192, v173
	v_cvt_pk_bf16_f32 v141, v164, v165
	v_cvt_pk_bf16_f32 v142, v142, v143
	v_cvt_pk_bf16_f32 v143, v144, v145
	v_cvt_pk_bf16_f32 v144, v166, v167
	v_cvt_pk_bf16_f32 v145, v168, v169
	v_cvt_pk_bf16_f32 v146, v146, v147
	v_cvt_pk_bf16_f32 v147, v148, v149
	v_cvt_pk_bf16_f32 v148, v158, v159
	v_cvt_pk_bf16_f32 v149, v160, v161
	v_cvt_pk_bf16_f32 v150, v150, v151
	v_cvt_pk_bf16_f32 v151, v152, v153
	v_cvt_pk_bf16_f32 v152, v154, v155
	v_cvt_pk_bf16_f32 v153, v156, v157
	s_waitcnt vmcnt(3) lgkmcnt(0)
	s_add_i32 s7, s7, 1
	s_cmpk_lg_i32 s7, 0x85
	s_cbranch_scc0 .Lx_rot1_exit
	s_mov_b32 s38, s24
	s_mov_b32 s24, s31
	s_branch .Lx_rot1_head

; template <int DQK, int DV, bool LEAD> ...
;     ...
;     int tid_ = threadIdx.x; asm volatile("" : "+v"(tid_));
;     const int tid = tid_, lane = tid & 63, q16 = lane & 15, g4 = lane >> 4, hi = lane >> 5; const int wid = __builtin_amdgcn_readfirstlane(tid >> 6);
;     const int kg = KS ? (wid >> 2) : 0, qoff = KS ? (wid & 3) * 64 : wid * 32;
;     const unsigned lds0 = (unsigned)(uintptr_t)shm;
;     const int krow_l = wid * 8 + (lane >> 3);
;     const int kc_l = (lane & 7) ^ (((krow_l >> 1) & 1) | (((krow_l >> 3) & 1) << 1) | (((krow_l >> 4) & 1) << 2));
;     const int vc_l = (lane & 7) ^ ((krow_l >> 1) & 7);
;     const bf16_t* ksrc = K + (size_t)(krow0 + krow_l) * kpitch + kc_l * 8;
;     const int rrow_l = (wid & 3) * 16 + (lane >> 2), rc_l = (lane & 3) ^ (((rrow_l >> 4) & 1) << 1);
;     const bf16_t* krsrc = (DQK == 96) ? KR + (size_t)(krow0 + rrow_l) * 32 + rc_l * 8 : nullptr;
;     const bf16_t* vsrc = Vt + (size_t)krow_l * NR + krow0 + vc_l * 8;
;     const unsigned kdst = lds0 + KOFF + wid * 1024, krdst = lds0 + KOFF + 8192 + (wid & 3) * 1024, vdst = lds0 + VOFF + wid * 1024;
;     ...
;     const int kr0 = 8 * (q16 >> 2) + (q16 & 3);
;     const int fk = ((kr0 >> 1) & 1) | (((kr0 >> 3) & 1) << 1) | (((kr0 >> 4) & 1) << 2);
;     const LAS unsigned char* kp[2]; const LAS unsigned char* vp[2];
; #pragma unroll
;     for (int ds = 0; ds < 2; ++ds) kp[ds] = shm + KOFF + kr0 * 128 + ((((ds << 2) | g4) ^ fk) << 4) + kg * 4096;
;     const LAS unsigned char* krp = shm + KOFF + 8192 + kr0 * 64 + ((g4 ^ (((kr0 >> 4) & 1) << 1)) << 4) + kg * 2048;
; #pragma unroll
;     for (int s_ = 0; s_ < 2; ++s_) vp[s_] = shm + VOFF + q16 * 128 + ((((s_ << 2) | g4) ^ ((q16 >> 1) & 7)) << 4);
;     const LAS unsigned char* vpk = kg ? vp[1] : vp[0];
;     ...
;     ATT_DMA_K(0, 0); ATT_DMA_V(0, 0); ATT_DMA_K(1, 1); ATT_DMA_K(2, 2);
;     bf16x8 qf[NQB * NDS];
;     {
; __global__ void __launch_bounds__(NWAVES * 64, 2) mega_fwd(Args args_) {
;     ...
;             for (int i = 0;; ++i) { const int u = i * F.G + F.vcu; if (u >= 2048) break; const int sid = u >> 5, qb = u & 31, b = sid >> 3, hc = sid & 7, h = hc >> 1, c = hc & 1;
;                 att::attn_unit<64, 128>(QK + h * 128 + c * 64, QKW, QK + 512 + h * 128 + c * 64, QKW, nullptr, VTE + (size_t)(h * 128) * NR, OB + hc * 128, 1024, b * TPS + qb * 256, b * TPS, 132, F.lds, IN(a, I_AQK) + j * 128, (const f32x2*)(ws + WS_ROPE64), qb * 256); }
.LBB0_939:
	s_lshl_b32 s6, s4, 1
	s_and_b32 s6, s6, 0x180
	s_lshr_b32 s5, s4, 8
	s_lshl_b32 s7, s6, 1
	s_add_u32 s16, s18, s7
	s_addc_u32 s22, s19, 0
	s_lshl_b32 s23, s4, 2
	s_and_b32 s23, s23, 0x80
	s_add_u32 s36, s16, s23
	s_addc_u32 s37, s22, 0
	s_add_u32 s7, s15, s7
	s_addc_u32 s16, s17, 0
	s_add_u32 s40, s7, s23
	s_addc_u32 s41, s16, 0
	s_mul_i32 s6, s6, 0x21000
	s_add_u32 s44, s10, s6
	s_addc_u32 s45, s11, 0
	s_lshl_b32 s6, s4, 3
	s_and_b32 s6, s6, 0x700
	s_add_u32 s26, s3, s6
	s_mov_b64 s[6:7], s[0:1]
	s_load_dwordx2 s[6:7], s[6:7], 0x48
	s_addc_u32 s27, s14, 0
	s_lshl_b32 s25, s4, 8
	s_mul_i32 s46, s5, 0x2100
	s_and_b32 s4, s25, 0x1f00
	s_add_i32 s30, s46, s4
	s_lshl_b64 s[22:23], s[20:21], 2
	s_waitcnt lgkmcnt(0)
	s_add_u32 s28, s6, s22
	s_addc_u32 s29, s7, s23
	v_readfirstlane_b32 s4, v0
	s_cmpk_gt_u32 s4, 0xff
	s_mov_b64 s[4:5], -1
	s_cbranch_scc0 .LBB0_946
	v_mov_b32_e32 v79, v0
	s_ashr_i32 s47, s46, 31
	v_readfirstlane_b32 s4, v79
	s_ashr_i32 s42, s4, 6
	v_bfe_u32 v1, v79, 3, 3
	v_lshl_or_b32 v6, s42, 3, v1
	s_lshl_b32 s5, s42, 1
	s_lshr_b32 s4, s4, 5
	v_ashrrev_i32_e32 v2, 1, v6
	s_and_b32 s5, s5, 2
	s_and_b32 s4, s4, 4
	v_and_b32_e32 v203, 7, v79
	v_and_b32_e32 v3, 1, v2
	s_or_b32 s4, s5, s4
	v_bitop3_b32 v7, s4, v203, v3 bitop3:0x36
	v_xor_b32_e32 v8, v2, v79
	v_add_u32_e32 v4, s46, v6
	v_mov_b64_e32 v[2:3], s[40:41]
	v_mad_i64_i32 v[2:3], s[4:5], v4, s92, v[2:3]
	v_mov_b64_e32 v[4:5], s[44:45]
	v_lshlrev_b32_e32 v194, 4, v7
	s_lshl_b32 s43, s42, 10
	v_mad_i64_i32 v[4:5], s[4:5], v6, s91, v[4:5]
	v_lshl_add_u64 v[204:205], v[2:3], 0, v[194:195]
	v_lshlrev_b32_e32 v2, 4, v8
	s_add_i32 s43, s43, 0
	v_lshl_add_u64 v[4:5], s[46:47], 1, v[4:5]
	v_and_b32_e32 v194, 0x70, v2
	s_mov_b32 s4, m0
	s_mov_b32 m0, s43
	s_nop 0
	global_load_lds_dwordx4 v[204:205], off
	s_mov_b32 m0, s4
	v_lshl_add_u64 v[206:207], v[4:5], 0, v[194:195]
	s_add_i32 s16, s43, 0x9000
	s_mov_b32 s4, m0
	s_mov_b32 m0, s16
	s_nop 0
	global_load_lds_dwordx4 v[206:207], off
	s_mov_b32 m0, s4
	s_mov_b64 s[4:5], 0x840000
	v_lshl_add_u64 v[208:209], v[206:207], 0, s[4:5]
	s_add_i32 s4, s16, 0x2000
	s_mov_b32 s5, m0
	s_mov_b32 m0, s4
	s_nop 0
	global_load_lds_dwordx4 v[208:209], off
	s_mov_b32 m0, s5
	s_mov_b64 s[4:5], 0x38000
	v_lshl_add_u64 v[2:3], v[204:205], 0, s[4:5]
	s_add_i32 s4, s43, 0x2000
	s_mov_b32 s5, m0
	s_mov_b32 m0, s4
	s_nop 0
	global_load_lds_dwordx4 v[2:3], off
	s_mov_b32 m0, s5
	s_lshl_b32 s6, s42, 5
	s_mov_b64 s[4:5], 0x70000
	v_and_b32_e32 v78, 15, v79
	v_lshl_add_u64 v[2:3], v[204:205], 0, s[4:5]
	s_add_i32 s31, s6, s30
	v_and_b32_e32 v194, 48, v79
	s_add_i32 s4, s43, 0x4000
	s_mov_b32 s5, m0
	s_mov_b32 m0, s4
	s_nop 0
	global_load_lds_dwordx4 v[2:3], off
	s_mov_b32 m0, s5
	v_or_b32_e32 v4, s31, v78
	v_lshl_add_u64 v[2:3], s[36:37], 0, v[194:195]
	v_lshrrev_b32_e32 v38, 1, v79
	v_or_b32_e32 v5, s6, v78
	v_mad_i64_i32 v[26:27], s[4:5], v4, s92, v[2:3]
	v_and_b32_e32 v28, 8, v38
	v_lshlrev_b32_e32 v5, 4, v5
	s_movk_i32 s4, 0x2f0
	v_or_b32_e32 v4, 16, v4
	v_and_or_b32 v5, v5, s4, v28
	v_mad_i64_i32 v[30:31], s[4:5], v4, s92, v[2:3]
	s_add_i32 s6, s6, s25
	s_lshr_b32 s4, s6, 2
	v_lshlrev_b32_e32 v22, 3, v5
	s_and_b32 s4, s4, 0x7f0
	global_load_dwordx4 v[50:53], v[26:27], off offset:64
	global_load_dwordx4 v[60:63], v22, s[8:9] offset:48
	global_load_dwordx4 v[70:73], v[30:31], off offset:64
	global_load_dwordx4 v[6:9], v22, s[8:9] offset:2096
	global_load_dwordx4 v[54:57], v22, s[8:9] offset:32
	global_load_dwordx4 v[14:17], v22, s[8:9] offset:2080
	global_load_dwordx4 v[2:5], v22, s[8:9] offset:16
	global_load_dwordx4 v[18:21], v22, s[8:9] offset:2064
	global_load_dwordx4 v[10:13], v22, s[8:9]
	s_nop 0
	global_load_dwordx4 v[22:25], v22, s[8:9] offset:2048
	s_nop 0
	global_load_dwordx4 v[82:85], v[26:27], off
	v_or_b32_e32 v26, s4, v28
	v_lshlrev_b32_e32 v39, 3, v26
	global_load_dwordx4 v[26:29], v39, s[8:9] offset:48
	global_load_dwordx4 v[86:89], v[30:31], off
	s_nop 0
	global_load_dwordx4 v[30:33], v39, s[8:9] offset:32
	global_load_dwordx4 v[34:37], v39, s[8:9] offset:16
	v_bfe_u32 v214, v79, 4, 2
	v_lshlrev_b32_e32 v215, 1, v79
	v_and_b32_e32 v40, 3, v79
	v_and_or_b32 v40, v215, 24, v40
	v_bitop3_b32 v38, v214, v38, 7 bitop3:0x78
	v_lshlrev_b32_e32 v59, 5, v214
	v_lshl_add_u32 v81, v40, 7, 0
	v_lshlrev_b32_e32 v80, 4, v38
	global_load_dwordx4 v[38:41], v39, s[8:9]
	s_nop 0
	global_load_dwordx4 v[42:45], v59, s[28:29] offset:144
	global_load_dwordx4 v[46:49], v59, s[28:29] offset:128
	v_and_b32_e32 v58, 63, v79
	v_cmp_gt_u32_e32 vcc, 32, v58
	s_mov_b32 s4, 0x3c800000
	v_add_u32_e32 v194, v81, v80
	v_lshlrev_b32_e32 v217, 7, v78
	s_mov_b32 s47, 1
	s_mov_b32 s48, 2
	v_or_b32_e32 v216, 4, v214
	s_waitcnt vmcnt(15)
	v_and_b32_e32 v65, 0xffff0000, v73
	v_lshlrev_b32_e32 v64, 16, v73
	v_and_b32_e32 v67, 0xffff0000, v72
	v_lshlrev_b32_e32 v66, 16, v72
	s_waitcnt vmcnt(13)
	v_cndmask_b32_e64 v95, v57, -v57, vcc
	v_cndmask_b32_e64 v94, v55, -v55, vcc
	v_and_b32_e32 v91, 0xffff0000, v53
	v_lshlrev_b32_e32 v90, 16, v53
	v_and_b32_e32 v93, 0xffff0000, v52
	s_waitcnt vmcnt(5)
; template <int DQK, int DV, bool LEAD> ...
;     ...
;           const bf16_t* qp = Q + (size_t)(qrow0 + qoff + qb * 16 + q16) * qpitch + g4 * 8;
;           bf16x8 raw[NDS];
; #pragma unroll
;           for (int ds = 0; ds < NDS; ++ds) raw[ds] = *(const bf16x8*)(qp + ds * 32);
;           float x[NDS][8];
; #pragma unroll
;           for (int ds = 0; ds < NDS; ++ds)
; #pragma unroll
;               for (int j = 0; j < 8; ++j) x[ds][j] = __uint_as_float(((unsigned)(unsigned short)raw[ds][j]) << 16);
;           const int tq = tq0 + qoff + qb * 16 + q16, prow = (tq >> 6) & 127, pcol = tq & 63;
;           float sn = 0.f;
; #pragma unroll
;           for (int ds = 0; ds < 2; ++ds)
; #pragma unroll
;               for (int j = 0; j < 8; ++j) sn += x[ds][j] * x[ds][j];
;           sn = lanes4_sum(sn);
;           const float rn = rsqrtf(sn * (1.f / 64.f) + EPS);
; #pragma unroll
;           for (int ds = 0; ds < 2; ++ds)
; #pragma unroll
;               for (int j = 0; j < 8; ++j) x[ds][j] *= rn * qgain[32 * ds + 8 * g4 + j];
;           if constexpr (DQK == 64) {
; #pragma unroll
;               for (int ds = 0; ds < 2; ++ds)
; #pragma unroll
;                   for (int j = 0; j < 8; ++j) {
;                       auto rr = __builtin_amdgcn_permlane32_swap(__float_as_uint(x[ds][j]), __float_as_uint(x[ds][j]), false, false);
;                       const float other = hi ? __uint_as_float(rr[0]) : __uint_as_float(rr[1]);
;                       float cc = 1.f, sg = 0.f;
;                       if (lat) { const f32x2 cs = rope[(ds ? pcol : prow) * 16 + 8 * (g4 & 1) + j]; cc = cs.x; sg = hi ? cs.y : -cs.y; }
;                       x[ds][j] = x[ds][j] * cc + other * sg; }
	v_and_b32_e32 v73, 0xffff0000, v89
	v_lshlrev_b32_e32 v72, 16, v89
	v_and_b32_e32 v75, 0xffff0000, v88
	v_lshlrev_b32_e32 v74, 16, v88
	v_and_b32_e32 v89, 0xffff0000, v83
	v_lshlrev_b32_e32 v88, 16, v83
	v_and_b32_e32 v83, 0xffff0000, v82
	v_lshlrev_b32_e32 v92, 16, v52
	v_mov_b32_e32 v55, v56
	v_and_b32_e32 v97, 0xffff0000, v51
	v_lshlrev_b32_e32 v96, 16, v51
	v_cndmask_b32_e64 v98, v3, -v3, vcc
	v_mov_b32_e32 v3, v4
	v_and_b32_e32 v101, 0xffff0000, v50
	v_lshlrev_b32_e32 v100, 16, v50
	global_load_dwordx4 v[50:53], v59, s[28:29] offset:16
	s_nop 0
	global_load_dwordx4 v[56:59], v59, s[28:29]
	v_lshlrev_b32_e32 v82, 16, v82
	v_mul_f32_e32 v4, v83, v83
	v_cndmask_b32_e64 v99, v5, -v5, vcc
	v_pk_fma_f32 v[4:5], v[82:83], v[82:83], v[4:5] op_sel_hi:[1,1,0]
	v_mul_f32_e32 v104, v89, v89
	v_pk_fma_f32 v[4:5], v[88:89], v[88:89], v[4:5]
	v_cndmask_b32_e64 v103, v13, -v13, vcc
	v_cndmask_b32_e64 v102, v11, -v11, vcc
	v_mov_b32_e32 v11, v12
	v_and_b32_e32 v13, 0xffff0000, v85
	v_lshlrev_b32_e32 v12, 16, v85
	v_and_b32_e32 v85, 0xffff0000, v84
	v_lshlrev_b32_e32 v84, 16, v84
	v_pk_add_f32 v[4:5], v[104:105], v[4:5] op_sel_hi:[0,1]
	v_pk_fma_f32 v[4:5], v[84:85], v[84:85], v[4:5]
	v_mul_f32_e32 v104, v85, v85
	v_pk_add_f32 v[4:5], v[104:105], v[4:5] op_sel_hi:[0,1]
	v_pk_fma_f32 v[4:5], v[12:13], v[12:13], v[4:5]
	v_mul_f32_e32 v104, v13, v13
	v_pk_add_f32 v[4:5], v[104:105], v[4:5] op_sel_hi:[0,1]
	v_pk_fma_f32 v[4:5], v[100:101], v[100:101], v[4:5]
	v_mul_f32_e32 v104, v101, v101
	v_pk_add_f32 v[4:5], v[104:105], v[4:5] op_sel_hi:[0,1]
	v_pk_fma_f32 v[4:5], v[96:97], v[96:97], v[4:5]
	v_mul_f32_e32 v104, v97, v97
	v_pk_add_f32 v[4:5], v[104:105], v[4:5] op_sel_hi:[0,1]
	v_pk_fma_f32 v[4:5], v[92:93], v[92:93], v[4:5]
	v_mul_f32_e32 v104, v93, v93
	v_pk_add_f32 v[4:5], v[104:105], v[4:5] op_sel_hi:[0,1]
	v_pk_fma_f32 v[4:5], v[90:91], v[90:91], v[4:5]
	v_mul_f32_e32 v104, v91, v91
	v_pk_add_f32 v[4:5], v[104:105], v[4:5] op_sel_hi:[0,1]
	v_mov_b32_e32 v5, v4
	s_nop 1
	v_permlane16_swap_b32_e32 v4, v5
	v_add_f32_e32 v5, v4, v5
	v_cndmask_b32_e64 v77, v63, -v63, vcc
	v_cndmask_b32_e64 v76, v61, -v61, vcc
	v_mov_b32_e32 v61, v62
	v_cndmask_b32_e64 v63, v9, -v9, vcc
	v_cndmask_b32_e64 v62, v7, -v7, vcc
	v_mov_b32_e32 v7, v8
	v_cndmask_b32_e64 v9, v17, -v17, vcc
	v_cndmask_b32_e64 v8, v15, -v15, vcc
	v_mov_b32_e32 v15, v16
	v_cndmask_b32_e64 v17, v21, -v21, vcc
	v_cndmask_b32_e64 v16, v19, -v19, vcc
	v_mov_b32_e32 v19, v20
	v_cndmask_b32_e64 v21, v25, -v25, vcc
	v_cndmask_b32_e64 v20, v23, -v23, vcc
	v_mov_b32_e32 v23, v24
	v_cndmask_b32_e64 v25, v29, -v29, vcc
	v_cndmask_b32_e64 v24, v27, -v27, vcc
	v_mov_b32_e32 v27, v28
	s_waitcnt vmcnt(6)
	v_cndmask_b32_e64 v29, v33, -v33, vcc
	v_cndmask_b32_e64 v28, v31, -v31, vcc
	v_mov_b32_e32 v31, v32
	s_waitcnt vmcnt(5)
	v_cndmask_b32_e64 v33, v37, -v37, vcc
	v_cndmask_b32_e64 v32, v35, -v35, vcc
	v_mov_b32_e32 v35, v36
	v_and_b32_e32 v37, 0xffff0000, v87
	v_lshlrev_b32_e32 v36, 16, v87
	v_mov_b32_e32 v87, v5
	v_and_b32_e32 v105, 0xffff0000, v86
	s_nop 0
	v_permlane32_swap_b32_e32 v5, v87
	v_lshlrev_b32_e32 v104, 16, v86
	v_mul_f32_e32 v4, v105, v105
	v_pk_fma_f32 v[106:107], v[104:105], v[104:105], v[4:5] op_sel_hi:[1,1,0]
	v_mul_f32_e32 v4, v37, v37
	v_pk_fma_f32 v[106:107], v[36:37], v[36:37], v[106:107]
	v_and_b32_e32 v69, 0xffff0000, v71
	v_pk_add_f32 v[106:107], v[4:5], v[106:107] op_sel_hi:[0,1]
	v_pk_fma_f32 v[106:107], v[74:75], v[74:75], v[106:107]
	v_mul_f32_e32 v4, v75, v75
	v_pk_add_f32 v[106:107], v[4:5], v[106:107] op_sel_hi:[0,1]
	v_pk_fma_f32 v[106:107], v[72:73], v[72:73], v[106:107]
	v_mul_f32_e32 v4, v73, v73
	v_lshlrev_b32_e32 v68, 16, v71
	v_and_b32_e32 v71, 0xffff0000, v70
	v_lshlrev_b32_e32 v70, 16, v70
	v_pk_add_f32 v[106:107], v[4:5], v[106:107] op_sel_hi:[0,1]
	v_pk_fma_f32 v[106:107], v[70:71], v[70:71], v[106:107]
	v_mul_f32_e32 v4, v71, v71
	v_pk_add_f32 v[106:107], v[4:5], v[106:107] op_sel_hi:[0,1]
	v_pk_fma_f32 v[106:107], v[68:69], v[68:69], v[106:107]
	v_mul_f32_e32 v4, v69, v69
	v_pk_add_f32 v[106:107], v[4:5], v[106:107] op_sel_hi:[0,1]
	v_pk_fma_f32 v[106:107], v[66:67], v[66:67], v[106:107]
	v_mul_f32_e32 v4, v67, v67
	v_pk_add_f32 v[106:107], v[4:5], v[106:107] op_sel_hi:[0,1]
	v_pk_fma_f32 v[106:107], v[64:65], v[64:65], v[106:107]
	v_mul_f32_e32 v4, v65, v65
	v_pk_add_f32 v[106:107], v[4:5], v[106:107] op_sel_hi:[0,1]
	v_mov_b32_e32 v4, v106
	s_nop 1
	v_permlane16_swap_b32_e32 v106, v4
	v_add_f32_e32 v4, v106, v4
	v_mov_b32_e32 v86, v4
	s_nop 1
	v_permlane32_swap_b32_e32 v4, v86
	v_pk_add_f32 v[4:5], v[4:5], v[86:87]
	s_waitcnt vmcnt(4)
	v_cndmask_b32_e64 v106, v39, -v39, vcc
	v_pk_fma_f32 v[86:87], v[4:5], s[4:5], v[196:197] op_sel_hi:[1,0,0]
	v_mov_b32_e32 v39, v40
	v_mul_f32_e32 v4, 0x4b800000, v87
	v_cmp_gt_f32_e64 s[4:5], s95, v87
	v_cndmask_b32_e64 v107, v41, -v41, vcc
	s_nop 0
	v_cndmask_b32_e64 v4, v87, v4, s[4:5]
	v_rsq_f32_e32 v4, v4
	s_nop 0
	v_mul_f32_e32 v5, 0x45800000, v4
	v_cndmask_b32_e64 v40, v4, v5, s[4:5]
	s_waitcnt vmcnt(3)
	v_pk_mul_f32 v[4:5], v[40:41], v[44:45] op_sel_hi:[0,1]
	v_pk_mul_f32 v[4:5], v[4:5], v[90:91]
	v_cmp_gt_f32_e64 s[4:5], s95, v86
	v_mov_b32_e32 v41, v4
	v_mov_b32_e32 v87, v4
	v_mov_b32_e32 v90, v5
	v_mov_b32_e32 v91, v5
	v_permlane32_swap_b32_e32 v41, v87
	s_nop 0
	v_permlane32_swap_b32_e32 v90, v91
	v_cndmask_b32_e32 v91, v90, v91, vcc
	v_cndmask_b32_e32 v90, v41, v87, vcc
	v_pk_mul_f32 v[76:77], v[76:77], v[90:91]
	s_nop 0
	v_pk_fma_f32 v[4:5], v[4:5], v[60:61], v[76:77]
	v_pk_mul_f32 v[60:61], v[40:41], v[42:43] op_sel_hi:[0,1]
	v_pk_mul_f32 v[4:5], v[4:5], s[94:95] op_sel_hi:[1,0]
	v_pk_mul_f32 v[60:61], v[60:61], v[92:93]
	v_cvt_pk_bf16_f32 v5, v4, v5
	v_mov_b32_e32 v4, v60
	v_mov_b32_e32 v41, v60
	v_mov_b32_e32 v76, v61
	v_mov_b32_e32 v77, v61
	v_permlane32_swap_b32_e32 v4, v41
	s_nop 0
	v_permlane32_swap_b32_e32 v76, v77
	v_cndmask_b32_e32 v77, v76, v77, vcc
	v_cndmask_b32_e32 v76, v4, v41, vcc
	v_pk_mul_f32 v[76:77], v[94:95], v[76:77]
	s_nop 0
	v_pk_fma_f32 v[54:55], v[60:61], v[54:55], v[76:77]
	s_nop 0
	v_pk_mul_f32 v[54:55], v[54:55], s[94:95] op_sel_hi:[1,0]
	s_nop 0
	v_cvt_pk_bf16_f32 v4, v54, v55
	s_waitcnt vmcnt(2)
; __device__ __forceinline__ unsigned cvtpk(float lo, float hi) { f32x2 v = {lo, hi}; bf16x2_t b = __builtin_convertvector(v, bf16x2_t); return __builtin_bit_cast(unsigned, b); }
; template <int DQK, int DV, bool LEAD> ...
;     ...
;           const float rn = rsqrtf(sn * (1.f / 64.f) + EPS);
; #pragma unroll
;           for (int ds = 0; ds < 2; ++ds)
; #pragma unroll
;               for (int j = 0; j < 8; ++j) x[ds][j] *= rn * qgain[32 * ds + 8 * g4 + j];
;           if constexpr (DQK == 64) {
; #pragma unroll
;               for (int ds = 0; ds < 2; ++ds)
; #pragma unroll
;                   for (int j = 0; j < 8; ++j) {
;                       auto rr = __builtin_amdgcn_permlane32_swap(__float_as_uint(x[ds][j]), __float_as_uint(x[ds][j]), false, false);
;                       const float other = hi ? __uint_as_float(rr[0]) : __uint_as_float(rr[1]);
;                       float cc = 1.f, sg = 0.f;
;                       if (lat) { const f32x2 cs = rope[(ds ? pcol : prow) * 16 + 8 * (g4 & 1) + j]; cc = cs.x; sg = hi ? cs.y : -cs.y; }
;                       x[ds][j] = x[ds][j] * cc + other * sg; }
;           } else {
;               float sr = 0.f;
; #pragma unroll
;               for (int j = 0; j < 8; ++j) sr += x[2][j] * x[2][j];
;               sr = lanes4_sum(sr);
;               const float rq = rsqrtf(sr * (1.f / 32.f) + EPS);
; #pragma unroll
;               for (int j = 0; j < 8; ++j) { const float av = x[2][j] * rq * qgain[64 + 8 * g4 + j];
;                   auto rr = __builtin_amdgcn_permlane16_swap(__float_as_uint(av), __float_as_uint(av), false, false);
;                   const float other = (g4 & 1) ? __uint_as_float(rr[0]) : __uint_as_float(rr[1]);
;                   float cc = 1.f, sg = 0.f;
;                   if (lat) { const f32x2 cs = rope[((g4 & 2) ? pcol : prow) * 8 + j]; cc = cs.x; sg = (g4 & 1) ? cs.y : -cs.y; }
;                   x[2][j] = av * cc + other * sg; }
;           }
; #pragma unroll
;           for (int ds = 0; ds < NDS; ++ds) { u32x4 w;
; #pragma unroll
;               for (int i = 0; i < 4; ++i) w[i] = cvtpk(x[ds][2 * i] * c2, x[ds][2 * i + 1] * c2);
;               qf[qb * NDS + ds] = __builtin_bit_cast(bf16x8, w); }
	v_pk_mul_f32 v[54:55], v[40:41], v[48:49] op_sel_hi:[0,1]
	v_pk_mul_f32 v[54:55], v[54:55], v[96:97]
	s_nop 0
	v_mov_b32_e32 v41, v54
	v_mov_b32_e32 v60, v54
	v_mov_b32_e32 v61, v55
	v_mov_b32_e32 v76, v55
	v_permlane32_swap_b32_e32 v41, v60
	s_nop 0
	v_permlane32_swap_b32_e32 v61, v76
	v_cndmask_b32_e32 v61, v61, v76, vcc
	v_cndmask_b32_e32 v60, v41, v60, vcc
	v_pk_mul_f32 v[60:61], v[98:99], v[60:61]
	s_nop 0
	v_pk_fma_f32 v[2:3], v[54:55], v[2:3], v[60:61]
	v_pk_mul_f32 v[54:55], v[46:47], v[40:41] op_sel_hi:[1,0]
	v_pk_mul_f32 v[2:3], v[2:3], s[94:95] op_sel_hi:[1,0]
	v_pk_mul_f32 v[54:55], v[54:55], v[100:101]
	v_cvt_pk_bf16_f32 v3, v2, v3
	v_mov_b32_e32 v2, v54
	v_mov_b32_e32 v41, v54
	v_mov_b32_e32 v60, v55
	v_mov_b32_e32 v61, v55
	v_permlane32_swap_b32_e32 v2, v41
	s_nop 0
	v_permlane32_swap_b32_e32 v60, v61
	v_cndmask_b32_e32 v61, v60, v61, vcc
	v_cndmask_b32_e32 v60, v2, v41, vcc
	v_pk_mul_f32 v[60:61], v[102:103], v[60:61]
	s_nop 0
	v_pk_fma_f32 v[10:11], v[54:55], v[10:11], v[60:61]
	s_nop 0
	v_pk_mul_f32 v[10:11], v[10:11], s[94:95] op_sel_hi:[1,0]
	s_nop 0
	v_cvt_pk_bf16_f32 v2, v10, v11
	s_waitcnt vmcnt(1)
	v_pk_mul_f32 v[10:11], v[52:53], v[40:41] op_sel_hi:[1,0]
	s_nop 0
	v_pk_mul_f32 v[10:11], v[10:11], v[12:13]
	s_nop 0
	v_mov_b32_e32 v12, v10
	v_mov_b32_e32 v41, v10
	v_mov_b32_e32 v13, v11
	v_mov_b32_e32 v54, v11
	v_permlane32_swap_b32_e32 v12, v41
	s_nop 0
	v_permlane32_swap_b32_e32 v13, v54
	v_cndmask_b32_e32 v13, v13, v54, vcc
	v_cndmask_b32_e32 v12, v12, v41, vcc
	v_pk_mul_f32 v[12:13], v[24:25], v[12:13]
	s_nop 0
	v_pk_fma_f32 v[10:11], v[10:11], v[26:27], v[12:13]
	s_nop 0
	v_pk_mul_f32 v[10:11], v[10:11], s[94:95] op_sel_hi:[1,0]
	s_nop 0
	v_cvt_pk_bf16_f32 v13, v10, v11
	v_pk_mul_f32 v[10:11], v[50:51], v[40:41] op_sel_hi:[1,0]
	s_nop 0
	v_pk_mul_f32 v[10:11], v[10:11], v[84:85]
	s_nop 0
	v_mov_b32_e32 v12, v10
	v_mov_b32_e32 v41, v10
	v_mov_b32_e32 v54, v11
	v_mov_b32_e32 v55, v11
	v_permlane32_swap_b32_e32 v12, v41
	s_nop 0
	v_permlane32_swap_b32_e32 v54, v55
	v_cndmask_b32_e32 v55, v54, v55, vcc
	v_cndmask_b32_e32 v54, v12, v41, vcc
	v_pk_mul_f32 v[54:55], v[28:29], v[54:55]
	s_nop 0
	v_pk_fma_f32 v[10:11], v[10:11], v[30:31], v[54:55]
	s_nop 0
	v_pk_mul_f32 v[10:11], v[10:11], s[94:95] op_sel_hi:[1,0]
	s_nop 0
	v_cvt_pk_bf16_f32 v12, v10, v11
	s_waitcnt vmcnt(0)
	v_pk_mul_f32 v[10:11], v[58:59], v[40:41] op_sel_hi:[1,0]
	s_nop 0
	v_pk_mul_f32 v[10:11], v[10:11], v[88:89]
	s_nop 0
	v_mov_b32_e32 v41, v10
	v_mov_b32_e32 v54, v10
	v_mov_b32_e32 v55, v11
	v_mov_b32_e32 v60, v11
	v_permlane32_swap_b32_e32 v41, v54
	s_nop 0
	v_permlane32_swap_b32_e32 v55, v60
	v_cndmask_b32_e32 v55, v55, v60, vcc
	v_cndmask_b32_e32 v54, v41, v54, vcc
	v_pk_mul_f32 v[54:55], v[32:33], v[54:55]
	v_pk_mul_f32 v[40:41], v[56:57], v[40:41] op_sel_hi:[1,0]
	v_pk_fma_f32 v[10:11], v[10:11], v[34:35], v[54:55]
	v_pk_mul_f32 v[40:41], v[40:41], v[82:83]
	v_pk_mul_f32 v[10:11], v[10:11], s[94:95] op_sel_hi:[1,0]
	v_mov_b32_e32 v54, v40
	v_cvt_pk_bf16_f32 v11, v10, v11
	v_mov_b32_e32 v10, v40
	s_nop 1
	v_permlane32_swap_b32_e32 v10, v54
	v_mov_b32_e32 v55, v41
	v_mov_b32_e32 v60, v41
	v_cndmask_b32_e32 v54, v10, v54, vcc
	v_mul_f32_e32 v10, 0x4b800000, v86
	v_permlane32_swap_b32_e32 v55, v60
	v_cndmask_b32_e64 v10, v86, v10, s[4:5]
	v_cndmask_b32_e32 v55, v55, v60, vcc
	v_rsq_f32_e32 v60, v10
	v_pk_mul_f32 v[54:55], v[106:107], v[54:55]
	s_nop 0
	v_pk_fma_f32 v[40:41], v[40:41], v[38:39], v[54:55]
	s_nop 0
	v_pk_mul_f32 v[40:41], v[40:41], s[94:95] op_sel_hi:[1,0]
	s_nop 0
	v_cvt_pk_bf16_f32 v10, v40, v41
	v_mul_f32_e32 v40, 0x45800000, v60
	v_cndmask_b32_e64 v40, v60, v40, s[4:5]
	v_pk_mul_f32 v[54:55], v[56:57], v[40:41] op_sel_hi:[1,0]
	v_pk_mul_f32 v[56:57], v[58:59], v[40:41] op_sel_hi:[1,0]
	v_pk_mul_f32 v[54:55], v[54:55], v[104:105]
	v_pk_mul_f32 v[36:37], v[56:57], v[36:37]
	v_pk_mul_f32 v[50:51], v[50:51], v[40:41] op_sel_hi:[1,0]
	v_pk_mul_f32 v[52:53], v[52:53], v[40:41] op_sel_hi:[1,0]
	v_pk_mul_f32 v[46:47], v[46:47], v[40:41] op_sel_hi:[1,0]
	v_pk_mul_f32 v[48:49], v[48:49], v[40:41] op_sel_hi:[1,0]
	v_pk_mul_f32 v[42:43], v[42:43], v[40:41] op_sel_hi:[1,0]
	v_pk_mul_f32 v[40:41], v[44:45], v[40:41] op_sel_hi:[1,0]
	v_mov_b32_e32 v44, v54
	v_mov_b32_e32 v56, v54
	v_mov_b32_e32 v45, v55
	v_mov_b32_e32 v57, v55
	v_permlane32_swap_b32_e32 v44, v56
	s_nop 0
	v_permlane32_swap_b32_e32 v45, v57
	v_cndmask_b32_e32 v45, v45, v57, vcc
	v_cndmask_b32_e32 v44, v44, v56, vcc
	v_pk_mul_f32 v[38:39], v[38:39], v[54:55]
	v_mov_b32_e32 v54, v36
	v_pk_fma_f32 v[38:39], v[106:107], v[44:45], v[38:39]
	v_mov_b32_e32 v44, v36
	v_mov_b32_e32 v45, v37
	v_mov_b32_e32 v55, v37
	v_permlane32_swap_b32_e32 v44, v54
	s_nop 0
	v_permlane32_swap_b32_e32 v45, v55
	v_pk_mul_f32 v[50:51], v[50:51], v[74:75]
	v_cndmask_b32_e32 v45, v45, v55, vcc
	v_cndmask_b32_e32 v44, v44, v54, vcc
	v_pk_mul_f32 v[34:35], v[34:35], v[36:37]
	v_mov_b32_e32 v36, v50
	v_pk_fma_f32 v[32:33], v[32:33], v[44:45], v[34:35]
	v_mov_b32_e32 v34, v50
	v_mov_b32_e32 v35, v51
	v_mov_b32_e32 v37, v51
	v_permlane32_swap_b32_e32 v34, v36
	s_nop 0
	v_permlane32_swap_b32_e32 v35, v37
	v_cndmask_b32_e32 v35, v35, v37, vcc
	v_cndmask_b32_e32 v34, v34, v36, vcc
	v_pk_mul_f32 v[52:53], v[52:53], v[72:73]
	v_pk_mul_f32 v[28:29], v[28:29], v[34:35]
	v_mov_b32_e32 v34, v52
	v_pk_fma_f32 v[28:29], v[30:31], v[50:51], v[28:29]
	v_mov_b32_e32 v30, v52
	v_mov_b32_e32 v31, v53
	v_mov_b32_e32 v35, v53
	v_permlane32_swap_b32_e32 v30, v34
	s_nop 0
	v_permlane32_swap_b32_e32 v31, v35
	v_cndmask_b32_e32 v31, v31, v35, vcc
	v_cndmask_b32_e32 v30, v30, v34, vcc
	v_pk_mul_f32 v[46:47], v[46:47], v[70:71]
; __device__ __forceinline__ unsigned cvtpk(float lo, float hi) { f32x2 v = {lo, hi}; bf16x2_t b = __builtin_convertvector(v, bf16x2_t); return __builtin_bit_cast(unsigned, b); }
; #define ATT_SB() __builtin_amdgcn_sched_barrier(0)
; #define ATT_DMA_K(t, sl) do { glds16(ksrc + (size_t)(t) * 64 * kpitch, (unsigned)__builtin_amdgcn_readfirstlane(kdst + (sl) * KSLOT)); \
;         if constexpr (DQK == 96) glds16(krsrc + (size_t)(t) * 64 * 32, (unsigned)__builtin_amdgcn_readfirstlane(krdst + (sl) * KSLOT)); } while (0)
; #define ATT_DMA_V(t, sl) do { glds16(vsrc + (size_t)(t) * 64, (unsigned)__builtin_amdgcn_readfirstlane(vdst + (sl) * VSLOT)); \
;         if constexpr (DV == 128) glds16(vsrc + (size_t)64 * NR + (size_t)(t) * 64, (unsigned)__builtin_amdgcn_readfirstlane(vdst + (sl) * VSLOT + 8192)); } while (0)
; #define ATT_KLOAD(sl) do { _Pragma("unroll") for (int kb_ = 0; kb_ < NKW; ++kb_) _Pragma("unroll") for (int ds_ = 0; ds_ < NDS; ++ds_) { \
;         if (ds_ < 2) kf[kb_ * NDS + ds_] = *(const LAS bf16x8*)(kp[ds_ & 1] + (sl) * KSLOT + (kb_ & 1) * 512 + (kb_ >> 1) * 4096); \
;         else kf[kb_ * NDS + ds_] = *(const LAS bf16x8*)(krp + (sl) * KSLOT + (kb_ & 1) * 256 + (kb_ >> 1) * 2048); } } while (0)
; template <int DQK, int DV, bool LEAD> ...
;     ...
;           for (int ds = 0; ds < NDS; ++ds) { u32x4 w;
; #pragma unroll
;               for (int i = 0; i < 4; ++i) w[i] = cvtpk(x[ds][2 * i] * c2, x[ds][2 * i + 1] * c2);
;               qf[qb * NDS + ds] = __builtin_bit_cast(bf16x8, w); }
;       }
; #pragma unroll
;       for (int d0 = 0; d0 < NQB * NDS; ++d0) asm volatile("" : "+v"(qf[d0])); }
;     wait_bar<0>();
;     bf16x8 kf[NKW * NDS], vf[NVF];
;     ATT_KLOAD(0);
;     asm volatile("s_waitcnt lgkmcnt(0)\n\ts_barrier" ::: "memory");
;     float lsum[NQB];
; #pragma unroll
;     for (int qb = 0; qb < NQB; ++qb) lsum[qb] = 0.f;
;     const f32x4 zero4 = {0.f, 0.f, 0.f, 0.f};
;     f32x4 o[NDB][NQB], c[NKW][NQB]; u32x4 pw[4];
; #pragma unroll
;     for (int i = 0; i < NDB; ++i)
; #pragma unroll
;         for (int qb = 0; qb < NQB; ++qb) o[i][qb] = zero4;
;     ATT_DMA_K(3, 0); ATT_DMA_V(1, 1);
;     ATT_QK(); ATT_SB();
;     ATT_KLOAD(1); ATT_SB();
;     if constexpr (LEAD) { ATT_EXP(); ATT_SUMPACK(); }
;     wait_bar<NDMA>();
;     int s_prev = 0, s_cur = 1, s_next = 2;
;     int one_ = 1; asm volatile("" : "+s"(one_));
	v_pk_mul_f32 v[24:25], v[24:25], v[30:31]
	v_mov_b32_e32 v30, v46
	v_pk_fma_f32 v[24:25], v[52:53], v[26:27], v[24:25]
	v_mov_b32_e32 v26, v46
	v_mov_b32_e32 v27, v47
	v_mov_b32_e32 v31, v47
	v_permlane32_swap_b32_e32 v26, v30
	s_nop 0
	v_permlane32_swap_b32_e32 v27, v31
	v_cndmask_b32_e32 v27, v27, v31, vcc
	v_cndmask_b32_e32 v26, v26, v30, vcc
	v_pk_mul_f32 v[48:49], v[48:49], v[68:69]
	v_pk_mul_f32 v[20:21], v[20:21], v[26:27]
	v_mov_b32_e32 v26, v48
	v_pk_fma_f32 v[20:21], v[46:47], v[22:23], v[20:21]
	v_mov_b32_e32 v22, v48
	v_mov_b32_e32 v23, v49
	v_mov_b32_e32 v27, v49
	v_permlane32_swap_b32_e32 v22, v26
	s_nop 0
	v_permlane32_swap_b32_e32 v23, v27
	v_cndmask_b32_e32 v23, v23, v27, vcc
	v_cndmask_b32_e32 v22, v22, v26, vcc
	v_pk_mul_f32 v[42:43], v[42:43], v[66:67]
	v_pk_mul_f32 v[16:17], v[16:17], v[22:23]
	v_mov_b32_e32 v22, v42
	v_pk_fma_f32 v[16:17], v[48:49], v[18:19], v[16:17]
	v_mov_b32_e32 v18, v42
	v_mov_b32_e32 v19, v43
	v_mov_b32_e32 v23, v43
	v_permlane32_swap_b32_e32 v18, v22
	s_nop 0
	v_permlane32_swap_b32_e32 v19, v23
	v_cndmask_b32_e32 v19, v19, v23, vcc
	v_cndmask_b32_e32 v18, v18, v22, vcc
	v_pk_mul_f32 v[40:41], v[40:41], v[64:65]
	v_pk_mul_f32 v[8:9], v[8:9], v[18:19]
	v_mov_b32_e32 v18, v40
	v_pk_fma_f32 v[8:9], v[42:43], v[14:15], v[8:9]
	v_mov_b32_e32 v14, v40
	v_mov_b32_e32 v15, v41
	v_mov_b32_e32 v19, v41
	v_permlane32_swap_b32_e32 v14, v18
	s_nop 0
	v_permlane32_swap_b32_e32 v15, v19
	v_cndmask_b32_e32 v15, v15, v19, vcc
	v_cndmask_b32_e32 v14, v14, v18, vcc
	v_pk_mul_f32 v[14:15], v[62:63], v[14:15]
	v_pk_mul_f32 v[8:9], v[8:9], s[94:95] op_sel_hi:[1,0]
	v_pk_fma_f32 v[6:7], v[40:41], v[6:7], v[14:15]
	v_pk_mul_f32 v[14:15], v[38:39], s[94:95] op_sel_hi:[1,0]
	v_pk_mul_f32 v[6:7], v[6:7], s[94:95] op_sel_hi:[1,0]
	v_cvt_pk_bf16_f32 v58, v14, v15
	v_pk_mul_f32 v[14:15], v[32:33], s[94:95] op_sel_hi:[1,0]
	v_cvt_pk_bf16_f32 v68, v8, v9
	v_cvt_pk_bf16_f32 v59, v14, v15
	v_pk_mul_f32 v[14:15], v[28:29], s[94:95] op_sel_hi:[1,0]
	v_cvt_pk_bf16_f32 v69, v6, v7
	v_cvt_pk_bf16_f32 v60, v14, v15
	v_pk_mul_f32 v[14:15], v[24:25], s[94:95] op_sel_hi:[1,0]
	v_bfe_u32 v22, v79, 1, 3
	v_cvt_pk_bf16_f32 v61, v14, v15
	v_pk_mul_f32 v[14:15], v[20:21], s[94:95] op_sel_hi:[1,0]
	v_bitop3_b32 v22, v214, v22, 4 bitop3:0x36
	v_cvt_pk_bf16_f32 v66, v14, v15
	v_pk_mul_f32 v[14:15], v[16:17], s[94:95] op_sel_hi:[1,0]
	v_lshlrev_b32_e32 v30, 4, v22
	v_cvt_pk_bf16_f32 v67, v14, v15
	s_waitcnt vmcnt(0) lgkmcnt(0)
	s_barrier
	ds_read_b128 v[6:9], v194
	ds_read_b128 v[14:17], v194 offset:512
	v_add_u32_e32 v220, v81, v30
	s_waitcnt lgkmcnt(1)
	v_mfma_f32_16x16x32_bf16 v[18:21], v[6:9], v[10:13], 0
	ds_read_b128 v[22:25], v220
	ds_read_b128 v[26:29], v220 offset:512
	v_add_u32_e32 v31, 0, v217
	v_add_u32_e32 v218, v31, v80
	v_mfma_f32_16x16x32_bf16 v[6:9], v[6:9], v[58:61], 0
	v_add_u32_e32 v219, v31, v30
	s_waitcnt lgkmcnt(1)
	v_mfma_f32_16x16x32_bf16 v[126:129], v[22:25], v[66:69], v[6:9]
	v_mfma_f32_16x16x32_bf16 v[6:9], v[14:17], v[10:13], 0
	s_waitcnt lgkmcnt(0)
	v_mfma_f32_16x16x32_bf16 v[122:125], v[26:29], v[2:5], v[6:9]
	v_mfma_f32_16x16x32_bf16 v[14:17], v[14:17], v[58:61], 0
	s_nop 4
	ds_read_b128 v[6:9], v194 offset:4096
	v_mfma_f32_16x16x32_bf16 v[138:141], v[22:25], v[2:5], v[18:21]
	v_mfma_f32_16x16x32_bf16 v[114:117], v[26:29], v[66:69], v[14:17]
	s_nop 2
	ds_read_b128 v[14:17], v220 offset:4096
	ds_read_b128 v[18:21], v194 offset:4608
	ds_read_b128 v[26:29], v220 offset:4608
	s_waitcnt lgkmcnt(0)
	s_barrier
	s_waitcnt lgkmcnt(3)
	v_mfma_f32_16x16x32_bf16 v[22:25], v[6:9], v[10:13], 0
	v_mfma_f32_16x16x32_bf16 v[6:9], v[6:9], v[58:61], 0
	s_waitcnt lgkmcnt(2)
	v_mfma_f32_16x16x32_bf16 v[130:133], v[14:17], v[2:5], v[22:25]
	s_nop 4
	v_lshl_add_u64 v[22:23], v[204:205], 0, s[96:97]
	v_mfma_f32_16x16x32_bf16 v[118:121], v[14:17], v[66:69], v[6:9]
	s_mov_b32 s4, m0
	s_mov_b32 m0, s43
	s_nop 0
	global_load_lds_dwordx4 v[22:23], off
	s_mov_b32 m0, s4
	v_lshl_add_u64 v[14:15], v[206:207], 0, s[66:67]
	s_add_i32 s4, s16, 0x4000
	s_waitcnt lgkmcnt(1)
	v_mfma_f32_16x16x32_bf16 v[6:9], v[18:21], v[10:13], 0
	s_mov_b32 s5, m0
	s_mov_b32 m0, s4
	s_nop 0
	global_load_lds_dwordx4 v[14:15], off
	s_mov_b32 m0, s5
	s_mov_b64 s[4:5], 0x840080
	v_lshl_add_u64 v[22:23], v[206:207], 0, s[4:5]
	v_mfma_f32_16x16x32_bf16 v[14:17], v[18:21], v[58:61], 0
	s_add_i32 s4, s16, 0x6000
	s_mov_b32 s5, m0
	s_mov_b32 m0, s4
	s_nop 0
	global_load_lds_dwordx4 v[22:23], off
	s_mov_b32 m0, s5
	s_mov_b32 s4, 0
	s_waitcnt lgkmcnt(0)
	v_mfma_f32_16x16x32_bf16 v[142:145], v[26:29], v[2:5], v[6:9]
	s_mov_b32 s6, s4
	s_mov_b32 s7, s4
	s_mov_b32 s5, s4
	v_mfma_f32_16x16x32_bf16 v[134:137], v[26:29], v[66:69], v[14:17]
	v_mov_b64_e32 v[8:9], s[6:7]
	v_mov_b64_e32 v[6:7], s[4:5]
	ds_read_b128 v[82:85], v194 offset:8192
	ds_read_b128 v[86:89], v194 offset:8704
	ds_read_b128 v[90:93], v220 offset:8192
	ds_read_b128 v[94:97], v220 offset:8704
	ds_read_b128 v[98:101], v194 offset:12288
	ds_read_b128 v[102:105], v194 offset:12800
	ds_read_b128 v[106:109], v220 offset:12288
	ds_read_b128 v[110:113], v220 offset:12800
	s_waitcnt vmcnt(3) lgkmcnt(0)
	s_barrier
	s_mov_b32 s5, 1
	v_mov_b32_e32 v42, 0
	s_cmp_lg_u32 s5, 0
	v_mov_b64_e32 v[16:17], v[8:9]
	v_mov_b64_e32 v[20:21], v[8:9]
	v_mov_b64_e32 v[24:25], v[8:9]
	v_mov_b64_e32 v[28:29], v[8:9]
	v_mov_b64_e32 v[32:33], v[8:9]
	v_mov_b64_e32 v[36:37], v[8:9]
	v_mov_b64_e32 v[40:41], v[8:9]
	s_cselect_b64 s[6:7], -1, 0
	v_mov_b64_e32 v[14:15], v[6:7]
	v_mov_b64_e32 v[18:19], v[6:7]
	v_mov_b64_e32 v[22:23], v[6:7]
	v_mov_b64_e32 v[26:27], v[6:7]
	v_mov_b64_e32 v[30:31], v[6:7]
	v_mov_b64_e32 v[34:35], v[6:7]
	v_mov_b64_e32 v[38:39], v[6:7]
	s_mov_b32 s38, 2
	v_mov_b32_e32 v43, v42
	v_mov_b32_e32 v44, v42
	v_mov_b32_e32 v45, v42
	v_mov_b32_e32 v46, v42
	v_mov_b32_e32 v47, v42
	v_mov_b32_e32 v48, v42
	v_mov_b32_e32 v49, v42
	v_mov_b32_e32 v50, v42
	v_mov_b32_e32 v51, v42
	v_mov_b32_e32 v52, v42
	v_mov_b32_e32 v53, v42
	v_mov_b32_e32 v54, v42
	v_mov_b32_e32 v55, v42
	v_mov_b32_e32 v56, v42
	v_mov_b32_e32 v57, v42
	v_mov_b32_e32 v62, v42
	v_mov_b32_e32 v63, v42
	v_mov_b32_e32 v64, v42
	v_mov_b32_e32 v65, v42
	v_mov_b32_e32 v70, v42
	v_mov_b32_e32 v71, v42
	v_mov_b32_e32 v72, v42
	v_mov_b32_e32 v73, v42
	v_mov_b32_e32 v74, v42
	v_mov_b32_e32 v75, v42
	v_mov_b32_e32 v76, v42
	v_mov_b32_e32 v77, v42
	v_mov_b32_e32 v78, v42
	v_mov_b32_e32 v79, v42
	v_mov_b32_e32 v80, v42
	v_mov_b32_e32 v81, v42
	v_mov_b32_e32 v210, v42
	v_mov_b32_e32 v211, v42
	s_branch .LBB0_941

; #define ATT_SB() __builtin_amdgcn_sched_barrier(0)
; template <int DQK, int DV, bool LEAD> ...
;     ...
;         ATT_SB();
;         wait_bar<NDMA>();
;         const int tmp = s_prev; s_prev = s_cur; s_cur = s_next; s_next = tmp;
.LBB0_943:
	v_add_f32_e32 v210, v210, v212
	v_add_f32_e32 v211, v211, v213
	s_waitcnt vmcnt(3) lgkmcnt(0)
	s_add_i32 s48, s48, 1
	s_cmpk_lg_i32 s48, 0x85
	s_cbranch_scc0 .Lx_rot2_exit
	s_mov_b32 s38, s4
	s_mov_b32 s4, s5
	s_branch .Lx_rot2_head

; #define LAS __attribute__((address_space(3)))
; template <int DQK, int DV, bool LEAD> ...
;     ...
;     int tid_ = threadIdx.x; asm volatile("" : "+v"(tid_));
;     const int tid = tid_, lane = tid & 63, q16 = lane & 15, g4 = lane >> 4, hi = lane >> 5; const int wid = __builtin_amdgcn_readfirstlane(tid >> 6);
;     const int kg = KS ? (wid >> 2) : 0, qoff = KS ? (wid & 3) * 64 : wid * 32;
;     const unsigned lds0 = (unsigned)(uintptr_t)shm;
;     const int krow_l = wid * 8 + (lane >> 3);
;     const int kc_l = (lane & 7) ^ (((krow_l >> 1) & 1) | (((krow_l >> 3) & 1) << 1) | (((krow_l >> 4) & 1) << 2));
;     const int vc_l = (lane & 7) ^ ((krow_l >> 1) & 7);
;     const bf16_t* ksrc = K + (size_t)(krow0 + krow_l) * kpitch + kc_l * 8;
;     const int rrow_l = (wid & 3) * 16 + (lane >> 2), rc_l = (lane & 3) ^ (((rrow_l >> 4) & 1) << 1);
;     const bf16_t* krsrc = (DQK == 96) ? KR + (size_t)(krow0 + rrow_l) * 32 + rc_l * 8 : nullptr;
;     const bf16_t* vsrc = Vt + (size_t)krow_l * NR + krow0 + vc_l * 8;
;     const unsigned kdst = lds0 + KOFF + wid * 1024, krdst = lds0 + KOFF + 8192 + (wid & 3) * 1024, vdst = lds0 + VOFF + wid * 1024;
;     ...
;     const int kr0 = 8 * (q16 >> 2) + (q16 & 3);
;     const int fk = ((kr0 >> 1) & 1) | (((kr0 >> 3) & 1) << 1) | (((kr0 >> 4) & 1) << 2);
;     const LAS unsigned char* kp[2]; const LAS unsigned char* vp[2];
; #pragma unroll
;     for (int ds = 0; ds < 2; ++ds) kp[ds] = shm + KOFF + kr0 * 128 + ((((ds << 2) | g4) ^ fk) << 4) + kg * 4096;
;     const LAS unsigned char* krp = shm + KOFF + 8192 + kr0 * 64 + ((g4 ^ (((kr0 >> 4) & 1) << 1)) << 4) + kg * 2048;
; #pragma unroll
;     for (int s_ = 0; s_ < 2; ++s_) vp[s_] = shm + VOFF + q16 * 128 + ((((s_ << 2) | g4) ^ ((q16 >> 1) & 7)) << 4);
;     const LAS unsigned char* vpk = kg ? vp[1] : vp[0];
;     ...
;     ATT_DMA_K(0, 0); ATT_DMA_V(0, 0); ATT_DMA_K(1, 1); ATT_DMA_K(2, 2);
;     bf16x8 qf[NQB * NDS];
;     {
;       const float c2 = (DQK == 64) ? C2_EVEN : C2_ODD; const bool lat = tq0 >= 0;
; #pragma unroll
;       for (int qb = 0; qb < NQB; ++qb) {
;           const bf16_t* qp = Q + (size_t)(qrow0 + qoff + qb * 16 + q16) * qpitch + g4 * 8;
;           bf16x8 raw[NDS];
; #pragma unroll
;           for (int ds = 0; ds < NDS; ++ds) raw[ds] = *(const bf16x8*)(qp + ds * 32);
;           float x[NDS][8];
; #pragma unroll
;           for (int ds = 0; ds < NDS; ++ds)
; #pragma unroll
.LBB0_946:
	s_and_b64 vcc, exec, s[4:5]
	s_cbranch_vccz .LBB0_938
	v_mov_b32_e32 v79, v0
	s_ashr_i32 s47, s46, 31
	v_readfirstlane_b32 s4, v79
	s_ashr_i32 s7, s4, 6
	v_bfe_u32 v1, v79, 3, 3
	v_lshl_or_b32 v6, s7, 3, v1
	s_lshl_b32 s5, s7, 1
	s_lshr_b32 s4, s4, 5
	v_ashrrev_i32_e32 v2, 1, v6
	s_and_b32 s5, s5, 2
	s_and_b32 s4, s4, 4
	v_and_b32_e32 v170, 7, v79
	v_and_b32_e32 v3, 1, v2
	s_or_b32 s4, s5, s4
	v_bitop3_b32 v7, s4, v170, v3 bitop3:0x36
	v_xor_b32_e32 v8, v2, v79
	v_add_u32_e32 v4, s46, v6
	s_lshl_b32 s4, s7, 10
	v_mov_b64_e32 v[2:3], s[40:41]
	s_add_i32 s31, s4, 0
	v_mad_i64_i32 v[2:3], s[4:5], v4, s92, v[2:3]
	v_mov_b64_e32 v[4:5], s[44:45]
	v_lshlrev_b32_e32 v194, 4, v7
	v_mad_i64_i32 v[4:5], s[4:5], v6, s91, v[4:5]
	v_lshl_add_u64 v[162:163], v[2:3], 0, v[194:195]
	v_lshlrev_b32_e32 v2, 4, v8
	v_lshl_add_u64 v[4:5], s[46:47], 1, v[4:5]
	v_and_b32_e32 v194, 0x70, v2
	s_mov_b32 s4, m0
	s_mov_b32 m0, s31
	s_nop 0
	global_load_lds_dwordx4 v[162:163], off
	s_mov_b32 m0, s4
	v_lshl_add_u64 v[164:165], v[4:5], 0, v[194:195]
	s_add_i32 s40, s31, 0x9000
	s_mov_b32 s4, m0
	s_mov_b32 m0, s40
	s_nop 0
	global_load_lds_dwordx4 v[164:165], off
	s_mov_b32 m0, s4
	s_mov_b64 s[4:5], 0x840000
	v_lshl_add_u64 v[166:167], v[164:165], 0, s[4:5]
	s_add_i32 s4, s40, 0x2000
	s_mov_b32 s5, m0
	s_mov_b32 m0, s4
	s_nop 0
	global_load_lds_dwordx4 v[166:167], off
	s_mov_b32 m0, s5
	s_mov_b64 s[4:5], 0x38000
	v_lshl_add_u64 v[2:3], v[162:163], 0, s[4:5]
	s_add_i32 s4, s31, 0x2000
	s_mov_b32 s5, m0
	s_mov_b32 m0, s4
	s_nop 0
	global_load_lds_dwordx4 v[2:3], off
	s_mov_b32 m0, s5
	s_lshl_b32 s16, s7, 5
	s_mov_b64 s[4:5], 0x70000
	v_and_b32_e32 v78, 15, v79
	v_lshl_add_u64 v[2:3], v[162:163], 0, s[4:5]
	s_add_i32 s6, s16, s30
	v_and_b32_e32 v194, 48, v79
	s_add_i32 s4, s31, 0x4000
	s_mov_b32 s5, m0
	s_mov_b32 m0, s4
	s_nop 0
	global_load_lds_dwordx4 v[2:3], off
	s_mov_b32 m0, s5
	v_or_b32_e32 v4, s6, v78
	v_lshl_add_u64 v[2:3], s[36:37], 0, v[194:195]
	v_lshrrev_b32_e32 v38, 1, v79
	v_or_b32_e32 v5, s16, v78
	v_mad_i64_i32 v[26:27], s[4:5], v4, s92, v[2:3]
	v_and_b32_e32 v28, 8, v38
	v_lshlrev_b32_e32 v5, 4, v5
	s_movk_i32 s4, 0x2f0
	v_or_b32_e32 v4, 16, v4
	v_and_or_b32 v5, v5, s4, v28
	v_mad_i64_i32 v[30:31], s[4:5], v4, s92, v[2:3]
	s_add_i32 s16, s16, s25
	s_lshr_b32 s4, s16, 2
	v_lshlrev_b32_e32 v22, 3, v5
	s_and_b32 s4, s4, 0x7f0
	global_load_dwordx4 v[50:53], v[26:27], off offset:64
	global_load_dwordx4 v[60:63], v22, s[8:9] offset:48
	global_load_dwordx4 v[70:73], v[30:31], off offset:64
	global_load_dwordx4 v[10:13], v22, s[8:9] offset:2096
	global_load_dwordx4 v[54:57], v22, s[8:9] offset:32
	global_load_dwordx4 v[14:17], v22, s[8:9] offset:2080
	global_load_dwordx4 v[2:5], v22, s[8:9] offset:16
	global_load_dwordx4 v[18:21], v22, s[8:9] offset:2064
	global_load_dwordx4 v[6:9], v22, s[8:9]
	s_nop 0
	global_load_dwordx4 v[22:25], v22, s[8:9] offset:2048
	s_nop 0
	global_load_dwordx4 v[82:85], v[26:27], off
	v_or_b32_e32 v26, s4, v28
	v_lshlrev_b32_e32 v39, 3, v26
	global_load_dwordx4 v[26:29], v39, s[8:9] offset:48
	global_load_dwordx4 v[86:89], v[30:31], off
	s_nop 0
	global_load_dwordx4 v[30:33], v39, s[8:9] offset:32
	global_load_dwordx4 v[34:37], v39, s[8:9] offset:16
	v_bfe_u32 v171, v79, 4, 2
	v_lshlrev_b32_e32 v172, 1, v79
	v_and_b32_e32 v40, 3, v79
	v_and_or_b32 v40, v172, 24, v40
	v_bitop3_b32 v38, v171, v38, 7 bitop3:0x78
	v_lshlrev_b32_e32 v59, 5, v171
	v_lshl_add_u32 v81, v40, 7, 0
	v_lshlrev_b32_e32 v80, 4, v38
	global_load_dwordx4 v[38:41], v39, s[8:9]
	s_nop 0
	global_load_dwordx4 v[42:45], v59, s[28:29] offset:144
	global_load_dwordx4 v[46:49], v59, s[28:29] offset:128
	v_and_b32_e32 v58, 63, v79
	v_cmp_gt_u32_e32 vcc, 32, v58
	s_mov_b32 s4, 0x3c800000
	v_add_u32_e32 v173, v81, v80
	v_lshlrev_b32_e32 v175, 7, v78
	s_mov_b32 s25, 1
	s_mov_b32 s16, 2
	v_or_b32_e32 v174, 4, v171
	s_waitcnt vmcnt(15)
	v_and_b32_e32 v65, 0xffff0000, v73
	v_lshlrev_b32_e32 v64, 16, v73
	v_and_b32_e32 v67, 0xffff0000, v72
	v_lshlrev_b32_e32 v66, 16, v72
	s_waitcnt vmcnt(13)
	v_cndmask_b32_e64 v95, v57, -v57, vcc
	v_cndmask_b32_e64 v94, v55, -v55, vcc
	v_and_b32_e32 v91, 0xffff0000, v53
	v_lshlrev_b32_e32 v90, 16, v53
	v_and_b32_e32 v93, 0xffff0000, v52
	s_waitcnt vmcnt(5)
	v_and_b32_e32 v73, 0xffff0000, v89
	v_lshlrev_b32_e32 v72, 16, v89
	v_and_b32_e32 v75, 0xffff0000, v88
	v_lshlrev_b32_e32 v74, 16, v88
	v_and_b32_e32 v89, 0xffff0000, v83
	v_lshlrev_b32_e32 v88, 16, v83
	v_and_b32_e32 v83, 0xffff0000, v82
	v_lshlrev_b32_e32 v92, 16, v52
	v_mov_b32_e32 v55, v56
	v_and_b32_e32 v97, 0xffff0000, v51
	v_lshlrev_b32_e32 v96, 16, v51
	v_cndmask_b32_e64 v98, v3, -v3, vcc
	v_mov_b32_e32 v3, v4
	v_and_b32_e32 v101, 0xffff0000, v50
	v_lshlrev_b32_e32 v100, 16, v50
	global_load_dwordx4 v[50:53], v59, s[28:29] offset:16
	s_nop 0
	global_load_dwordx4 v[56:59], v59, s[28:29]
	v_lshlrev_b32_e32 v82, 16, v82
	v_mul_f32_e32 v4, v83, v83
	v_cndmask_b32_e64 v99, v5, -v5, vcc
	v_pk_fma_f32 v[4:5], v[82:83], v[82:83], v[4:5] op_sel_hi:[1,1,0]
	v_mul_f32_e32 v104, v89, v89
	v_pk_fma_f32 v[4:5], v[88:89], v[88:89], v[4:5]
	v_cndmask_b32_e64 v103, v9, -v9, vcc
	v_cndmask_b32_e64 v102, v7, -v7, vcc
	v_mov_b32_e32 v7, v8
	v_and_b32_e32 v9, 0xffff0000, v85
	v_lshlrev_b32_e32 v8, 16, v85
	v_and_b32_e32 v85, 0xffff0000, v84
	v_lshlrev_b32_e32 v84, 16, v84
	v_pk_add_f32 v[4:5], v[104:105], v[4:5] op_sel_hi:[0,1]
	v_pk_fma_f32 v[4:5], v[84:85], v[84:85], v[4:5]
	v_mul_f32_e32 v104, v85, v85
	v_pk_add_f32 v[4:5], v[104:105], v[4:5] op_sel_hi:[0,1]
	v_pk_fma_f32 v[4:5], v[8:9], v[8:9], v[4:5]
	v_mul_f32_e32 v104, v9, v9
	v_pk_add_f32 v[4:5], v[104:105], v[4:5] op_sel_hi:[0,1]
	v_pk_fma_f32 v[4:5], v[100:101], v[100:101], v[4:5]
	v_mul_f32_e32 v104, v101, v101
	v_pk_add_f32 v[4:5], v[104:105], v[4:5] op_sel_hi:[0,1]
	v_pk_fma_f32 v[4:5], v[96:97], v[96:97], v[4:5]
	v_mul_f32_e32 v104, v97, v97
	v_pk_add_f32 v[4:5], v[104:105], v[4:5] op_sel_hi:[0,1]
	v_pk_fma_f32 v[4:5], v[92:93], v[92:93], v[4:5]
	v_mul_f32_e32 v104, v93, v93
	v_pk_add_f32 v[4:5], v[104:105], v[4:5] op_sel_hi:[0,1]
	v_pk_fma_f32 v[4:5], v[90:91], v[90:91], v[4:5]
	v_mul_f32_e32 v104, v91, v91
	v_pk_add_f32 v[4:5], v[104:105], v[4:5] op_sel_hi:[0,1]
	v_mov_b32_e32 v5, v4
	s_nop 1
	v_permlane16_swap_b32_e32 v4, v5
	v_add_f32_e32 v5, v4, v5
	v_cndmask_b32_e64 v77, v63, -v63, vcc
	v_cndmask_b32_e64 v76, v61, -v61, vcc
	v_mov_b32_e32 v61, v62
	v_cndmask_b32_e64 v63, v13, -v13, vcc
	v_cndmask_b32_e64 v62, v11, -v11, vcc
	v_mov_b32_e32 v11, v12
	v_cndmask_b32_e64 v13, v17, -v17, vcc
	v_cndmask_b32_e64 v12, v15, -v15, vcc
	v_mov_b32_e32 v15, v16
	v_cndmask_b32_e64 v17, v21, -v21, vcc
	v_cndmask_b32_e64 v16, v19, -v19, vcc
	v_mov_b32_e32 v19, v20
	v_cndmask_b32_e64 v21, v25, -v25, vcc
	v_cndmask_b32_e64 v20, v23, -v23, vcc
	v_mov_b32_e32 v23, v24
	v_cndmask_b32_e64 v25, v29, -v29, vcc
	v_cndmask_b32_e64 v24, v27, -v27, vcc
	v_mov_b32_e32 v27, v28
	s_waitcnt vmcnt(6)
; template <int DQK, int DV, bool LEAD> ...
;     ...
; #pragma unroll
;           for (int ds = 0; ds < 2; ++ds)
; #pragma unroll
;               for (int j = 0; j < 8; ++j) sn += x[ds][j] * x[ds][j];
;           sn = lanes4_sum(sn);
;           const float rn = rsqrtf(sn * (1.f / 64.f) + EPS);
; #pragma unroll
;           for (int ds = 0; ds < 2; ++ds)
; #pragma unroll
;               for (int j = 0; j < 8; ++j) x[ds][j] *= rn * qgain[32 * ds + 8 * g4 + j];
;           if constexpr (DQK == 64) {
; #pragma unroll
;               for (int ds = 0; ds < 2; ++ds)
; #pragma unroll
;                   for (int j = 0; j < 8; ++j) {
;                       auto rr = __builtin_amdgcn_permlane32_swap(__float_as_uint(x[ds][j]), __float_as_uint(x[ds][j]), false, false);
;                       const float other = hi ? __uint_as_float(rr[0]) : __uint_as_float(rr[1]);
;                       float cc = 1.f, sg = 0.f;
;                       if (lat) { const f32x2 cs = rope[(ds ? pcol : prow) * 16 + 8 * (g4 & 1) + j]; cc = cs.x; sg = hi ? cs.y : -cs.y; }
;                       x[ds][j] = x[ds][j] * cc + other * sg; }
	v_cndmask_b32_e64 v29, v33, -v33, vcc
	v_cndmask_b32_e64 v28, v31, -v31, vcc
	v_mov_b32_e32 v31, v32
	s_waitcnt vmcnt(5)
	v_cndmask_b32_e64 v33, v37, -v37, vcc
	v_cndmask_b32_e64 v32, v35, -v35, vcc
	v_mov_b32_e32 v35, v36
	v_and_b32_e32 v37, 0xffff0000, v87
	v_lshlrev_b32_e32 v36, 16, v87
	v_mov_b32_e32 v87, v5
	v_and_b32_e32 v105, 0xffff0000, v86
	s_nop 0
	v_permlane32_swap_b32_e32 v5, v87
	v_lshlrev_b32_e32 v104, 16, v86
	v_mul_f32_e32 v4, v105, v105
	v_pk_fma_f32 v[106:107], v[104:105], v[104:105], v[4:5] op_sel_hi:[1,1,0]
	v_mul_f32_e32 v4, v37, v37
	v_pk_fma_f32 v[106:107], v[36:37], v[36:37], v[106:107]
	v_and_b32_e32 v69, 0xffff0000, v71
	v_pk_add_f32 v[106:107], v[4:5], v[106:107] op_sel_hi:[0,1]
	v_pk_fma_f32 v[106:107], v[74:75], v[74:75], v[106:107]
	v_mul_f32_e32 v4, v75, v75
	v_pk_add_f32 v[106:107], v[4:5], v[106:107] op_sel_hi:[0,1]
	v_pk_fma_f32 v[106:107], v[72:73], v[72:73], v[106:107]
	v_mul_f32_e32 v4, v73, v73
	v_lshlrev_b32_e32 v68, 16, v71
	v_and_b32_e32 v71, 0xffff0000, v70
	v_lshlrev_b32_e32 v70, 16, v70
	v_pk_add_f32 v[106:107], v[4:5], v[106:107] op_sel_hi:[0,1]
	v_pk_fma_f32 v[106:107], v[70:71], v[70:71], v[106:107]
	v_mul_f32_e32 v4, v71, v71
	v_pk_add_f32 v[106:107], v[4:5], v[106:107] op_sel_hi:[0,1]
	v_pk_fma_f32 v[106:107], v[68:69], v[68:69], v[106:107]
	v_mul_f32_e32 v4, v69, v69
	v_pk_add_f32 v[106:107], v[4:5], v[106:107] op_sel_hi:[0,1]
	v_pk_fma_f32 v[106:107], v[66:67], v[66:67], v[106:107]
	v_mul_f32_e32 v4, v67, v67
	v_pk_add_f32 v[106:107], v[4:5], v[106:107] op_sel_hi:[0,1]
	v_pk_fma_f32 v[106:107], v[64:65], v[64:65], v[106:107]
	v_mul_f32_e32 v4, v65, v65
	v_pk_add_f32 v[106:107], v[4:5], v[106:107] op_sel_hi:[0,1]
	v_mov_b32_e32 v4, v106
	s_nop 1
	v_permlane16_swap_b32_e32 v106, v4
	v_add_f32_e32 v4, v106, v4
	v_mov_b32_e32 v86, v4
	s_nop 1
	v_permlane32_swap_b32_e32 v4, v86
	v_pk_add_f32 v[4:5], v[4:5], v[86:87]
	s_waitcnt vmcnt(4)
	v_cndmask_b32_e64 v106, v39, -v39, vcc
	v_pk_fma_f32 v[86:87], v[4:5], s[4:5], v[196:197] op_sel_hi:[1,0,0]
	v_mov_b32_e32 v39, v40
	v_mul_f32_e32 v4, 0x4b800000, v87
	v_cmp_gt_f32_e64 s[4:5], s95, v87
	v_cndmask_b32_e64 v107, v41, -v41, vcc
	s_mov_b32 s28, 0
	v_cndmask_b32_e64 v4, v87, v4, s[4:5]
	v_rsq_f32_e32 v4, v4
	s_nop 0
	v_mul_f32_e32 v5, 0x45800000, v4
	v_cndmask_b32_e64 v40, v4, v5, s[4:5]
	s_waitcnt vmcnt(3)
	v_pk_mul_f32 v[4:5], v[40:41], v[44:45] op_sel_hi:[0,1]
	v_pk_mul_f32 v[4:5], v[4:5], v[90:91]
	v_cmp_gt_f32_e64 s[4:5], s95, v86
	v_mov_b32_e32 v41, v4
	v_mov_b32_e32 v87, v4
	v_mov_b32_e32 v90, v5
	v_mov_b32_e32 v91, v5
	v_permlane32_swap_b32_e32 v41, v87
	s_nop 0
	v_permlane32_swap_b32_e32 v90, v91
	v_cndmask_b32_e32 v91, v90, v91, vcc
	v_cndmask_b32_e32 v90, v41, v87, vcc
	v_pk_mul_f32 v[76:77], v[76:77], v[90:91]
	s_nop 0
	v_pk_fma_f32 v[4:5], v[4:5], v[60:61], v[76:77]
	v_pk_mul_f32 v[60:61], v[40:41], v[42:43] op_sel_hi:[0,1]
	v_pk_mul_f32 v[4:5], v[4:5], s[94:95] op_sel_hi:[1,0]
	v_pk_mul_f32 v[60:61], v[60:61], v[92:93]
	v_cvt_pk_bf16_f32 v5, v4, v5
	v_mov_b32_e32 v4, v60
	v_mov_b32_e32 v41, v60
	v_mov_b32_e32 v76, v61
	v_mov_b32_e32 v77, v61
	v_permlane32_swap_b32_e32 v4, v41
	s_nop 0
	v_permlane32_swap_b32_e32 v76, v77
	v_cndmask_b32_e32 v77, v76, v77, vcc
	v_cndmask_b32_e32 v76, v4, v41, vcc
	v_pk_mul_f32 v[76:77], v[94:95], v[76:77]
	s_nop 0
	v_pk_fma_f32 v[54:55], v[60:61], v[54:55], v[76:77]
	s_nop 0
	v_pk_mul_f32 v[54:55], v[54:55], s[94:95] op_sel_hi:[1,0]
	s_nop 0
	v_cvt_pk_bf16_f32 v4, v54, v55
	s_waitcnt vmcnt(2)
	v_pk_mul_f32 v[54:55], v[40:41], v[48:49] op_sel_hi:[0,1]
	v_pk_mul_f32 v[54:55], v[54:55], v[96:97]
	s_nop 0
	v_mov_b32_e32 v41, v54
	v_mov_b32_e32 v60, v54
	v_mov_b32_e32 v61, v55
	v_mov_b32_e32 v76, v55
	v_permlane32_swap_b32_e32 v41, v60
	s_nop 0
	v_permlane32_swap_b32_e32 v61, v76
	v_cndmask_b32_e32 v61, v61, v76, vcc
	v_cndmask_b32_e32 v60, v41, v60, vcc
	v_pk_mul_f32 v[60:61], v[98:99], v[60:61]
	s_nop 0
	v_pk_fma_f32 v[2:3], v[54:55], v[2:3], v[60:61]
	v_pk_mul_f32 v[54:55], v[46:47], v[40:41] op_sel_hi:[1,0]
	v_pk_mul_f32 v[2:3], v[2:3], s[94:95] op_sel_hi:[1,0]
	v_pk_mul_f32 v[54:55], v[54:55], v[100:101]
	v_cvt_pk_bf16_f32 v3, v2, v3
	v_mov_b32_e32 v2, v54
	v_mov_b32_e32 v41, v54
	v_mov_b32_e32 v60, v55
	v_mov_b32_e32 v61, v55
	v_permlane32_swap_b32_e32 v2, v41
	s_nop 0
	v_permlane32_swap_b32_e32 v60, v61
	v_cndmask_b32_e32 v61, v60, v61, vcc
	v_cndmask_b32_e32 v60, v2, v41, vcc
	v_pk_mul_f32 v[60:61], v[102:103], v[60:61]
	s_nop 0
	v_pk_fma_f32 v[6:7], v[54:55], v[6:7], v[60:61]
	s_nop 0
	v_pk_mul_f32 v[6:7], v[6:7], s[94:95] op_sel_hi:[1,0]
	s_nop 0
	v_cvt_pk_bf16_f32 v2, v6, v7
	s_waitcnt vmcnt(1)
	v_pk_mul_f32 v[6:7], v[52:53], v[40:41] op_sel_hi:[1,0]
	s_nop 0
	v_pk_mul_f32 v[6:7], v[6:7], v[8:9]
	s_nop 0
	v_mov_b32_e32 v8, v6
	v_mov_b32_e32 v41, v6
	v_mov_b32_e32 v9, v7
	v_mov_b32_e32 v54, v7
	v_permlane32_swap_b32_e32 v8, v41
	s_nop 0
	v_permlane32_swap_b32_e32 v9, v54
	v_cndmask_b32_e32 v9, v9, v54, vcc
	v_cndmask_b32_e32 v8, v8, v41, vcc
	v_pk_mul_f32 v[8:9], v[24:25], v[8:9]
	s_nop 0
	v_pk_fma_f32 v[6:7], v[6:7], v[26:27], v[8:9]
	s_nop 0
	v_pk_mul_f32 v[6:7], v[6:7], s[94:95] op_sel_hi:[1,0]
	s_nop 0
	v_cvt_pk_bf16_f32 v9, v6, v7
	v_pk_mul_f32 v[6:7], v[50:51], v[40:41] op_sel_hi:[1,0]
	s_nop 0
	v_pk_mul_f32 v[6:7], v[6:7], v[84:85]
	s_nop 0
	v_mov_b32_e32 v8, v6
	v_mov_b32_e32 v41, v6
	v_mov_b32_e32 v54, v7
	v_mov_b32_e32 v55, v7
	v_permlane32_swap_b32_e32 v8, v41
	s_nop 0
	v_permlane32_swap_b32_e32 v54, v55
	v_cndmask_b32_e32 v55, v54, v55, vcc
	v_cndmask_b32_e32 v54, v8, v41, vcc
	v_pk_mul_f32 v[54:55], v[28:29], v[54:55]
	s_nop 0
	v_pk_fma_f32 v[6:7], v[6:7], v[30:31], v[54:55]
	s_nop 0
	v_pk_mul_f32 v[6:7], v[6:7], s[94:95] op_sel_hi:[1,0]
	s_nop 0
	v_cvt_pk_bf16_f32 v8, v6, v7
	s_waitcnt vmcnt(0)
; template <int DQK, int DV, bool LEAD> ...
;     ...
;           const float rn = rsqrtf(sn * (1.f / 64.f) + EPS);
; #pragma unroll
;           for (int ds = 0; ds < 2; ++ds)
; #pragma unroll
;               for (int j = 0; j < 8; ++j) x[ds][j] *= rn * qgain[32 * ds + 8 * g4 + j];
;           if constexpr (DQK == 64) {
; #pragma unroll
;               for (int ds = 0; ds < 2; ++ds)
; #pragma unroll
;                   for (int j = 0; j < 8; ++j) {
;                       auto rr = __builtin_amdgcn_permlane32_swap(__float_as_uint(x[ds][j]), __float_as_uint(x[ds][j]), false, false);
;                       const float other = hi ? __uint_as_float(rr[0]) : __uint_as_float(rr[1]);
;                       float cc = 1.f, sg = 0.f;
;                       if (lat) { const f32x2 cs = rope[(ds ? pcol : prow) * 16 + 8 * (g4 & 1) + j]; cc = cs.x; sg = hi ? cs.y : -cs.y; }
;                       x[ds][j] = x[ds][j] * cc + other * sg; }
;           } else {
;               float sr = 0.f;
; #pragma unroll
;               for (int j = 0; j < 8; ++j) sr += x[2][j] * x[2][j];
;               sr = lanes4_sum(sr);
;               const float rq = rsqrtf(sr * (1.f / 32.f) + EPS);
; #pragma unroll
;               for (int j = 0; j < 8; ++j) { const float av = x[2][j] * rq * qgain[64 + 8 * g4 + j];
;                   auto rr = __builtin_amdgcn_permlane16_swap(__float_as_uint(av), __float_as_uint(av), false, false);
;                   const float other = (g4 & 1) ? __uint_as_float(rr[0]) : __uint_as_float(rr[1]);
;                   float cc = 1.f, sg = 0.f;
;                   if (lat) { const f32x2 cs = rope[((g4 & 2) ? pcol : prow) * 8 + j]; cc = cs.x; sg = (g4 & 1) ? cs.y : -cs.y; }
;                   x[2][j] = av * cc + other * sg; }
;           }
; #pragma unroll
;           for (int ds = 0; ds < NDS; ++ds) { u32x4 w;
; #pragma unroll
;               for (int i = 0; i < 4; ++i) w[i] = cvtpk(x[ds][2 * i] * c2, x[ds][2 * i + 1] * c2);
;               qf[qb * NDS + ds] = __builtin_bit_cast(bf16x8, w); }
;       }
; #pragma unroll
;       for (int d0 = 0; d0 < NQB * NDS; ++d0) asm volatile("" : "+v"(qf[d0])); }
;     wait_bar<0>();
;     bf16x8 kf[NKW * NDS], vf[NVF];
;     ATT_KLOAD(0);
;     asm volatile("s_waitcnt lgkmcnt(0)\n\ts_barrier" ::: "memory");
	v_pk_mul_f32 v[6:7], v[58:59], v[40:41] op_sel_hi:[1,0]
	s_nop 0
	v_pk_mul_f32 v[6:7], v[6:7], v[88:89]
	s_nop 0
	v_mov_b32_e32 v41, v6
	v_mov_b32_e32 v54, v6
	v_mov_b32_e32 v55, v7
	v_mov_b32_e32 v60, v7
	v_permlane32_swap_b32_e32 v41, v54
	s_nop 0
	v_permlane32_swap_b32_e32 v55, v60
	v_cndmask_b32_e32 v55, v55, v60, vcc
	v_cndmask_b32_e32 v54, v41, v54, vcc
	v_pk_mul_f32 v[54:55], v[32:33], v[54:55]
	v_pk_mul_f32 v[40:41], v[56:57], v[40:41] op_sel_hi:[1,0]
	v_pk_fma_f32 v[6:7], v[6:7], v[34:35], v[54:55]
	v_pk_mul_f32 v[40:41], v[40:41], v[82:83]
	v_pk_mul_f32 v[6:7], v[6:7], s[94:95] op_sel_hi:[1,0]
	v_mov_b32_e32 v54, v40
	v_cvt_pk_bf16_f32 v7, v6, v7
	v_mov_b32_e32 v6, v40
	s_nop 1
	v_permlane32_swap_b32_e32 v6, v54
	v_mov_b32_e32 v55, v41
	v_mov_b32_e32 v60, v41
	v_cndmask_b32_e32 v54, v6, v54, vcc
	v_mul_f32_e32 v6, 0x4b800000, v86
	v_permlane32_swap_b32_e32 v55, v60
	v_cndmask_b32_e64 v6, v86, v6, s[4:5]
	v_cndmask_b32_e32 v55, v55, v60, vcc
	v_rsq_f32_e32 v60, v6
	v_pk_mul_f32 v[54:55], v[106:107], v[54:55]
	s_nop 0
	v_pk_fma_f32 v[40:41], v[40:41], v[38:39], v[54:55]
	s_nop 0
	v_pk_mul_f32 v[40:41], v[40:41], s[94:95] op_sel_hi:[1,0]
	s_nop 0
	v_cvt_pk_bf16_f32 v6, v40, v41
	v_mul_f32_e32 v40, 0x45800000, v60
	v_cndmask_b32_e64 v40, v60, v40, s[4:5]
	v_pk_mul_f32 v[54:55], v[56:57], v[40:41] op_sel_hi:[1,0]
	v_pk_mul_f32 v[56:57], v[58:59], v[40:41] op_sel_hi:[1,0]
	v_pk_mul_f32 v[54:55], v[54:55], v[104:105]
	v_pk_mul_f32 v[36:37], v[56:57], v[36:37]
	v_pk_mul_f32 v[50:51], v[50:51], v[40:41] op_sel_hi:[1,0]
	v_pk_mul_f32 v[52:53], v[52:53], v[40:41] op_sel_hi:[1,0]
	v_pk_mul_f32 v[46:47], v[46:47], v[40:41] op_sel_hi:[1,0]
	v_pk_mul_f32 v[48:49], v[48:49], v[40:41] op_sel_hi:[1,0]
	v_pk_mul_f32 v[42:43], v[42:43], v[40:41] op_sel_hi:[1,0]
	v_pk_mul_f32 v[40:41], v[44:45], v[40:41] op_sel_hi:[1,0]
	v_mov_b32_e32 v44, v54
	v_mov_b32_e32 v56, v54
	v_mov_b32_e32 v45, v55
	v_mov_b32_e32 v57, v55
	v_permlane32_swap_b32_e32 v44, v56
	s_nop 0
	v_permlane32_swap_b32_e32 v45, v57
	v_cndmask_b32_e32 v45, v45, v57, vcc
	v_cndmask_b32_e32 v44, v44, v56, vcc
	v_pk_mul_f32 v[38:39], v[38:39], v[54:55]
	v_mov_b32_e32 v54, v36
	v_pk_fma_f32 v[38:39], v[106:107], v[44:45], v[38:39]
	v_mov_b32_e32 v44, v36
	v_mov_b32_e32 v45, v37
	v_mov_b32_e32 v55, v37
	v_permlane32_swap_b32_e32 v44, v54
	s_nop 0
	v_permlane32_swap_b32_e32 v45, v55
	v_pk_mul_f32 v[50:51], v[50:51], v[74:75]
	v_cndmask_b32_e32 v45, v45, v55, vcc
	v_cndmask_b32_e32 v44, v44, v54, vcc
	v_pk_mul_f32 v[34:35], v[34:35], v[36:37]
	v_mov_b32_e32 v36, v50
	v_pk_fma_f32 v[32:33], v[32:33], v[44:45], v[34:35]
	v_mov_b32_e32 v34, v50
	v_mov_b32_e32 v35, v51
	v_mov_b32_e32 v37, v51
	v_permlane32_swap_b32_e32 v34, v36
	s_nop 0
	v_permlane32_swap_b32_e32 v35, v37
	v_cndmask_b32_e32 v35, v35, v37, vcc
	v_cndmask_b32_e32 v34, v34, v36, vcc
	v_pk_mul_f32 v[52:53], v[52:53], v[72:73]
	v_pk_mul_f32 v[28:29], v[28:29], v[34:35]
	v_mov_b32_e32 v34, v52
	v_pk_fma_f32 v[28:29], v[30:31], v[50:51], v[28:29]
	v_mov_b32_e32 v30, v52
	v_mov_b32_e32 v31, v53
	v_mov_b32_e32 v35, v53
	v_permlane32_swap_b32_e32 v30, v34
	s_nop 0
	v_permlane32_swap_b32_e32 v31, v35
	v_cndmask_b32_e32 v31, v31, v35, vcc
	v_cndmask_b32_e32 v30, v30, v34, vcc
	v_pk_mul_f32 v[46:47], v[46:47], v[70:71]
	v_pk_mul_f32 v[24:25], v[24:25], v[30:31]
	v_mov_b32_e32 v30, v46
	v_pk_fma_f32 v[24:25], v[52:53], v[26:27], v[24:25]
	v_mov_b32_e32 v26, v46
	v_mov_b32_e32 v27, v47
	v_mov_b32_e32 v31, v47
	v_permlane32_swap_b32_e32 v26, v30
	s_nop 0
	v_permlane32_swap_b32_e32 v27, v31
	v_cndmask_b32_e32 v27, v27, v31, vcc
	v_cndmask_b32_e32 v26, v26, v30, vcc
	v_pk_mul_f32 v[48:49], v[48:49], v[68:69]
	v_pk_mul_f32 v[20:21], v[20:21], v[26:27]
	v_mov_b32_e32 v26, v48
	v_pk_fma_f32 v[20:21], v[46:47], v[22:23], v[20:21]
	v_mov_b32_e32 v22, v48
	v_mov_b32_e32 v23, v49
	v_mov_b32_e32 v27, v49
	v_permlane32_swap_b32_e32 v22, v26
	s_nop 0
	v_permlane32_swap_b32_e32 v23, v27
	v_cndmask_b32_e32 v23, v23, v27, vcc
	v_cndmask_b32_e32 v22, v22, v26, vcc
	v_pk_mul_f32 v[42:43], v[42:43], v[66:67]
	v_pk_mul_f32 v[16:17], v[16:17], v[22:23]
	v_mov_b32_e32 v22, v42
	v_pk_fma_f32 v[16:17], v[48:49], v[18:19], v[16:17]
	v_mov_b32_e32 v18, v42
	v_mov_b32_e32 v19, v43
	v_mov_b32_e32 v23, v43
	v_permlane32_swap_b32_e32 v18, v22
	s_nop 0
	v_permlane32_swap_b32_e32 v19, v23
	v_cndmask_b32_e32 v19, v19, v23, vcc
	v_cndmask_b32_e32 v18, v18, v22, vcc
	v_pk_mul_f32 v[40:41], v[40:41], v[64:65]
	v_pk_mul_f32 v[12:13], v[12:13], v[18:19]
	v_pk_mul_f32 v[16:17], v[16:17], s[94:95] op_sel_hi:[1,0]
	v_pk_fma_f32 v[18:19], v[42:43], v[14:15], v[12:13]
	v_mov_b32_e32 v12, v40
	v_mov_b32_e32 v14, v40
	v_mov_b32_e32 v13, v41
	v_mov_b32_e32 v15, v41
	v_permlane32_swap_b32_e32 v12, v14
	s_nop 0
	v_permlane32_swap_b32_e32 v13, v15
	v_cndmask_b32_e32 v13, v13, v15, vcc
	v_cndmask_b32_e32 v12, v12, v14, vcc
	v_pk_mul_f32 v[12:13], v[62:63], v[12:13]
	v_pk_mul_f32 v[14:15], v[24:25], s[94:95] op_sel_hi:[1,0]
	v_pk_fma_f32 v[22:23], v[40:41], v[10:11], v[12:13]
	v_pk_mul_f32 v[10:11], v[38:39], s[94:95] op_sel_hi:[1,0]
	v_pk_mul_f32 v[12:13], v[32:33], s[94:95] op_sel_hi:[1,0]
	v_cvt_pk_bf16_f32 v10, v10, v11
	v_cvt_pk_bf16_f32 v11, v12, v13
	v_pk_mul_f32 v[12:13], v[28:29], s[94:95] op_sel_hi:[1,0]
	v_bfe_u32 v30, v79, 1, 3
	v_cvt_pk_bf16_f32 v12, v12, v13
	v_cvt_pk_bf16_f32 v13, v14, v15
	v_pk_mul_f32 v[14:15], v[20:21], s[94:95] op_sel_hi:[1,0]
	v_bitop3_b32 v30, v171, v30, 4 bitop3:0x36
	v_cvt_pk_bf16_f32 v14, v14, v15
	v_cvt_pk_bf16_f32 v15, v16, v17
	v_pk_mul_f32 v[16:17], v[18:19], s[94:95] op_sel_hi:[1,0]
	v_pk_mul_f32 v[18:19], v[22:23], s[94:95] op_sel_hi:[1,0]
	v_cvt_pk_bf16_f32 v16, v16, v17
	v_cvt_pk_bf16_f32 v17, v18, v19
	s_waitcnt vmcnt(0) lgkmcnt(0)
	s_barrier
; #define ATT_SB() __builtin_amdgcn_sched_barrier(0)
; #define ATT_DMA_K(t, sl) do { glds16(ksrc + (size_t)(t) * 64 * kpitch, (unsigned)__builtin_amdgcn_readfirstlane(kdst + (sl) * KSLOT)); \
;         if constexpr (DQK == 96) glds16(krsrc + (size_t)(t) * 64 * 32, (unsigned)__builtin_amdgcn_readfirstlane(krdst + (sl) * KSLOT)); } while (0)
; #define ATT_DMA_V(t, sl) do { glds16(vsrc + (size_t)(t) * 64, (unsigned)__builtin_amdgcn_readfirstlane(vdst + (sl) * VSLOT)); \
;         if constexpr (DV == 128) glds16(vsrc + (size_t)64 * NR + (size_t)(t) * 64, (unsigned)__builtin_amdgcn_readfirstlane(vdst + (sl) * VSLOT + 8192)); } while (0)
; #define ATT_KLOAD(sl) do { _Pragma("unroll") for (int kb_ = 0; kb_ < NKW; ++kb_) _Pragma("unroll") for (int ds_ = 0; ds_ < NDS; ++ds_) { \
;         if (ds_ < 2) kf[kb_ * NDS + ds_] = *(const LAS bf16x8*)(kp[ds_ & 1] + (sl) * KSLOT + (kb_ & 1) * 512 + (kb_ >> 1) * 4096); \
;         else kf[kb_ * NDS + ds_] = *(const LAS bf16x8*)(krp + (sl) * KSLOT + (kb_ & 1) * 256 + (kb_ >> 1) * 2048); } } while (0)
; #define ATT_QK() do { _Pragma("unroll") for (int kb_ = 0; kb_ < NKW; ++kb_) _Pragma("unroll") for (int ds_ = 0; ds_ < NDS; ++ds_) _Pragma("unroll") for (int qb_ = 0; qb_ < NQB; ++qb_) \
;         c[kb_][qb_] = __builtin_amdgcn_mfma_f32_16x16x32_bf16(kf[kb_ * NDS + ds_], qf[qb_ * NDS + ds_], ds_ == 0 ? zero4 : c[kb_][qb_], 0, 0, 0); } while (0)
; #define ATT_EXP() do { _Pragma("unroll") for (int kb_ = 0; kb_ < NKW; ++kb_) _Pragma("unroll") for (int qb_ = 0; qb_ < NQB; ++qb_) _Pragma("unroll") for (int i_ = 0; i_ < 4; ++i_) \
;         c[kb_][qb_][i_] = __builtin_amdgcn_exp2f(c[kb_][qb_][i_]); } while (0)
; template <int DQK, int DV, bool LEAD> ...
;     ...
;     ATT_KLOAD(0);
;     asm volatile("s_waitcnt lgkmcnt(0)\n\ts_barrier" ::: "memory");
;     float lsum[NQB];
; #pragma unroll
;     for (int qb = 0; qb < NQB; ++qb) lsum[qb] = 0.f;
;     const f32x4 zero4 = {0.f, 0.f, 0.f, 0.f};
;     f32x4 o[NDB][NQB], c[NKW][NQB]; u32x4 pw[4];
; #pragma unroll
;     for (int i = 0; i < NDB; ++i)
; #pragma unroll
;         for (int qb = 0; qb < NQB; ++qb) o[i][qb] = zero4;
;     ATT_DMA_K(3, 0); ATT_DMA_V(1, 1);
;     ATT_QK(); ATT_SB();
;     ATT_KLOAD(1); ATT_SB();
;     if constexpr (LEAD) { ATT_EXP(); ATT_SUMPACK(); }
;     wait_bar<NDMA>();
;     int s_prev = 0, s_cur = 1, s_next = 2;
;     int one_ = 1; asm volatile("" : "+s"(one_));
	ds_read_b128 v[18:21], v173
	ds_read_b128 v[22:25], v173 offset:512
	v_lshlrev_b32_e32 v54, 4, v30
	v_add_u32_e32 v176, v81, v54
	s_waitcnt lgkmcnt(1)
	v_mfma_f32_16x16x32_bf16 v[26:29], v[18:21], v[6:9], 0
	ds_read_b128 v[30:33], v176
	ds_read_b128 v[34:37], v176 offset:512
	v_add_u32_e32 v55, 0, v175
	v_add_u32_e32 v178, v55, v80
	v_mfma_f32_16x16x32_bf16 v[18:21], v[18:21], v[10:13], 0
	v_add_u32_e32 v177, v55, v54
	s_waitcnt lgkmcnt(1)
	v_mfma_f32_16x16x32_bf16 v[26:29], v[30:33], v[2:5], v[26:29]
	v_mfma_f32_16x16x32_bf16 v[18:21], v[30:33], v[14:17], v[18:21]
	v_mfma_f32_16x16x32_bf16 v[30:33], v[22:25], v[6:9], 0
	v_mfma_f32_16x16x32_bf16 v[22:25], v[22:25], v[10:13], 0
	s_waitcnt lgkmcnt(0)
	v_mfma_f32_16x16x32_bf16 v[30:33], v[34:37], v[2:5], v[30:33]
	v_mfma_f32_16x16x32_bf16 v[22:25], v[34:37], v[14:17], v[22:25]
	ds_read_b128 v[34:37], v173 offset:4096
	ds_read_b128 v[38:41], v173 offset:4608
	ds_read_b128 v[46:49], v176 offset:4096
	ds_read_b128 v[50:53], v176 offset:4608
	s_waitcnt lgkmcnt(3)
	v_mfma_f32_16x16x32_bf16 v[42:45], v[34:37], v[6:9], 0
	s_waitcnt lgkmcnt(0)
	s_barrier
	v_mfma_f32_16x16x32_bf16 v[34:37], v[34:37], v[10:13], 0
	s_waitcnt lgkmcnt(1)
	v_mfma_f32_16x16x32_bf16 v[58:61], v[46:49], v[14:17], v[34:37]
	v_mfma_f32_16x16x32_bf16 v[34:37], v[38:41], v[6:9], 0
	v_mfma_f32_16x16x32_bf16 v[38:41], v[38:41], v[10:13], 0
	v_mfma_f32_16x16x32_bf16 v[42:45], v[46:49], v[2:5], v[42:45]
	v_lshl_add_u64 v[46:47], v[162:163], 0, s[96:97]
	s_mov_b32 s4, m0
	s_mov_b32 m0, s31
	s_nop 0
	global_load_lds_dwordx4 v[46:47], off
	s_mov_b32 m0, s4
	v_lshl_add_u64 v[46:47], v[164:165], 0, s[66:67]
	s_add_i32 s4, s40, 0x4000
	s_mov_b32 s5, m0
	s_mov_b32 m0, s4
	s_nop 0
	global_load_lds_dwordx4 v[46:47], off
	s_mov_b32 m0, s5
	s_mov_b64 s[4:5], 0x840080
	s_waitcnt lgkmcnt(0)
	v_mfma_f32_16x16x32_bf16 v[74:77], v[50:53], v[2:5], v[34:37]
	v_lshl_add_u64 v[46:47], v[164:165], 0, s[4:5]
	s_add_i32 s4, s40, 0x6000
	s_mov_b32 s5, m0
	s_mov_b32 m0, s4
	s_nop 0
	global_load_lds_dwordx4 v[46:47], off
	s_mov_b32 m0, s5
	v_mfma_f32_16x16x32_bf16 v[78:81], v[50:53], v[14:17], v[38:41]
	ds_read_b128 v[34:37], v173 offset:8192
	s_nop 1
	ds_read_b128 v[38:41], v173 offset:8704
	ds_read_b128 v[46:49], v176 offset:8192
	ds_read_b128 v[50:53], v176 offset:8704
	ds_read_b128 v[54:57], v173 offset:12288
	ds_read_b128 v[62:65], v173 offset:12800
	ds_read_b128 v[66:69], v176 offset:12288
	ds_read_b128 v[70:73], v176 offset:12800
	v_exp_f32_e32 v26, v26
	v_exp_f32_e32 v27, v27
	v_exp_f32_e32 v28, v28
	v_exp_f32_e32 v29, v29
	v_exp_f32_e32 v86, v18
	v_exp_f32_e32 v87, v19
	v_exp_f32_e32 v20, v20
	v_exp_f32_e32 v21, v21
	v_exp_f32_e32 v30, v30
	v_exp_f32_e32 v22, v22
	v_add_f32_e32 v18, v26, v27
	v_add_f32_e32 v19, v28, v29
	v_exp_f32_e32 v31, v31
	v_exp_f32_e32 v23, v23
	v_add_f32_e32 v18, v18, v19
	v_add_f32_e32 v19, v86, v87
	v_add_f32_e32 v82, v20, v21
	v_add_f32_e32 v19, v19, v82
	v_exp_f32_e32 v32, v32
	v_exp_f32_e32 v24, v24
	v_add_f32_e32 v18, v18, v30
	v_add_f32_e32 v19, v19, v22
	v_exp_f32_e32 v33, v33
	v_exp_f32_e32 v25, v25
	v_add_f32_e32 v18, v31, v18
	v_add_f32_e32 v19, v23, v19
	v_exp_f32_e32 v42, v42
	v_exp_f32_e32 v58, v58
	v_add_f32_e32 v18, v32, v18
	v_add_f32_e32 v19, v24, v19
	v_exp_f32_e32 v43, v43
	v_exp_f32_e32 v59, v59
	v_add_f32_e32 v18, v33, v18
	v_add_f32_e32 v19, v25, v19
	v_exp_f32_e32 v44, v44
	v_exp_f32_e32 v60, v60
	v_add_f32_e32 v18, v42, v18
	v_add_f32_e32 v19, v58, v19
	v_exp_f32_e32 v45, v45
	v_exp_f32_e32 v61, v61
	v_add_f32_e32 v18, v43, v18
	v_add_f32_e32 v19, v59, v19
	v_exp_f32_e32 v74, v74
	v_exp_f32_e32 v78, v78
	v_add_f32_e32 v18, v44, v18
	v_add_f32_e32 v19, v60, v19
	v_exp_f32_e32 v75, v75
	v_exp_f32_e32 v79, v79
	v_add_f32_e32 v18, v45, v18
	v_add_f32_e32 v19, v61, v19
	v_exp_f32_e32 v76, v76
	v_exp_f32_e32 v80, v80
	v_add_f32_e32 v18, v74, v18
	v_add_f32_e32 v19, v78, v19
	v_exp_f32_e32 v77, v77
	v_exp_f32_e32 v81, v81
	v_add_f32_e32 v18, v75, v18
	v_add_f32_e32 v19, v79, v19
	s_mov_b32 s4, 1
	v_add_f32_e32 v18, v76, v18
	v_add_f32_e32 v82, v80, v19
	v_cvt_pk_bf16_f32 v83, v28, v29
	v_add_f32_e32 v19, v77, v18
	v_add_f32_e32 v18, v81, v82
	s_waitcnt vmcnt(3) lgkmcnt(0)
	s_barrier
	s_cmp_lg_u32 s4, 0
	v_pk_add_f32 v[168:169], v[18:19], 0 op_sel_hi:[1,0]
	v_mov_b32_e32 v18, 0
	v_cvt_pk_bf16_f32 v82, v26, v27
	v_cvt_pk_bf16_f32 v84, v30, v31
	v_cvt_pk_bf16_f32 v85, v32, v33
	v_cvt_pk_bf16_f32 v94, v86, v87
	v_cvt_pk_bf16_f32 v95, v20, v21
	v_cvt_pk_bf16_f32 v96, v22, v23
	v_cvt_pk_bf16_f32 v97, v24, v25
	v_cvt_pk_bf16_f32 v98, v42, v43
	v_cvt_pk_bf16_f32 v99, v44, v45
	v_cvt_pk_bf16_f32 v100, v74, v75
	v_cvt_pk_bf16_f32 v101, v76, v77
	v_cvt_pk_bf16_f32 v102, v58, v59
	v_cvt_pk_bf16_f32 v103, v60, v61
	v_cvt_pk_bf16_f32 v104, v78, v79
	v_cvt_pk_bf16_f32 v105, v80, v81
	s_cselect_b64 s[4:5], -1, 0
	s_mov_b32 s30, 2
	v_mov_b32_e32 v19, v18
	v_mov_b32_e32 v20, v18
	v_mov_b32_e32 v21, v18
	v_mov_b32_e32 v22, v18
	v_mov_b32_e32 v23, v18
	v_mov_b32_e32 v24, v18
	v_mov_b32_e32 v25, v18
	v_mov_b32_e32 v26, v18
	v_mov_b32_e32 v27, v18
	v_mov_b32_e32 v28, v18
	v_mov_b32_e32 v29, v18
	v_mov_b32_e32 v30, v18
	v_mov_b32_e32 v31, v18
	v_mov_b32_e32 v32, v18
	v_mov_b32_e32 v33, v18
	v_mov_b32_e32 v42, v18
	v_mov_b32_e32 v43, v18
	v_mov_b32_e32 v44, v18
	v_mov_b32_e32 v45, v18
	v_mov_b32_e32 v58, v18
	v_mov_b32_e32 v59, v18
	v_mov_b32_e32 v60, v18
	v_mov_b32_e32 v61, v18
	v_mov_b32_e32 v74, v18
	v_mov_b32_e32 v75, v18
	v_mov_b32_e32 v76, v18
	v_mov_b32_e32 v77, v18
	v_mov_b32_e32 v78, v18
	v_mov_b32_e32 v79, v18
	v_mov_b32_e32 v80, v18
	v_mov_b32_e32 v81, v18
	v_mov_b32_e32 v86, v18
	v_mov_b32_e32 v87, v18
	v_mov_b32_e32 v88, v18
	v_mov_b32_e32 v89, v18
	v_mov_b32_e32 v90, v18
	v_mov_b32_e32 v91, v18
	v_mov_b32_e32 v92, v18
	v_mov_b32_e32 v93, v18
	v_mov_b32_e32 v106, v18
	v_mov_b32_e32 v107, v18
	v_mov_b32_e32 v108, v18
	v_mov_b32_e32 v109, v18
	v_mov_b32_e32 v110, v18
	v_mov_b32_e32 v111, v18
	v_mov_b32_e32 v112, v18
	v_mov_b32_e32 v113, v18
	v_mov_b32_e32 v114, v18
	v_mov_b32_e32 v115, v18
	v_mov_b32_e32 v116, v18
	v_mov_b32_e32 v117, v18
	v_mov_b32_e32 v118, v18
	v_mov_b32_e32 v119, v18
	v_mov_b32_e32 v120, v18
	v_mov_b32_e32 v121, v18
	v_mov_b32_e32 v122, v18
	v_mov_b32_e32 v123, v18
	v_mov_b32_e32 v124, v18
	v_mov_b32_e32 v125, v18
	v_mov_b32_e32 v126, v18
	v_mov_b32_e32 v127, v18
	v_mov_b32_e32 v128, v18
	v_mov_b32_e32 v129, v18
	s_branch .LBB0_948

; #define ATT_SB() __builtin_amdgcn_sched_barrier(0)
; #define ATT_KLOAD(sl) do { _Pragma("unroll") for (int kb_ = 0; kb_ < NKW; ++kb_) _Pragma("unroll") for (int ds_ = 0; ds_ < NDS; ++ds_) { \
;         if (ds_ < 2) kf[kb_ * NDS + ds_] = *(const LAS bf16x8*)(kp[ds_ & 1] + (sl) * KSLOT + (kb_ & 1) * 512 + (kb_ >> 1) * 4096); \
;         else kf[kb_ * NDS + ds_] = *(const LAS bf16x8*)(krp + (sl) * KSLOT + (kb_ & 1) * 256 + (kb_ >> 1) * 2048); } } while (0)
; #define ATT_QK() do { _Pragma("unroll") for (int kb_ = 0; kb_ < NKW; ++kb_) _Pragma("unroll") for (int ds_ = 0; ds_ < NDS; ++ds_) _Pragma("unroll") for (int qb_ = 0; qb_ < NQB; ++qb_) \
;         c[kb_][qb_] = __builtin_amdgcn_mfma_f32_16x16x32_bf16(kf[kb_ * NDS + ds_], qf[qb_ * NDS + ds_], ds_ == 0 ? zero4 : c[kb_][qb_], 0, 0, 0); } while (0)
; template <int DQK, int DV, bool LEAD> ...
;     ...
;         if constexpr (LEAD) {
;             ATT_QK(); ATT_SB();
;             ATT_PVP(0); ATT_SB();
;             if constexpr (DV == 128) { ATT_VLOAD(s_prev, 1); ATT_SB(); ATT_EXP(); ATT_SB(); ATT_PVP(1); ATT_SB(); }
;             if (one_) ATT_KLOAD(s_next);
;             ATT_SB();
;             if constexpr (DV == 64) ATT_EXP();
;             ATT_SUMPACK();
;             asm volatile("" : "+v"(pw[0]), "+v"(pw[1]), "+v"(pw[2]), "+v"(pw[3]));
; #pragma unroll
;             for (int qb = 0; qb < NQB; ++qb) asm volatile("" : "+v"(lsum[qb]));
;         } else {
;             if constexpr (DV == 128) {
;                 ATT_PVP(0); ATT_SB();
;                 ATT_VLOAD(s_prev, 1); ATT_SB();
;                 ATT_QK(); ATT_SB();
;                 if (one_) { ATT_KLOAD(s_next); ATT_SB(); ATT_PVP(1); }
;                 ATT_SB();
;             } else {
;                 __builtin_amdgcn_s_setprio(1);
;                 ATT_QK(); ATT_SB();
;                 if (one_) { ATT_KLOAD(s_next); ATT_SB(); ATT_PVP(0); }
;                 ATT_SB();
;                 __builtin_amdgcn_s_setprio(0);
;             }
; #pragma unroll
;             for (int kb = 0; kb < NKW; ++kb)
; #pragma unroll
;                 for (int qb = 0; qb < NQB; ++qb) asm volatile("" : "+v"(c[kb][qb]));
;         }
;         ATT_SB();
;         wait_bar<NDMA>();
;         const int tmp = s_prev; s_prev = s_cur; s_cur = s_next; s_next = tmp;
.LBB0_950:
	v_exp_f32_e32 v82, v158
	v_exp_f32_e32 v83, v159
	v_exp_f32_e32 v84, v160
	v_exp_f32_e32 v85, v161
	v_exp_f32_e32 v94, v154
	v_exp_f32_e32 v95, v155
	v_exp_f32_e32 v96, v156
	v_exp_f32_e32 v97, v157
	v_exp_f32_e32 v98, v150
	v_exp_f32_e32 v99, v151
	v_exp_f32_e32 v100, v152
	v_exp_f32_e32 v101, v153
	v_exp_f32_e32 v102, v146
	v_exp_f32_e32 v103, v147
	v_exp_f32_e32 v104, v148
	v_exp_f32_e32 v105, v149
	v_exp_f32_e32 v142, v142
	v_exp_f32_e32 v143, v143
	v_exp_f32_e32 v144, v144
	v_exp_f32_e32 v145, v145
	v_exp_f32_e32 v138, v138
	v_exp_f32_e32 v139, v139
	v_exp_f32_e32 v140, v140
	v_exp_f32_e32 v141, v141
	v_exp_f32_e32 v134, v134
	v_exp_f32_e32 v135, v135
	v_exp_f32_e32 v136, v136
	v_exp_f32_e32 v137, v137
	v_exp_f32_e32 v130, v130
	v_exp_f32_e32 v131, v131
	v_exp_f32_e32 v132, v132
	v_exp_f32_e32 v133, v133
	v_add_f32_e32 v146, v82, v83
	v_add_f32_e32 v147, v84, v85
	v_add_f32_e32 v146, v146, v147
	v_add_f32_e32 v147, v94, v95
	v_add_f32_e32 v148, v96, v97
	v_add_f32_e32 v147, v147, v148
	v_add_f32_e32 v146, v146, v98
	v_add_f32_e32 v147, v147, v102
	v_cvt_pk_bf16_f32 v82, v82, v83
	v_add_f32_e32 v146, v99, v146
	v_add_f32_e32 v147, v103, v147
	v_cvt_pk_bf16_f32 v83, v84, v85
	v_add_f32_e32 v146, v100, v146
	v_add_f32_e32 v147, v104, v147
	v_cvt_pk_bf16_f32 v84, v98, v99
	v_add_f32_e32 v146, v101, v146
	v_add_f32_e32 v147, v105, v147
	v_cvt_pk_bf16_f32 v85, v100, v101
	v_add_f32_e32 v146, v142, v146
	v_add_f32_e32 v147, v138, v147
	v_cvt_pk_bf16_f32 v94, v94, v95
	v_add_f32_e32 v146, v143, v146
	v_add_f32_e32 v147, v139, v147
	v_cvt_pk_bf16_f32 v95, v96, v97
	v_add_f32_e32 v146, v144, v146
	v_add_f32_e32 v147, v140, v147
	v_cvt_pk_bf16_f32 v96, v102, v103
	v_add_f32_e32 v146, v145, v146
	v_add_f32_e32 v147, v141, v147
	v_cvt_pk_bf16_f32 v97, v104, v105
	v_add_f32_e32 v146, v134, v146
	v_add_f32_e32 v147, v130, v147
	v_cvt_pk_bf16_f32 v98, v142, v143
	v_add_f32_e32 v146, v135, v146
	v_add_f32_e32 v147, v131, v147
	v_cvt_pk_bf16_f32 v99, v144, v145
	v_add_f32_e32 v146, v136, v146
	v_add_f32_e32 v147, v132, v147
	v_cvt_pk_bf16_f32 v100, v134, v135
	v_add_f32_e32 v146, v137, v146
	v_add_f32_e32 v147, v133, v147
	v_cvt_pk_bf16_f32 v101, v136, v137
	v_add_f32_e32 v169, v169, v146
	v_add_f32_e32 v168, v168, v147
	v_cvt_pk_bf16_f32 v102, v138, v139
	v_cvt_pk_bf16_f32 v103, v140, v141
	v_cvt_pk_bf16_f32 v104, v130, v131
	v_cvt_pk_bf16_f32 v105, v132, v133
	s_waitcnt vmcnt(3) lgkmcnt(0)
	s_add_i32 s16, s16, 1
	s_cmpk_lg_i32 s16, 0x85
	s_cbranch_scc0 .Lx_rot3_exit
	s_mov_b32 s30, s28
	s_mov_b32 s28, s29
	s_branch .Lx_rot3_head

; template <int DQK, int DV, bool LEAD> ...
;     ...
;     int tid_ = threadIdx.x; asm volatile("" : "+v"(tid_));
;     const int tid = tid_, lane = tid & 63, q16 = lane & 15, g4 = lane >> 4, hi = lane >> 5; const int wid = __builtin_amdgcn_readfirstlane(tid >> 6);
;     const int kg = KS ? (wid >> 2) : 0, qoff = KS ? (wid & 3) * 64 : wid * 32;
;     const unsigned lds0 = (unsigned)(uintptr_t)shm;
;     const int krow_l = wid * 8 + (lane >> 3);
;     const int kc_l = (lane & 7) ^ (((krow_l >> 1) & 1) | (((krow_l >> 3) & 1) << 1) | (((krow_l >> 4) & 1) << 2));
;     const int vc_l = (lane & 7) ^ ((krow_l >> 1) & 7);
;     const bf16_t* ksrc = K + (size_t)(krow0 + krow_l) * kpitch + kc_l * 8;
;     const int rrow_l = (wid & 3) * 16 + (lane >> 2), rc_l = (lane & 3) ^ (((rrow_l >> 4) & 1) << 1);
;     const bf16_t* krsrc = (DQK == 96) ? KR + (size_t)(krow0 + rrow_l) * 32 + rc_l * 8 : nullptr;
;     const bf16_t* vsrc = Vt + (size_t)krow_l * NR + krow0 + vc_l * 8;
;     const unsigned kdst = lds0 + KOFF + wid * 1024, krdst = lds0 + KOFF + 8192 + (wid & 3) * 1024, vdst = lds0 + VOFF + wid * 1024;
;     ...
;     const int kr0 = 8 * (q16 >> 2) + (q16 & 3);
;     const int fk = ((kr0 >> 1) & 1) | (((kr0 >> 3) & 1) << 1) | (((kr0 >> 4) & 1) << 2);
;     const LAS unsigned char* kp[2]; const LAS unsigned char* vp[2];
; #pragma unroll
;     for (int ds = 0; ds < 2; ++ds) kp[ds] = shm + KOFF + kr0 * 128 + ((((ds << 2) | g4) ^ fk) << 4) + kg * 4096;
;     const LAS unsigned char* krp = shm + KOFF + 8192 + kr0 * 64 + ((g4 ^ (((kr0 >> 4) & 1) << 1)) << 4) + kg * 2048;
; #pragma unroll
;     for (int s_ = 0; s_ < 2; ++s_) vp[s_] = shm + VOFF + q16 * 128 + ((((s_ << 2) | g4) ^ ((q16 >> 1) & 7)) << 4);
;     const LAS unsigned char* vpk = kg ? vp[1] : vp[0];
;     ...
;     ATT_DMA_K(0, 0); ATT_DMA_V(0, 0); ATT_DMA_K(1, 1); ATT_DMA_K(2, 2);
; __global__ void __launch_bounds__(NWAVES * 64, 2) mega_fwd(Args args_) {
;     ...
;             for (int i = 0;; ++i) { const int u = i * F.G + F.vcu; if (u >= 2048) break; const int sid = u >> 5, qb = u & 31, b = sid >> 3, kvh = (sid >> 2) & 1, g = sid & 3;
;                 att::attn_unit<64, 64>(QK + 1024 + kvh * 256 + g * 64, QKW, QK + 1536 + kvh * 64, QKW, nullptr, VTE + (size_t)(512 + kvh * 64) * NR, H + 512 + kvh * 256 + g * 64, 1024, b * TPS + qb * 256, b * TPS, 132, F.lds, IN(a, I_BQK) + j * 128, (const f32x2*)(ws + WS_ROPE64), qb * 256); }
.LBB0_955:
	s_bfe_u32 s46, s4, 0x10007
	s_lshr_b32 s5, s4, 8
	s_lshl_b32 s6, s46, 9
	s_add_u32 s6, s15, s6
	s_addc_u32 s7, s17, 0
	s_lshl_b32 s16, s4, 1
	s_and_b32 s16, s16, 0xc0
	s_lshl_b32 s43, s16, 1
	s_add_u32 s28, s6, s43
	s_addc_u32 s29, s7, 0
	s_lshl_b32 s6, s46, 7
	s_add_u32 s36, s24, s6
	s_addc_u32 s37, s25, 0
	s_mul_i32 s6, s46, 0x840000
	s_add_u32 s6, s10, s6
	s_addc_u32 s7, s11, 0
	s_add_u32 s40, s6, 0x4200000
	s_addc_u32 s41, s7, 0
	s_mov_b64 s[6:7], s[0:1]
	s_load_dwordx2 s[6:7], s[6:7], 0x60
	s_lshl_b32 s47, s4, 8
	s_mul_i32 s44, s5, 0x2100
	s_and_b32 s4, s47, 0x1f00
	s_add_i32 s48, s44, s4
	s_waitcnt lgkmcnt(0)
	s_add_u32 s26, s6, s22
	s_addc_u32 s27, s7, s23
	v_readfirstlane_b32 s4, v0
	s_cmpk_gt_u32 s4, 0xff
	s_mov_b64 s[4:5], -1
	s_cbranch_scc0 .LBB0_962
	v_mov_b32_e32 v162, v0
	s_ashr_i32 s45, s44, 31
	v_readfirstlane_b32 s6, v162
	s_ashr_i32 s4, s6, 6
	v_bfe_u32 v2, v162, 3, 3
	v_lshl_or_b32 v6, s4, 3, v2
	s_lshl_b32 s5, s4, 1
	s_lshr_b32 s7, s6, 5
	v_ashrrev_i32_e32 v3, 1, v6
	s_and_b32 s5, s5, 2
	s_and_b32 s7, s7, 4
	v_and_b32_e32 v2, 7, v162
	v_and_b32_e32 v4, 1, v3
	s_or_b32 s5, s5, s7
	v_bitop3_b32 v7, s5, v2, v4 bitop3:0x36
	v_xor_b32_e32 v8, v3, v162
	v_add_u32_e32 v4, s44, v6
	v_mov_b64_e32 v[2:3], s[36:37]
	s_and_b32 s49, s4, 3
	s_lshl_b32 s50, s4, 10
	v_mad_i64_i32 v[2:3], s[4:5], v4, s92, v[2:3]
	v_mov_b64_e32 v[4:5], s[40:41]
	v_lshlrev_b32_e32 v194, 4, v7
	v_mad_i64_i32 v[4:5], s[4:5], v6, s91, v[4:5]
	v_lshl_add_u64 v[164:165], v[2:3], 0, v[194:195]
	v_lshlrev_b32_e32 v2, 4, v8
	s_add_i32 s50, s50, 0
	v_lshl_add_u64 v[4:5], s[44:45], 1, v[4:5]
	v_and_b32_e32 v194, 0x70, v2
	s_mov_b32 s4, m0
	s_mov_b32 m0, s50
	s_nop 0
	global_load_lds_dwordx4 v[164:165], off
	s_mov_b32 m0, s4
	v_lshl_add_u64 v[166:167], v[4:5], 0, v[194:195]
	s_add_i32 s45, s50, 0x9000
	s_mov_b32 s4, m0
	s_mov_b32 m0, s45
	s_nop 0
	global_load_lds_dwordx4 v[166:167], off
	s_mov_b32 m0, s4
	s_mov_b64 s[4:5], 0x38000
	v_and_b32_e32 v1, 15, v162
	s_lshl_b32 s7, s49, 6
	v_lshl_add_u64 v[2:3], v[164:165], 0, s[4:5]
	s_add_i32 s4, s50, 0x2000
	s_mov_b32 s5, m0
	s_mov_b32 m0, s4
	s_nop 0
	global_load_lds_dwordx4 v[2:3], off
	s_mov_b32 m0, s5
	v_lshlrev_b32_e32 v163, 7, v1
	s_mov_b64 s[4:5], 0x70000
	v_or_b32_e32 v1, s7, v1
	v_and_b32_e32 v194, 48, v162
	v_lshrrev_b32_e32 v34, 1, v162
	v_lshl_add_u64 v[2:3], v[164:165], 0, s[4:5]
	s_add_i32 s4, s50, 0x4000
	v_or_b32_e32 v1, s48, v1
	v_lshl_add_u64 v[6:7], s[28:29], 0, v[194:195]
	s_mov_b32 s5, m0
	s_mov_b32 m0, s4
	s_nop 0
	global_load_lds_dwordx4 v[2:3], off
	s_mov_b32 m0, s5
	v_and_b32_e32 v35, 8, v34
	v_mad_i64_i32 v[8:9], s[4:5], v1, s92, v[6:7]
	v_or_b32_e32 v10, 16, v1
	v_or_b32_e32 v14, 32, v1
	v_or_b32_e32 v1, 48, v1
	v_lshl_or_b32 v194, v35, 3, v163
	v_mad_i64_i32 v[24:25], s[4:5], v10, s92, v[6:7]
	v_mad_i64_i32 v[26:27], s[4:5], v14, s92, v[6:7]
	v_mad_i64_i32 v[30:31], s[4:5], v1, s92, v[6:7]
	v_lshl_add_u64 v[22:23], s[8:9], 0, v[194:195]
	s_mov_b64 s[4:5], 0x1800
	v_lshl_add_u64 v[28:29], v[22:23], 0, s[60:61]
	v_lshl_add_u64 v[32:33], v[22:23], 0, s[4:5]
	s_movk_i32 s4, 0x1000
	global_load_dwordx4 v[72:75], v[8:9], off offset:64
	global_load_dwordx4 v[2:5], v194, s[8:9] offset:48
	global_load_dwordx4 v[128:131], v[24:25], off offset:64
	global_load_dwordx4 v[10:13], v194, s[8:9] offset:2096
	global_load_dwordx4 v[152:155], v[26:27], off offset:64
	global_load_dwordx4 v[68:71], v[28:29], off offset:48
	global_load_dwordx4 v[176:179], v[30:31], off offset:64
	global_load_dwordx4 v[14:17], v[32:33], off offset:48
	global_load_dwordx4 v[102:105], v194, s[8:9] offset:32
	global_load_dwordx4 v[94:97], v194, s[8:9] offset:2080
	global_load_dwordx4 v[64:67], v[28:29], off offset:32
	global_load_dwordx4 v[18:21], v[32:33], off offset:32
	global_load_dwordx4 v[110:113], v[8:9], off
	s_nop 0
	global_load_dwordx4 v[6:9], v194, s[8:9]
	global_load_dwordx4 v[106:109], v[24:25], off
	global_load_dwordx4 v[98:101], v194, s[8:9] offset:16
	global_load_dwordx4 v[82:85], v[26:27], off
	global_load_dwordx4 v[86:89], v194, s[8:9] offset:2064
	v_add_co_u32_e32 v26, vcc, s4, v22
	v_lshlrev_b32_e32 v22, 1, v162
	s_nop 0
	v_addc_co_u32_e32 v27, vcc, 0, v23, vcc
	v_and_b32_e32 v23, 3, v162
	global_load_dwordx4 v[56:59], v[26:27], off
	global_load_dwordx4 v[78:81], v[30:31], off
	global_load_dwordx4 v[60:63], v[28:29], off offset:16
	global_load_dwordx4 v[90:93], v194, s[8:9] offset:2048
	v_and_or_b32 v28, v22, 24, v23
	global_load_dwordx4 v[22:25], v[32:33], off offset:16
	s_lshl_b32 s4, s6, 4
	s_and_b32 s4, s4, 0xfffff000
	s_add_i32 s4, s4, 0
	v_lshl_add_u32 v170, v28, 7, s4
	s_or_b32 s4, s7, s47
	v_bfe_u32 v169, v162, 4, 2
	s_lshr_b32 s4, s4, 2
	v_bitop3_b32 v28, v169, v34, 7 bitop3:0x78
	s_and_b32 s4, s4, 0x7f0
	v_lshlrev_b32_e32 v168, 4, v28
	v_or_b32_e32 v28, s4, v35
	v_lshlrev_b32_e32 v28, 3, v28
	v_lshlrev_b32_e32 v76, 5, v169
	global_load_dwordx4 v[32:35], v28, s[8:9] offset:48
	global_load_dwordx4 v[36:39], v28, s[8:9] offset:32
	global_load_dwordx4 v[40:43], v28, s[8:9] offset:16
	global_load_dwordx4 v[44:47], v28, s[8:9]
	s_nop 0
	global_load_dwordx4 v[28:31], v[26:27], off offset:2048
	global_load_dwordx4 v[48:51], v76, s[26:27] offset:144
	global_load_dwordx4 v[52:55], v76, s[26:27] offset:128
	v_and_b32_e32 v1, 63, v162
	v_cmp_gt_u32_e32 vcc, 32, v1
	s_mov_b32 s4, 0x358637bd
	s_mov_b32 s12, 0x3c800000
	v_add_u32_e32 v174, v170, v168
	s_cmpk_lt_u32 s6, 0x100
	s_mov_b32 s51, 1
	s_mov_b32 s16, 2
	s_waitcnt vmcnt(22)
	v_cndmask_b32_e64 v115, v17, -v17, vcc
	v_cndmask_b32_e64 v114, v15, -v15, vcc
	v_mov_b32_e32 v15, v16
	s_waitcnt vmcnt(20)
; template <int DQK, int DV, bool LEAD> ...
;     ...
;           for (int ds = 0; ds < NDS; ++ds) raw[ds] = *(const bf16x8*)(qp + ds * 32);
;           float x[NDS][8];
; #pragma unroll
;           for (int ds = 0; ds < NDS; ++ds)
; #pragma unroll
;               for (int j = 0; j < 8; ++j) x[ds][j] = __uint_as_float(((unsigned)(unsigned short)raw[ds][j]) << 16);
;           const int tq = tq0 + qoff + qb * 16 + q16, prow = (tq >> 6) & 127, pcol = tq & 63;
;           float sn = 0.f;
; #pragma unroll
;           for (int ds = 0; ds < 2; ++ds)
; #pragma unroll
;               for (int j = 0; j < 8; ++j) sn += x[ds][j] * x[ds][j];
;           sn = lanes4_sum(sn);
;           const float rn = rsqrtf(sn * (1.f / 64.f) + EPS);
; #pragma unroll
;           for (int ds = 0; ds < 2; ++ds)
; #pragma unroll
;               for (int j = 0; j < 8; ++j) x[ds][j] *= rn * qgain[32 * ds + 8 * g4 + j];
	v_cndmask_b32_e64 v135, v97, -v97, vcc
	v_cndmask_b32_e64 v134, v95, -v95, vcc
	v_cndmask_b32_e64 v144, v3, -v3, vcc
	v_mov_b32_e32 v3, v4
	v_cndmask_b32_e64 v27, v13, -v13, vcc
	v_cndmask_b32_e64 v26, v11, -v11, vcc
	v_and_b32_e32 v117, 0xffff0000, v179
	v_lshlrev_b32_e32 v116, 16, v179
	s_waitcnt vmcnt(17)
	v_and_b32_e32 v179, 0xffff0000, v110
	v_mov_b32_e32 v11, v12
	v_cndmask_b32_e64 v13, v105, -v105, vcc
	v_cndmask_b32_e64 v12, v103, -v103, vcc
	v_mov_b32_e32 v103, v104
	v_cndmask_b32_e64 v105, v67, -v67, vcc
	v_cndmask_b32_e64 v104, v65, -v65, vcc
	v_mov_b32_e32 v65, v66
	v_and_b32_e32 v67, 0xffff0000, v178
	v_lshlrev_b32_e32 v66, 16, v178
	v_lshlrev_b32_e32 v178, 16, v110
	v_mul_f32_e32 v4, v179, v179
	v_cndmask_b32_e64 v145, v5, -v5, vcc
	v_mov_b32_e32 v95, v96
	v_cndmask_b32_e64 v17, v21, -v21, vcc
	v_cndmask_b32_e64 v16, v19, -v19, vcc
	v_mov_b32_e32 v19, v20
	v_and_b32_e32 v97, 0xffff0000, v177
	v_lshlrev_b32_e32 v96, 16, v177
	s_waitcnt vmcnt(7)
	v_cndmask_b32_e64 v21, v25, -v25, vcc
	v_cndmask_b32_e64 v20, v23, -v23, vcc
	v_mov_b32_e32 v23, v24
	v_cndmask_b32_e64 v25, v93, -v93, vcc
	v_cndmask_b32_e64 v24, v91, -v91, vcc
	v_mov_b32_e32 v91, v92
	v_and_b32_e32 v93, 0xffff0000, v176
	v_lshlrev_b32_e32 v92, 16, v176
	v_and_b32_e32 v177, 0xffff0000, v111
	v_lshlrev_b32_e32 v176, 16, v111
	v_pk_fma_f32 v[4:5], v[178:179], v[178:179], v[4:5] op_sel_hi:[1,1,0]
	v_and_b32_e32 v149, 0xffff0000, v75
	v_lshlrev_b32_e32 v148, 16, v75
	v_cndmask_b32_e64 v119, v71, -v71, vcc
	v_cndmask_b32_e64 v118, v69, -v69, vcc
	v_mov_b32_e32 v69, v70
	v_and_b32_e32 v151, 0xffff0000, v74
	v_lshlrev_b32_e32 v150, 16, v74
	v_and_b32_e32 v157, 0xffff0000, v73
	v_lshlrev_b32_e32 v156, 16, v73
	v_and_b32_e32 v161, 0xffff0000, v72
	v_lshlrev_b32_e32 v160, 16, v72
	global_load_dwordx4 v[70:73], v76, s[26:27] offset:16
	s_nop 0
	global_load_dwordx4 v[74:77], v76, s[26:27]
	v_pk_fma_f32 v[4:5], v[176:177], v[176:177], v[4:5]
	v_mul_f32_e32 v110, v177, v177
	v_and_b32_e32 v173, 0xffff0000, v112
	v_lshlrev_b32_e32 v172, 16, v112
	v_pk_add_f32 v[4:5], v[110:111], v[4:5] op_sel_hi:[0,1]
	v_pk_fma_f32 v[4:5], v[172:173], v[172:173], v[4:5]
	v_mul_f32_e32 v110, v173, v173
	v_cndmask_b32_e64 v159, v9, -v9, vcc
	v_cndmask_b32_e64 v158, v7, -v7, vcc
	v_mov_b32_e32 v7, v8
	v_and_b32_e32 v9, 0xffff0000, v113
	v_lshlrev_b32_e32 v8, 16, v113
	v_pk_add_f32 v[4:5], v[110:111], v[4:5] op_sel_hi:[0,1]
	v_pk_fma_f32 v[4:5], v[8:9], v[8:9], v[4:5]
	v_mul_f32_e32 v110, v9, v9
	v_pk_add_f32 v[4:5], v[110:111], v[4:5] op_sel_hi:[0,1]
	v_pk_fma_f32 v[4:5], v[160:161], v[160:161], v[4:5]
	v_mul_f32_e32 v110, v161, v161
	v_pk_add_f32 v[4:5], v[110:111], v[4:5] op_sel_hi:[0,1]
	v_pk_fma_f32 v[4:5], v[156:157], v[156:157], v[4:5]
	v_mul_f32_e32 v110, v157, v157
	v_pk_add_f32 v[4:5], v[110:111], v[4:5] op_sel_hi:[0,1]
	v_pk_fma_f32 v[4:5], v[150:151], v[150:151], v[4:5]
	v_mul_f32_e32 v110, v151, v151
	v_pk_add_f32 v[4:5], v[110:111], v[4:5] op_sel_hi:[0,1]
	v_pk_fma_f32 v[4:5], v[148:149], v[148:149], v[4:5]
	v_mul_f32_e32 v110, v149, v149
	v_pk_add_f32 v[4:5], v[110:111], v[4:5] op_sel_hi:[0,1]
	v_mov_b32_e32 v5, v4
	s_nop 1
	v_permlane16_swap_b32_e32 v4, v5
	v_add_f32_e32 v5, v4, v5
	v_and_b32_e32 v127, 0xffff0000, v153
	v_lshlrev_b32_e32 v126, 16, v153
	v_and_b32_e32 v147, 0xffff0000, v107
	v_lshlrev_b32_e32 v146, 16, v107
	v_mov_b32_e32 v107, v5
	v_and_b32_e32 v153, 0xffff0000, v106
	v_and_b32_e32 v133, 0xffff0000, v131
	v_lshlrev_b32_e32 v132, 16, v131
	v_and_b32_e32 v137, 0xffff0000, v130
	v_lshlrev_b32_e32 v136, 16, v130
	v_and_b32_e32 v131, 0xffff0000, v152
	v_lshlrev_b32_e32 v130, 16, v152
	v_permlane32_swap_b32_e32 v5, v107
	v_lshlrev_b32_e32 v152, 16, v106
	v_mul_f32_e32 v4, v153, v153
	v_pk_fma_f32 v[110:111], v[152:153], v[152:153], v[4:5] op_sel_hi:[1,1,0]
	v_mul_f32_e32 v4, v147, v147
	v_pk_fma_f32 v[110:111], v[146:147], v[146:147], v[110:111]
	v_and_b32_e32 v113, 0xffff0000, v108
	v_lshlrev_b32_e32 v112, 16, v108
	v_pk_add_f32 v[110:111], v[4:5], v[110:111] op_sel_hi:[0,1]
	v_pk_fma_f32 v[110:111], v[112:113], v[112:113], v[110:111]
	v_mul_f32_e32 v4, v113, v113
	v_and_b32_e32 v143, 0xffff0000, v109
	v_lshlrev_b32_e32 v142, 16, v109
	v_pk_add_f32 v[110:111], v[4:5], v[110:111] op_sel_hi:[0,1]
	v_pk_fma_f32 v[110:111], v[142:143], v[142:143], v[110:111]
	v_mul_f32_e32 v4, v143, v143
	v_cndmask_b32_e64 v125, v63, -v63, vcc
	v_cndmask_b32_e64 v124, v61, -v61, vcc
	v_mov_b32_e32 v61, v62
	v_and_b32_e32 v63, 0xffff0000, v128
	v_lshlrev_b32_e32 v62, 16, v128
	v_pk_add_f32 v[110:111], v[4:5], v[110:111] op_sel_hi:[0,1]
	v_pk_fma_f32 v[110:111], v[62:63], v[62:63], v[110:111]
	v_mul_f32_e32 v4, v63, v63
	v_and_b32_e32 v141, 0xffff0000, v129
	v_lshlrev_b32_e32 v140, 16, v129
	v_pk_add_f32 v[110:111], v[4:5], v[110:111] op_sel_hi:[0,1]
	v_pk_fma_f32 v[110:111], v[140:141], v[140:141], v[110:111]
	v_mul_f32_e32 v4, v141, v141
	v_pk_add_f32 v[110:111], v[4:5], v[110:111] op_sel_hi:[0,1]
	v_pk_fma_f32 v[110:111], v[136:137], v[136:137], v[110:111]
	v_mul_f32_e32 v4, v137, v137
	v_pk_add_f32 v[110:111], v[4:5], v[110:111] op_sel_hi:[0,1]
	v_pk_fma_f32 v[110:111], v[132:133], v[132:133], v[110:111]
	v_mul_f32_e32 v4, v133, v133
	v_pk_add_f32 v[110:111], v[4:5], v[110:111] op_sel_hi:[0,1]
	v_mov_b32_e32 v4, v110
	s_nop 1
	v_permlane16_swap_b32_e32 v110, v4
	v_add_f32_e32 v4, v110, v4
	v_mov_b32_e32 v106, v4
	s_nop 1
	v_permlane32_swap_b32_e32 v4, v106
	v_pk_add_f32 v[4:5], v[4:5], v[106:107]
	v_mov_b64_e32 v[110:111], s[4:5]
	v_pk_fma_f32 v[180:181], v[4:5], s[12:13], v[110:111] op_sel_hi:[1,0,0]
	s_waitcnt vmcnt(5)
; template <int DQK, int DV, bool LEAD> ...
;     ...
;           const float rn = rsqrtf(sn * (1.f / 64.f) + EPS);
; #pragma unroll
;           for (int ds = 0; ds < 2; ++ds)
; #pragma unroll
;               for (int j = 0; j < 8; ++j) x[ds][j] *= rn * qgain[32 * ds + 8 * g4 + j];
;           if constexpr (DQK == 64) {
; #pragma unroll
;               for (int ds = 0; ds < 2; ++ds)
; #pragma unroll
;                   for (int j = 0; j < 8; ++j) {
;                       auto rr = __builtin_amdgcn_permlane32_swap(__float_as_uint(x[ds][j]), __float_as_uint(x[ds][j]), false, false);
;                       const float other = hi ? __uint_as_float(rr[0]) : __uint_as_float(rr[1]);
;                       float cc = 1.f, sg = 0.f;
;                       if (lat) { const f32x2 cs = rope[(ds ? pcol : prow) * 16 + 8 * (g4 & 1) + j]; cc = cs.x; sg = hi ? cs.y : -cs.y; }
;                       x[ds][j] = x[ds][j] * cc + other * sg; }
	v_cndmask_b32_e64 v106, v45, -v45, vcc
	v_mul_f32_e32 v4, 0x4b800000, v181
	v_cmp_gt_f32_e64 s[4:5], s95, v181
	v_mov_b32_e32 v45, v46
	v_cndmask_b32_e64 v139, v89, -v89, vcc
	v_cndmask_b32_e64 v4, v181, v4, s[4:5]
	v_rsq_f32_e32 v4, v4
	v_cndmask_b32_e64 v138, v87, -v87, vcc
	v_mov_b32_e32 v87, v88
	s_waitcnt vmcnt(4)
	v_cndmask_b32_e64 v89, v31, -v31, vcc
	v_mul_f32_e32 v5, 0x45800000, v4
	v_cndmask_b32_e64 v46, v4, v5, s[4:5]
	s_waitcnt vmcnt(3)
	v_pk_mul_f32 v[4:5], v[46:47], v[50:51] op_sel_hi:[0,1]
	v_pk_mul_f32 v[4:5], v[4:5], v[148:149]
	v_cndmask_b32_e64 v88, v29, -v29, vcc
	v_mov_b32_e32 v29, v30
	v_cndmask_b32_e64 v31, v35, -v35, vcc
	v_cndmask_b32_e64 v30, v33, -v33, vcc
	v_mov_b32_e32 v33, v34
	v_cndmask_b32_e64 v35, v39, -v39, vcc
	v_cndmask_b32_e64 v34, v37, -v37, vcc
	v_mov_b32_e32 v37, v38
	v_cndmask_b32_e64 v39, v43, -v43, vcc
	v_cndmask_b32_e64 v38, v41, -v41, vcc
	v_mov_b32_e32 v41, v42
	v_and_b32_e32 v109, 0xffff0000, v83
	v_lshlrev_b32_e32 v108, 16, v83
	v_and_b32_e32 v43, 0xffff0000, v79
	v_lshlrev_b32_e32 v42, 16, v79
	v_cndmask_b32_e64 v107, v47, -v47, vcc
	v_mov_b32_e32 v47, v4
	v_mov_b32_e32 v79, v4
	v_mov_b32_e32 v83, v5
	v_mov_b32_e32 v148, v5
	v_permlane32_swap_b32_e32 v47, v79
	s_nop 0
	v_permlane32_swap_b32_e32 v83, v148
	v_cndmask_b32_e32 v149, v83, v148, vcc
	v_cndmask_b32_e32 v148, v47, v79, vcc
	v_pk_mul_f32 v[144:145], v[144:145], v[148:149]
	v_and_b32_e32 v121, 0xffff0000, v155
	v_pk_fma_f32 v[2:3], v[4:5], v[2:3], v[144:145]
	v_lshlrev_b32_e32 v120, 16, v155
	v_pk_mul_f32 v[2:3], v[2:3], s[94:95] op_sel_hi:[1,0]
	v_and_b32_e32 v123, 0xffff0000, v154
	v_cvt_pk_bf16_f32 v5, v2, v3
	v_pk_mul_f32 v[2:3], v[46:47], v[48:49] op_sel_hi:[0,1]
	v_pk_mul_f32 v[2:3], v[2:3], v[150:151]
	v_lshlrev_b32_e32 v122, 16, v154
	v_mov_b32_e32 v4, v2
	v_mov_b32_e32 v47, v2
	v_mov_b32_e32 v79, v3
	v_mov_b32_e32 v83, v3
	v_permlane32_swap_b32_e32 v4, v47
	s_nop 0
	v_permlane32_swap_b32_e32 v79, v83
	v_cndmask_b32_e32 v145, v79, v83, vcc
	v_cndmask_b32_e32 v144, v4, v47, vcc
	v_pk_mul_f32 v[12:13], v[12:13], v[144:145]
	v_cndmask_b32_e64 v155, v101, -v101, vcc
	v_pk_fma_f32 v[2:3], v[2:3], v[102:103], v[12:13]
	v_cndmask_b32_e64 v154, v99, -v99, vcc
	v_pk_mul_f32 v[2:3], v[2:3], s[94:95] op_sel_hi:[1,0]
	v_mov_b32_e32 v99, v100
	v_cvt_pk_bf16_f32 v4, v2, v3
	s_waitcnt vmcnt(2)
	v_pk_mul_f32 v[2:3], v[46:47], v[54:55] op_sel_hi:[0,1]
	v_pk_mul_f32 v[2:3], v[2:3], v[156:157]
	v_cmp_gt_f32_e64 s[4:5], s95, v180
	v_mov_b32_e32 v12, v2
	v_mov_b32_e32 v47, v2
	v_mov_b32_e32 v13, v3
	v_mov_b32_e32 v79, v3
	v_permlane32_swap_b32_e32 v12, v47
	s_nop 0
	v_permlane32_swap_b32_e32 v13, v79
	v_cndmask_b32_e32 v13, v13, v79, vcc
	v_cndmask_b32_e32 v12, v12, v47, vcc
	v_pk_mul_f32 v[12:13], v[154:155], v[12:13]
	v_cndmask_b32_e64 v129, v59, -v59, vcc
	v_pk_fma_f32 v[2:3], v[2:3], v[98:99], v[12:13]
	v_pk_mul_f32 v[12:13], v[52:53], v[46:47] op_sel_hi:[1,0]
	v_pk_mul_f32 v[2:3], v[2:3], s[94:95] op_sel_hi:[1,0]
	v_pk_mul_f32 v[12:13], v[12:13], v[160:161]
	v_cvt_pk_bf16_f32 v3, v2, v3
	v_mov_b32_e32 v2, v12
	v_mov_b32_e32 v47, v12
	v_mov_b32_e32 v79, v13
	v_mov_b32_e32 v83, v13
	v_permlane32_swap_b32_e32 v2, v47
	s_nop 0
	v_permlane32_swap_b32_e32 v79, v83
	v_cndmask_b32_e32 v99, v79, v83, vcc
	v_cndmask_b32_e32 v98, v2, v47, vcc
	v_pk_mul_f32 v[98:99], v[158:159], v[98:99]
	v_cndmask_b32_e64 v128, v57, -v57, vcc
	v_pk_fma_f32 v[6:7], v[12:13], v[6:7], v[98:99]
	v_mov_b32_e32 v57, v58
	v_pk_mul_f32 v[6:7], v[6:7], s[94:95] op_sel_hi:[1,0]
	v_and_b32_e32 v59, 0xffff0000, v85
	v_cvt_pk_bf16_f32 v2, v6, v7
	s_waitcnt vmcnt(1)
	v_pk_mul_f32 v[6:7], v[72:73], v[46:47] op_sel_hi:[1,0]
	v_lshlrev_b32_e32 v58, 16, v85
	v_pk_mul_f32 v[6:7], v[6:7], v[8:9]
	v_and_b32_e32 v85, 0xffff0000, v84
	v_mov_b32_e32 v8, v6
	v_mov_b32_e32 v12, v6
	v_mov_b32_e32 v9, v7
	v_mov_b32_e32 v13, v7
	v_permlane32_swap_b32_e32 v8, v12
	s_nop 0
	v_permlane32_swap_b32_e32 v9, v13
	v_cndmask_b32_e32 v9, v9, v13, vcc
	v_cndmask_b32_e32 v8, v8, v12, vcc
	v_pk_mul_f32 v[8:9], v[30:31], v[8:9]
	v_lshlrev_b32_e32 v84, 16, v84
	v_pk_fma_f32 v[6:7], v[6:7], v[32:33], v[8:9]
	v_and_b32_e32 v101, 0xffff0000, v81
	v_pk_mul_f32 v[6:7], v[6:7], s[94:95] op_sel_hi:[1,0]
	v_lshlrev_b32_e32 v100, 16, v81
	v_cvt_pk_bf16_f32 v9, v6, v7
	v_pk_mul_f32 v[6:7], v[70:71], v[46:47] op_sel_hi:[1,0]
	v_and_b32_e32 v81, 0xffff0000, v80
	v_pk_mul_f32 v[6:7], v[6:7], v[172:173]
	v_lshlrev_b32_e32 v80, 16, v80
	v_mov_b32_e32 v8, v6
	v_mov_b32_e32 v12, v6
	v_mov_b32_e32 v13, v7
	v_mov_b32_e32 v47, v7
	v_permlane32_swap_b32_e32 v8, v12
	s_nop 0
	v_permlane32_swap_b32_e32 v13, v47
	v_cndmask_b32_e32 v13, v13, v47, vcc
	v_cndmask_b32_e32 v12, v8, v12, vcc
	v_pk_mul_f32 v[12:13], v[34:35], v[12:13]
	s_nop 0
	v_pk_fma_f32 v[6:7], v[6:7], v[36:37], v[12:13]
	s_nop 0
	v_pk_mul_f32 v[6:7], v[6:7], s[94:95] op_sel_hi:[1,0]
	s_nop 0
	v_cvt_pk_bf16_f32 v8, v6, v7
	s_waitcnt vmcnt(0)
; __device__ __forceinline__ unsigned cvtpk(float lo, float hi) { f32x2 v = {lo, hi}; bf16x2_t b = __builtin_convertvector(v, bf16x2_t); return __builtin_bit_cast(unsigned, b); }
; template <int DQK, int DV, bool LEAD> ...
;     ...
;           const float rn = rsqrtf(sn * (1.f / 64.f) + EPS);
; #pragma unroll
;           for (int ds = 0; ds < 2; ++ds)
; #pragma unroll
;               for (int j = 0; j < 8; ++j) x[ds][j] *= rn * qgain[32 * ds + 8 * g4 + j];
;           if constexpr (DQK == 64) {
; #pragma unroll
;               for (int ds = 0; ds < 2; ++ds)
; #pragma unroll
;                   for (int j = 0; j < 8; ++j) {
;                       auto rr = __builtin_amdgcn_permlane32_swap(__float_as_uint(x[ds][j]), __float_as_uint(x[ds][j]), false, false);
;                       const float other = hi ? __uint_as_float(rr[0]) : __uint_as_float(rr[1]);
;                       float cc = 1.f, sg = 0.f;
;                       if (lat) { const f32x2 cs = rope[(ds ? pcol : prow) * 16 + 8 * (g4 & 1) + j]; cc = cs.x; sg = hi ? cs.y : -cs.y; }
;                       x[ds][j] = x[ds][j] * cc + other * sg; }
;           } else {
;               float sr = 0.f;
; #pragma unroll
;               for (int j = 0; j < 8; ++j) sr += x[2][j] * x[2][j];
;               sr = lanes4_sum(sr);
;               const float rq = rsqrtf(sr * (1.f / 32.f) + EPS);
; #pragma unroll
;               for (int j = 0; j < 8; ++j) { const float av = x[2][j] * rq * qgain[64 + 8 * g4 + j];
;                   auto rr = __builtin_amdgcn_permlane16_swap(__float_as_uint(av), __float_as_uint(av), false, false);
;                   const float other = (g4 & 1) ? __uint_as_float(rr[0]) : __uint_as_float(rr[1]);
;                   float cc = 1.f, sg = 0.f;
;                   if (lat) { const f32x2 cs = rope[((g4 & 2) ? pcol : prow) * 8 + j]; cc = cs.x; sg = (g4 & 1) ? cs.y : -cs.y; }
;                   x[2][j] = av * cc + other * sg; }
;           }
; #pragma unroll
;           for (int ds = 0; ds < NDS; ++ds) { u32x4 w;
; #pragma unroll
;               for (int i = 0; i < 4; ++i) w[i] = cvtpk(x[ds][2 * i] * c2, x[ds][2 * i + 1] * c2);
;               qf[qb * NDS + ds] = __builtin_bit_cast(bf16x8, w); }
	v_pk_mul_f32 v[6:7], v[76:77], v[46:47] op_sel_hi:[1,0]
	s_nop 0
	v_pk_mul_f32 v[6:7], v[6:7], v[176:177]
	s_nop 0
	v_mov_b32_e32 v12, v6
	v_mov_b32_e32 v47, v6
	v_mov_b32_e32 v13, v7
	v_mov_b32_e32 v79, v7
	v_permlane32_swap_b32_e32 v12, v47
	s_nop 0
	v_permlane32_swap_b32_e32 v13, v79
	v_cndmask_b32_e32 v13, v13, v79, vcc
	v_cndmask_b32_e32 v12, v12, v47, vcc
	v_pk_mul_f32 v[12:13], v[38:39], v[12:13]
	s_nop 0
	v_pk_fma_f32 v[6:7], v[6:7], v[40:41], v[12:13]
	v_pk_mul_f32 v[12:13], v[74:75], v[46:47] op_sel_hi:[1,0]
	v_pk_mul_f32 v[6:7], v[6:7], s[94:95] op_sel_hi:[1,0]
	v_pk_mul_f32 v[12:13], v[12:13], v[178:179]
	v_cvt_pk_bf16_f32 v7, v6, v7
	v_mov_b32_e32 v6, v12
	v_mov_b32_e32 v46, v12
	s_nop 1
	v_permlane32_swap_b32_e32 v6, v46
	v_mov_b32_e32 v47, v13
	v_mov_b32_e32 v79, v13
	v_cndmask_b32_e32 v46, v6, v46, vcc
	v_mul_f32_e32 v6, 0x4b800000, v180
	v_permlane32_swap_b32_e32 v47, v79
	v_cndmask_b32_e64 v6, v180, v6, s[4:5]
	v_cndmask_b32_e32 v47, v47, v79, vcc
	v_rsq_f32_e32 v79, v6
	v_pk_mul_f32 v[46:47], v[106:107], v[46:47]
	s_nop 0
	v_pk_fma_f32 v[12:13], v[12:13], v[44:45], v[46:47]
	s_nop 0
	v_pk_mul_f32 v[12:13], v[12:13], s[94:95] op_sel_hi:[1,0]
	s_nop 0
	v_cvt_pk_bf16_f32 v6, v12, v13
	v_mul_f32_e32 v12, 0x45800000, v79
	v_cndmask_b32_e64 v46, v79, v12, s[4:5]
	v_pk_mul_f32 v[12:13], v[50:51], v[46:47] op_sel_hi:[1,0]
	s_nop 0
	v_pk_mul_f32 v[12:13], v[12:13], v[132:133]
	s_nop 0
	v_mov_b32_e32 v47, v12
	v_mov_b32_e32 v79, v12
	v_mov_b32_e32 v83, v13
	v_mov_b32_e32 v98, v13
	v_permlane32_swap_b32_e32 v47, v79
	s_nop 0
	v_permlane32_swap_b32_e32 v83, v98
	v_cndmask_b32_e32 v99, v83, v98, vcc
	v_cndmask_b32_e32 v98, v47, v79, vcc
	v_pk_mul_f32 v[26:27], v[26:27], v[98:99]
	v_and_b32_e32 v83, 0xffff0000, v82
	v_pk_fma_f32 v[10:11], v[12:13], v[10:11], v[26:27]
	v_lshlrev_b32_e32 v82, 16, v82
	v_pk_mul_f32 v[10:11], v[10:11], s[94:95] op_sel_hi:[1,0]
	s_nop 0
	v_cvt_pk_bf16_f32 v13, v10, v11
	v_pk_mul_f32 v[10:11], v[48:49], v[46:47] op_sel_hi:[1,0]
	s_nop 0
	v_pk_mul_f32 v[10:11], v[10:11], v[136:137]
	s_nop 0
	v_mov_b32_e32 v12, v10
	v_mov_b32_e32 v26, v10
	v_mov_b32_e32 v27, v11
	v_mov_b32_e32 v47, v11
	v_permlane32_swap_b32_e32 v12, v26
	s_nop 0
	v_permlane32_swap_b32_e32 v27, v47
	v_cndmask_b32_e32 v27, v27, v47, vcc
	v_cndmask_b32_e32 v26, v12, v26, vcc
	v_pk_mul_f32 v[26:27], v[134:135], v[26:27]
	s_nop 0
	v_pk_fma_f32 v[10:11], v[10:11], v[94:95], v[26:27]
	s_nop 0
	v_pk_mul_f32 v[10:11], v[10:11], s[94:95] op_sel_hi:[1,0]
	s_nop 0
	v_cvt_pk_bf16_f32 v12, v10, v11
	v_pk_mul_f32 v[10:11], v[54:55], v[46:47] op_sel_hi:[1,0]
	s_nop 0
	v_pk_mul_f32 v[10:11], v[10:11], v[140:141]
	s_nop 0
	v_mov_b32_e32 v26, v10
	v_mov_b32_e32 v47, v10
	v_mov_b32_e32 v27, v11
	v_mov_b32_e32 v79, v11
	v_permlane32_swap_b32_e32 v26, v47
	s_nop 0
	v_permlane32_swap_b32_e32 v27, v79
	v_cndmask_b32_e32 v27, v27, v79, vcc
	v_cndmask_b32_e32 v26, v26, v47, vcc
	v_pk_mul_f32 v[26:27], v[138:139], v[26:27]
	s_nop 0
	v_pk_fma_f32 v[10:11], v[10:11], v[86:87], v[26:27]
	v_pk_mul_f32 v[26:27], v[52:53], v[46:47] op_sel_hi:[1,0]
	v_pk_mul_f32 v[10:11], v[10:11], s[94:95] op_sel_hi:[1,0]
	v_pk_mul_f32 v[26:27], v[26:27], v[62:63]
	v_cvt_pk_bf16_f32 v11, v10, v11
	v_mov_b32_e32 v10, v26
	v_mov_b32_e32 v47, v26
	v_mov_b32_e32 v62, v27
	v_mov_b32_e32 v63, v27
	v_permlane32_swap_b32_e32 v10, v47
	s_nop 0
	v_permlane32_swap_b32_e32 v62, v63
	v_cndmask_b32_e32 v63, v62, v63, vcc
	v_cndmask_b32_e32 v62, v10, v47, vcc
	v_pk_mul_f32 v[24:25], v[24:25], v[62:63]
	s_nop 0
	v_pk_fma_f32 v[24:25], v[26:27], v[90:91], v[24:25]
	v_and_b32_e32 v91, 0xffff0000, v78
	v_pk_mul_f32 v[24:25], v[24:25], s[94:95] op_sel_hi:[1,0]
	v_lshlrev_b32_e32 v90, 16, v78
	v_cvt_pk_bf16_f32 v10, v24, v25
	v_pk_mul_f32 v[24:25], v[72:73], v[46:47] op_sel_hi:[1,0]
	s_nop 0
	v_pk_mul_f32 v[24:25], v[24:25], v[142:143]
	s_nop 0
	v_mov_b32_e32 v26, v24
	v_mov_b32_e32 v47, v24
	v_mov_b32_e32 v27, v25
	v_mov_b32_e32 v62, v25
	v_permlane32_swap_b32_e32 v26, v47
	s_nop 0
	v_permlane32_swap_b32_e32 v27, v62
	v_cndmask_b32_e32 v27, v27, v62, vcc
	v_cndmask_b32_e32 v26, v26, v47, vcc
	v_pk_mul_f32 v[26:27], v[30:31], v[26:27]
	s_nop 0
	v_pk_fma_f32 v[24:25], v[24:25], v[32:33], v[26:27]
	s_nop 0
	v_pk_mul_f32 v[24:25], v[24:25], s[94:95] op_sel_hi:[1,0]
	s_nop 0
	v_cvt_pk_bf16_f32 v27, v24, v25
	v_pk_mul_f32 v[24:25], v[70:71], v[46:47] op_sel_hi:[1,0]
	s_nop 0
	v_pk_mul_f32 v[24:25], v[24:25], v[112:113]
	s_nop 0
	v_mov_b32_e32 v26, v24
	v_mov_b32_e32 v47, v24
	v_mov_b32_e32 v62, v25
	v_mov_b32_e32 v63, v25
	v_permlane32_swap_b32_e32 v26, v47
	s_nop 0
	v_permlane32_swap_b32_e32 v62, v63
	v_cndmask_b32_e32 v63, v62, v63, vcc
	v_cndmask_b32_e32 v62, v26, v47, vcc
	v_pk_mul_f32 v[62:63], v[34:35], v[62:63]
	s_nop 0
	v_pk_fma_f32 v[24:25], v[36:37], v[24:25], v[62:63]
	s_nop 0
	v_pk_mul_f32 v[24:25], v[24:25], s[94:95] op_sel_hi:[1,0]
	s_nop 0
	v_cvt_pk_bf16_f32 v26, v24, v25
	v_pk_mul_f32 v[24:25], v[76:77], v[46:47] op_sel_hi:[1,0]
	s_nop 0
	v_pk_mul_f32 v[24:25], v[24:25], v[146:147]
	s_nop 0
	v_mov_b32_e32 v47, v24
	v_mov_b32_e32 v62, v24
	v_mov_b32_e32 v63, v25
	v_mov_b32_e32 v79, v25
	v_permlane32_swap_b32_e32 v47, v62
	s_nop 0
	v_permlane32_swap_b32_e32 v63, v79
	v_cndmask_b32_e32 v63, v63, v79, vcc
	v_cndmask_b32_e32 v62, v47, v62, vcc
	v_pk_mul_f32 v[24:25], v[40:41], v[24:25]
	v_pk_mul_f32 v[46:47], v[74:75], v[46:47] op_sel_hi:[1,0]
	v_pk_fma_f32 v[24:25], v[38:39], v[62:63], v[24:25]
	v_pk_mul_f32 v[46:47], v[46:47], v[152:153]
	v_pk_mul_f32 v[24:25], v[24:25], s[94:95] op_sel_hi:[1,0]
	v_mov_b32_e32 v62, v46
	v_cvt_pk_bf16_f32 v25, v24, v25
	v_mov_b32_e32 v24, v46
	s_nop 1
; template <int DQK, int DV, bool LEAD> ...
;     ...
; #pragma unroll
;           for (int ds = 0; ds < 2; ++ds)
; #pragma unroll
;               for (int j = 0; j < 8; ++j) sn += x[ds][j] * x[ds][j];
;           sn = lanes4_sum(sn);
;           const float rn = rsqrtf(sn * (1.f / 64.f) + EPS);
; #pragma unroll
;           for (int ds = 0; ds < 2; ++ds)
; #pragma unroll
;               for (int j = 0; j < 8; ++j) x[ds][j] *= rn * qgain[32 * ds + 8 * g4 + j];
;           if constexpr (DQK == 64) {
; #pragma unroll
;               for (int ds = 0; ds < 2; ++ds)
; #pragma unroll
;                   for (int j = 0; j < 8; ++j) {
;                       auto rr = __builtin_amdgcn_permlane32_swap(__float_as_uint(x[ds][j]), __float_as_uint(x[ds][j]), false, false);
;                       const float other = hi ? __uint_as_float(rr[0]) : __uint_as_float(rr[1]);
;                       float cc = 1.f, sg = 0.f;
;                       if (lat) { const f32x2 cs = rope[(ds ? pcol : prow) * 16 + 8 * (g4 & 1) + j]; cc = cs.x; sg = hi ? cs.y : -cs.y; }
;                       x[ds][j] = x[ds][j] * cc + other * sg; }
	v_permlane32_swap_b32_e32 v24, v62
	v_cndmask_b32_e32 v62, v24, v62, vcc
	v_mul_f32_e32 v24, v83, v83
	v_pk_fma_f32 v[86:87], v[82:83], v[82:83], v[24:25] op_sel_hi:[1,1,0]
	v_mul_f32_e32 v24, v109, v109
	v_pk_fma_f32 v[86:87], v[108:109], v[108:109], v[86:87]
	v_mov_b32_e32 v63, v47
	v_pk_add_f32 v[86:87], v[24:25], v[86:87] op_sel_hi:[0,1]
	v_pk_fma_f32 v[86:87], v[84:85], v[84:85], v[86:87]
	v_mul_f32_e32 v24, v85, v85
	v_pk_add_f32 v[86:87], v[24:25], v[86:87] op_sel_hi:[0,1]
	v_pk_fma_f32 v[86:87], v[58:59], v[58:59], v[86:87]
	v_mul_f32_e32 v24, v59, v59
	v_pk_add_f32 v[86:87], v[24:25], v[86:87] op_sel_hi:[0,1]
	v_pk_fma_f32 v[86:87], v[130:131], v[130:131], v[86:87]
	v_mul_f32_e32 v24, v131, v131
	v_pk_add_f32 v[86:87], v[24:25], v[86:87] op_sel_hi:[0,1]
	v_pk_fma_f32 v[86:87], v[126:127], v[126:127], v[86:87]
	v_mul_f32_e32 v24, v127, v127
	v_pk_add_f32 v[86:87], v[24:25], v[86:87] op_sel_hi:[0,1]
	v_pk_fma_f32 v[86:87], v[122:123], v[122:123], v[86:87]
	v_mul_f32_e32 v24, v123, v123
	v_pk_add_f32 v[86:87], v[24:25], v[86:87] op_sel_hi:[0,1]
	v_pk_fma_f32 v[86:87], v[120:121], v[120:121], v[86:87]
	v_mul_f32_e32 v24, v121, v121
	v_pk_add_f32 v[86:87], v[24:25], v[86:87] op_sel_hi:[0,1]
	v_mov_b32_e32 v79, v47
	v_mov_b32_e32 v24, v86
	s_nop 0
	v_permlane32_swap_b32_e32 v63, v79
	v_permlane16_swap_b32_e32 v86, v24
	v_cndmask_b32_e32 v63, v63, v79, vcc
	v_add_f32_e32 v79, v86, v24
	v_mul_f32_e32 v24, v91, v91
	v_pk_fma_f32 v[94:95], v[90:91], v[90:91], v[24:25] op_sel_hi:[1,1,0]
	v_mul_f32_e32 v24, v43, v43
	v_pk_fma_f32 v[94:95], v[42:43], v[42:43], v[94:95]
	v_mov_b32_e32 v87, v79
	v_pk_add_f32 v[94:95], v[24:25], v[94:95] op_sel_hi:[0,1]
	v_pk_fma_f32 v[94:95], v[80:81], v[80:81], v[94:95]
	v_mul_f32_e32 v24, v81, v81
	v_pk_add_f32 v[94:95], v[24:25], v[94:95] op_sel_hi:[0,1]
	v_pk_fma_f32 v[94:95], v[100:101], v[100:101], v[94:95]
	v_mul_f32_e32 v24, v101, v101
	v_pk_add_f32 v[94:95], v[24:25], v[94:95] op_sel_hi:[0,1]
	v_pk_fma_f32 v[94:95], v[92:93], v[92:93], v[94:95]
	v_mul_f32_e32 v24, v93, v93
	v_pk_add_f32 v[94:95], v[24:25], v[94:95] op_sel_hi:[0,1]
	v_pk_fma_f32 v[94:95], v[96:97], v[96:97], v[94:95]
	v_mul_f32_e32 v24, v97, v97
	v_pk_add_f32 v[94:95], v[24:25], v[94:95] op_sel_hi:[0,1]
	v_pk_fma_f32 v[94:95], v[66:67], v[66:67], v[94:95]
	v_mul_f32_e32 v24, v67, v67
	v_pk_add_f32 v[94:95], v[24:25], v[94:95] op_sel_hi:[0,1]
	v_pk_fma_f32 v[94:95], v[116:117], v[116:117], v[94:95]
	v_mul_f32_e32 v24, v117, v117
	v_pk_add_f32 v[94:95], v[24:25], v[94:95] op_sel_hi:[0,1]
	v_mov_b32_e32 v24, v94
	s_nop 1
	v_permlane16_swap_b32_e32 v94, v24
	v_add_f32_e32 v78, v94, v24
	v_mov_b32_e32 v86, v78
	v_permlane32_swap_b32_e32 v79, v87
	s_nop 0
	v_permlane32_swap_b32_e32 v78, v86
	v_pk_add_f32 v[78:79], v[78:79], v[86:87]
	v_pk_mul_f32 v[46:47], v[44:45], v[46:47]
	v_pk_fma_f32 v[78:79], v[78:79], s[12:13], v[110:111] op_sel_hi:[1,0,0]
	v_pk_fma_f32 v[46:47], v[106:107], v[62:63], v[46:47]
	v_mul_f32_e32 v24, 0x4b800000, v79
	v_cmp_gt_f32_e64 s[4:5], s95, v79
	v_pk_mul_f32 v[46:47], v[46:47], s[94:95] op_sel_hi:[1,0]
	s_nop 0
	v_cndmask_b32_e64 v24, v79, v24, s[4:5]
	v_rsq_f32_e32 v79, v24
	v_cvt_pk_bf16_f32 v24, v46, v47
	v_mul_f32_e32 v46, 0x45800000, v79
	v_cndmask_b32_e64 v46, v79, v46, s[4:5]
	v_pk_mul_f32 v[62:63], v[50:51], v[46:47] op_sel_hi:[1,0]
	v_cmp_gt_f32_e64 s[4:5], s95, v78
	v_pk_mul_f32 v[62:63], v[62:63], v[120:121]
	s_nop 0
	v_mov_b32_e32 v47, v62
	v_mov_b32_e32 v79, v62
	v_mov_b32_e32 v86, v63
	v_mov_b32_e32 v87, v63
	v_permlane32_swap_b32_e32 v47, v79
	s_nop 0
	v_permlane32_swap_b32_e32 v86, v87
	v_cndmask_b32_e32 v87, v86, v87, vcc
	v_cndmask_b32_e32 v86, v47, v79, vcc
	v_pk_mul_f32 v[86:87], v[118:119], v[86:87]
	s_nop 0
	v_pk_fma_f32 v[62:63], v[62:63], v[68:69], v[86:87]
	v_pk_mul_f32 v[68:69], v[48:49], v[46:47] op_sel_hi:[1,0]
	v_pk_mul_f32 v[62:63], v[62:63], s[94:95] op_sel_hi:[1,0]
	v_pk_mul_f32 v[68:69], v[68:69], v[122:123]
	v_cvt_pk_bf16_f32 v63, v62, v63
	v_mov_b32_e32 v47, v68
	v_mov_b32_e32 v62, v68
	v_mov_b32_e32 v79, v69
	v_mov_b32_e32 v86, v69
	v_permlane32_swap_b32_e32 v47, v62
	s_nop 0
	v_permlane32_swap_b32_e32 v79, v86
	v_cndmask_b32_e32 v87, v79, v86, vcc
	v_cndmask_b32_e32 v86, v47, v62, vcc
	v_pk_mul_f32 v[86:87], v[104:105], v[86:87]
	s_nop 0
	v_pk_fma_f32 v[64:65], v[68:69], v[64:65], v[86:87]
	s_nop 0
	v_pk_mul_f32 v[64:65], v[64:65], s[94:95] op_sel_hi:[1,0]
	s_nop 0
	v_cvt_pk_bf16_f32 v62, v64, v65
	v_pk_mul_f32 v[64:65], v[54:55], v[46:47] op_sel_hi:[1,0]
	s_nop 0
	v_pk_mul_f32 v[64:65], v[64:65], v[126:127]
	s_nop 0
	v_mov_b32_e32 v47, v64
	v_mov_b32_e32 v68, v64
	v_mov_b32_e32 v69, v65
	v_mov_b32_e32 v79, v65
	v_permlane32_swap_b32_e32 v47, v68
	s_nop 0
	v_permlane32_swap_b32_e32 v69, v79
	v_cndmask_b32_e32 v69, v69, v79, vcc
	v_cndmask_b32_e32 v68, v47, v68, vcc
	v_pk_mul_f32 v[68:69], v[124:125], v[68:69]
	s_nop 0
	v_pk_fma_f32 v[60:61], v[64:65], v[60:61], v[68:69]
	v_pk_mul_f32 v[64:65], v[52:53], v[46:47] op_sel_hi:[1,0]
	v_pk_mul_f32 v[60:61], v[60:61], s[94:95] op_sel_hi:[1,0]
	v_pk_mul_f32 v[64:65], v[64:65], v[130:131]
	v_cvt_pk_bf16_f32 v61, v60, v61
	v_mov_b32_e32 v47, v64
	v_mov_b32_e32 v60, v64
	v_mov_b32_e32 v68, v65
	v_mov_b32_e32 v69, v65
	v_permlane32_swap_b32_e32 v47, v60
	s_nop 0
	v_permlane32_swap_b32_e32 v68, v69
	v_cndmask_b32_e32 v69, v68, v69, vcc
	v_cndmask_b32_e32 v68, v47, v60, vcc
	v_pk_mul_f32 v[68:69], v[128:129], v[68:69]
	s_nop 0
	v_pk_fma_f32 v[56:57], v[64:65], v[56:57], v[68:69]
	s_nop 0
	v_pk_mul_f32 v[56:57], v[56:57], s[94:95] op_sel_hi:[1,0]
	s_nop 0
	v_cvt_pk_bf16_f32 v60, v56, v57
	v_pk_mul_f32 v[56:57], v[72:73], v[46:47] op_sel_hi:[1,0]
; __device__ __forceinline__ unsigned cvtpk(float lo, float hi) { f32x2 v = {lo, hi}; bf16x2_t b = __builtin_convertvector(v, bf16x2_t); return __builtin_bit_cast(unsigned, b); }
; template <int DQK, int DV, bool LEAD> ...
;     ...
;           const float rn = rsqrtf(sn * (1.f / 64.f) + EPS);
; #pragma unroll
;           for (int ds = 0; ds < 2; ++ds)
; #pragma unroll
;               for (int j = 0; j < 8; ++j) x[ds][j] *= rn * qgain[32 * ds + 8 * g4 + j];
;           if constexpr (DQK == 64) {
; #pragma unroll
;               for (int ds = 0; ds < 2; ++ds)
; #pragma unroll
;                   for (int j = 0; j < 8; ++j) {
;                       auto rr = __builtin_amdgcn_permlane32_swap(__float_as_uint(x[ds][j]), __float_as_uint(x[ds][j]), false, false);
;                       const float other = hi ? __uint_as_float(rr[0]) : __uint_as_float(rr[1]);
;                       float cc = 1.f, sg = 0.f;
;                       if (lat) { const f32x2 cs = rope[(ds ? pcol : prow) * 16 + 8 * (g4 & 1) + j]; cc = cs.x; sg = hi ? cs.y : -cs.y; }
;                       x[ds][j] = x[ds][j] * cc + other * sg; }
;           } else {
;               float sr = 0.f;
; #pragma unroll
;               for (int j = 0; j < 8; ++j) sr += x[2][j] * x[2][j];
;               sr = lanes4_sum(sr);
;               const float rq = rsqrtf(sr * (1.f / 32.f) + EPS);
; #pragma unroll
;               for (int j = 0; j < 8; ++j) { const float av = x[2][j] * rq * qgain[64 + 8 * g4 + j];
;                   auto rr = __builtin_amdgcn_permlane16_swap(__float_as_uint(av), __float_as_uint(av), false, false);
;                   const float other = (g4 & 1) ? __uint_as_float(rr[0]) : __uint_as_float(rr[1]);
;                   float cc = 1.f, sg = 0.f;
;                   if (lat) { const f32x2 cs = rope[((g4 & 2) ? pcol : prow) * 8 + j]; cc = cs.x; sg = (g4 & 1) ? cs.y : -cs.y; }
;                   x[2][j] = av * cc + other * sg; }
;           }
; #pragma unroll
;           for (int ds = 0; ds < NDS; ++ds) { u32x4 w;
; #pragma unroll
;               for (int i = 0; i < 4; ++i) w[i] = cvtpk(x[ds][2 * i] * c2, x[ds][2 * i + 1] * c2);
;               qf[qb * NDS + ds] = __builtin_bit_cast(bf16x8, w); }
;       }
; #pragma unroll
;       for (int d0 = 0; d0 < NQB * NDS; ++d0) asm volatile("" : "+v"(qf[d0])); }
;     wait_bar<0>();
	s_nop 0
	v_pk_mul_f32 v[56:57], v[56:57], v[58:59]
	s_nop 0
	v_mov_b32_e32 v47, v56
	v_mov_b32_e32 v58, v56
	v_mov_b32_e32 v59, v57
	v_mov_b32_e32 v64, v57
	v_permlane32_swap_b32_e32 v47, v58
	s_nop 0
	v_permlane32_swap_b32_e32 v59, v64
	v_cndmask_b32_e32 v59, v59, v64, vcc
	v_cndmask_b32_e32 v58, v47, v58, vcc
	v_pk_mul_f32 v[58:59], v[30:31], v[58:59]
	s_nop 0
	v_pk_fma_f32 v[56:57], v[56:57], v[32:33], v[58:59]
	s_nop 0
	v_pk_mul_f32 v[56:57], v[56:57], s[94:95] op_sel_hi:[1,0]
	s_nop 0
	v_cvt_pk_bf16_f32 v59, v56, v57
	v_pk_mul_f32 v[56:57], v[70:71], v[46:47] op_sel_hi:[1,0]
	s_nop 0
	v_pk_mul_f32 v[56:57], v[56:57], v[84:85]
	s_nop 0
	v_mov_b32_e32 v47, v56
	v_mov_b32_e32 v58, v56
	v_mov_b32_e32 v64, v57
	v_mov_b32_e32 v65, v57
	v_permlane32_swap_b32_e32 v47, v58
	s_nop 0
	v_permlane32_swap_b32_e32 v64, v65
	v_cndmask_b32_e32 v65, v64, v65, vcc
	v_cndmask_b32_e32 v64, v47, v58, vcc
	v_pk_mul_f32 v[64:65], v[34:35], v[64:65]
	s_nop 0
	v_pk_fma_f32 v[56:57], v[36:37], v[56:57], v[64:65]
	s_nop 0
	v_pk_mul_f32 v[56:57], v[56:57], s[94:95] op_sel_hi:[1,0]
	s_nop 0
	v_cvt_pk_bf16_f32 v58, v56, v57
	v_pk_mul_f32 v[56:57], v[76:77], v[46:47] op_sel_hi:[1,0]
	s_nop 0
	v_pk_mul_f32 v[56:57], v[56:57], v[108:109]
	s_nop 0
	v_mov_b32_e32 v47, v56
	v_mov_b32_e32 v64, v56
	v_mov_b32_e32 v65, v57
	v_mov_b32_e32 v68, v57
	v_permlane32_swap_b32_e32 v47, v64
	s_nop 0
	v_permlane32_swap_b32_e32 v65, v68
	v_cndmask_b32_e32 v65, v65, v68, vcc
	v_cndmask_b32_e32 v64, v47, v64, vcc
	v_pk_mul_f32 v[56:57], v[40:41], v[56:57]
	v_pk_mul_f32 v[46:47], v[74:75], v[46:47] op_sel_hi:[1,0]
	v_pk_fma_f32 v[56:57], v[38:39], v[64:65], v[56:57]
	v_pk_mul_f32 v[46:47], v[46:47], v[82:83]
	v_pk_mul_f32 v[56:57], v[56:57], s[94:95] op_sel_hi:[1,0]
	v_mov_b32_e32 v64, v46
	v_cvt_pk_bf16_f32 v57, v56, v57
	v_mov_b32_e32 v56, v46
	s_nop 1
	v_permlane32_swap_b32_e32 v56, v64
	v_mov_b32_e32 v65, v47
	v_mov_b32_e32 v68, v47
	v_cndmask_b32_e32 v64, v56, v64, vcc
	v_mul_f32_e32 v56, 0x4b800000, v78
	v_permlane32_swap_b32_e32 v65, v68
	v_cndmask_b32_e64 v56, v78, v56, s[4:5]
	v_cndmask_b32_e32 v65, v65, v68, vcc
	v_rsq_f32_e32 v68, v56
	v_pk_mul_f32 v[46:47], v[44:45], v[46:47]
	s_nop 0
	v_pk_fma_f32 v[46:47], v[106:107], v[64:65], v[46:47]
	s_nop 0
	v_pk_mul_f32 v[46:47], v[46:47], s[94:95] op_sel_hi:[1,0]
	s_nop 0
	v_cvt_pk_bf16_f32 v56, v46, v47
	v_mul_f32_e32 v46, 0x45800000, v68
	v_cndmask_b32_e64 v46, v68, v46, s[4:5]
	v_pk_mul_f32 v[64:65], v[74:75], v[46:47] op_sel_hi:[1,0]
	v_pk_mul_f32 v[68:69], v[76:77], v[46:47] op_sel_hi:[1,0]
	v_pk_mul_f32 v[64:65], v[64:65], v[90:91]
	v_pk_mul_f32 v[48:49], v[48:49], v[46:47] op_sel_hi:[1,0]
	v_pk_mul_f32 v[42:43], v[68:69], v[42:43]
	v_pk_mul_f32 v[68:69], v[70:71], v[46:47] op_sel_hi:[1,0]
	v_pk_mul_f32 v[70:71], v[72:73], v[46:47] op_sel_hi:[1,0]
	v_pk_mul_f32 v[52:53], v[52:53], v[46:47] op_sel_hi:[1,0]
	v_pk_mul_f32 v[54:55], v[54:55], v[46:47] op_sel_hi:[1,0]
	v_pk_mul_f32 v[48:49], v[48:49], v[66:67]
	v_pk_mul_f32 v[46:47], v[50:51], v[46:47] op_sel_hi:[1,0]
	v_mov_b32_e32 v50, v64
	v_mov_b32_e32 v66, v64
	v_mov_b32_e32 v51, v65
	v_mov_b32_e32 v67, v65
	v_permlane32_swap_b32_e32 v50, v66
	s_nop 0
	v_permlane32_swap_b32_e32 v51, v67
	v_cndmask_b32_e32 v51, v51, v67, vcc
	v_cndmask_b32_e32 v50, v50, v66, vcc
	v_pk_mul_f32 v[44:45], v[44:45], v[64:65]
	v_mov_b32_e32 v64, v42
	v_pk_fma_f32 v[44:45], v[106:107], v[50:51], v[44:45]
	v_mov_b32_e32 v50, v42
	v_mov_b32_e32 v51, v43
	v_mov_b32_e32 v65, v43
	v_permlane32_swap_b32_e32 v50, v64
	s_nop 0
	v_permlane32_swap_b32_e32 v51, v65
	v_pk_mul_f32 v[68:69], v[68:69], v[80:81]
	v_cndmask_b32_e32 v51, v51, v65, vcc
	v_cndmask_b32_e32 v50, v50, v64, vcc
	v_pk_mul_f32 v[40:41], v[40:41], v[42:43]
	v_mov_b32_e32 v42, v68
	v_pk_fma_f32 v[38:39], v[38:39], v[50:51], v[40:41]
	v_mov_b32_e32 v40, v68
	v_mov_b32_e32 v41, v69
	v_mov_b32_e32 v43, v69
	v_permlane32_swap_b32_e32 v40, v42
	s_nop 0
	v_permlane32_swap_b32_e32 v41, v43
	v_cndmask_b32_e32 v41, v41, v43, vcc
	v_cndmask_b32_e32 v40, v40, v42, vcc
	v_pk_mul_f32 v[70:71], v[70:71], v[100:101]
	v_pk_mul_f32 v[34:35], v[34:35], v[40:41]
	v_mov_b32_e32 v40, v70
	v_pk_fma_f32 v[34:35], v[36:37], v[68:69], v[34:35]
	v_mov_b32_e32 v36, v70
	v_mov_b32_e32 v37, v71
	v_mov_b32_e32 v41, v71
	v_permlane32_swap_b32_e32 v36, v40
	s_nop 0
	v_permlane32_swap_b32_e32 v37, v41
	v_cndmask_b32_e32 v37, v37, v41, vcc
	v_cndmask_b32_e32 v36, v36, v40, vcc
	v_pk_mul_f32 v[52:53], v[52:53], v[92:93]
	v_pk_mul_f32 v[30:31], v[30:31], v[36:37]
	v_mov_b32_e32 v36, v52
	v_pk_fma_f32 v[30:31], v[70:71], v[32:33], v[30:31]
	v_mov_b32_e32 v32, v52
	v_mov_b32_e32 v33, v53
	v_mov_b32_e32 v37, v53
	v_permlane32_swap_b32_e32 v32, v36
	s_nop 0
	v_permlane32_swap_b32_e32 v33, v37
	v_cndmask_b32_e32 v33, v33, v37, vcc
	v_cndmask_b32_e32 v32, v32, v36, vcc
	v_pk_mul_f32 v[54:55], v[54:55], v[96:97]
	v_pk_mul_f32 v[32:33], v[88:89], v[32:33]
	v_mov_b32_e32 v36, v54
	v_pk_fma_f32 v[28:29], v[52:53], v[28:29], v[32:33]
	v_mov_b32_e32 v32, v54
	v_mov_b32_e32 v33, v55
	v_mov_b32_e32 v37, v55
	v_permlane32_swap_b32_e32 v32, v36
	s_nop 0
	v_permlane32_swap_b32_e32 v33, v37
	v_cndmask_b32_e32 v33, v33, v37, vcc
	v_cndmask_b32_e32 v32, v32, v36, vcc
	v_pk_mul_f32 v[20:21], v[20:21], v[32:33]
	v_mov_b32_e32 v32, v48
	v_pk_fma_f32 v[20:21], v[54:55], v[22:23], v[20:21]
	v_mov_b32_e32 v22, v48
	v_mov_b32_e32 v23, v49
	v_mov_b32_e32 v33, v49
	v_permlane32_swap_b32_e32 v22, v32
	s_nop 0
	v_permlane32_swap_b32_e32 v23, v33
	v_cndmask_b32_e32 v23, v23, v33, vcc
	v_cndmask_b32_e32 v22, v22, v32, vcc
	v_pk_mul_f32 v[46:47], v[46:47], v[116:117]
	v_pk_mul_f32 v[16:17], v[16:17], v[22:23]
	v_mov_b32_e32 v22, v46
	v_pk_fma_f32 v[16:17], v[48:49], v[18:19], v[16:17]
	v_mov_b32_e32 v18, v46
	v_mov_b32_e32 v19, v47
	v_mov_b32_e32 v23, v47
	v_permlane32_swap_b32_e32 v18, v22
	s_nop 0
	v_permlane32_swap_b32_e32 v19, v23
	v_cndmask_b32_e32 v19, v19, v23, vcc
	v_cndmask_b32_e32 v18, v18, v22, vcc
	v_pk_mul_f32 v[18:19], v[114:115], v[18:19]
	v_pk_mul_f32 v[16:17], v[16:17], s[94:95] op_sel_hi:[1,0]
	v_pk_fma_f32 v[14:15], v[46:47], v[14:15], v[18:19]
	v_pk_mul_f32 v[18:19], v[44:45], s[94:95] op_sel_hi:[1,0]
	v_pk_mul_f32 v[14:15], v[14:15], s[94:95] op_sel_hi:[1,0]
	v_cvt_pk_bf16_f32 v76, v18, v19
	v_pk_mul_f32 v[18:19], v[38:39], s[94:95] op_sel_hi:[1,0]
	v_cvt_pk_bf16_f32 v86, v16, v17
	v_cvt_pk_bf16_f32 v77, v18, v19
	v_pk_mul_f32 v[18:19], v[34:35], s[94:95] op_sel_hi:[1,0]
	v_cvt_pk_bf16_f32 v87, v14, v15
	v_cvt_pk_bf16_f32 v78, v18, v19
	v_pk_mul_f32 v[18:19], v[30:31], s[94:95] op_sel_hi:[1,0]
	v_bfe_u32 v22, v162, 1, 3
	v_cvt_pk_bf16_f32 v79, v18, v19
	v_pk_mul_f32 v[18:19], v[28:29], s[94:95] op_sel_hi:[1,0]
	v_bitop3_b32 v22, v169, v22, 4 bitop3:0x36
	v_cvt_pk_bf16_f32 v84, v18, v19
	v_pk_mul_f32 v[18:19], v[20:21], s[94:95] op_sel_hi:[1,0]
	v_lshlrev_b32_e32 v22, 4, v22
	v_cvt_pk_bf16_f32 v85, v18, v19
	s_waitcnt vmcnt(0) lgkmcnt(0)
	s_barrier
; #define ATT_SB() __builtin_amdgcn_sched_barrier(0)
; #define ATT_DMA_K(t, sl) do { glds16(ksrc + (size_t)(t) * 64 * kpitch, (unsigned)__builtin_amdgcn_readfirstlane(kdst + (sl) * KSLOT)); \
;         if constexpr (DQK == 96) glds16(krsrc + (size_t)(t) * 64 * 32, (unsigned)__builtin_amdgcn_readfirstlane(krdst + (sl) * KSLOT)); } while (0)
; #define ATT_DMA_V(t, sl) do { glds16(vsrc + (size_t)(t) * 64, (unsigned)__builtin_amdgcn_readfirstlane(vdst + (sl) * VSLOT)); \
;         if constexpr (DV == 128) glds16(vsrc + (size_t)64 * NR + (size_t)(t) * 64, (unsigned)__builtin_amdgcn_readfirstlane(vdst + (sl) * VSLOT + 8192)); } while (0)
; #define ATT_KLOAD(sl) do { _Pragma("unroll") for (int kb_ = 0; kb_ < NKW; ++kb_) _Pragma("unroll") for (int ds_ = 0; ds_ < NDS; ++ds_) { \
;         if (ds_ < 2) kf[kb_ * NDS + ds_] = *(const LAS bf16x8*)(kp[ds_ & 1] + (sl) * KSLOT + (kb_ & 1) * 512 + (kb_ >> 1) * 4096); \
;         else kf[kb_ * NDS + ds_] = *(const LAS bf16x8*)(krp + (sl) * KSLOT + (kb_ & 1) * 256 + (kb_ >> 1) * 2048); } } while (0)
; #define ATT_QK() do { _Pragma("unroll") for (int kb_ = 0; kb_ < NKW; ++kb_) _Pragma("unroll") for (int ds_ = 0; ds_ < NDS; ++ds_) _Pragma("unroll") for (int qb_ = 0; qb_ < NQB; ++qb_) \
;         c[kb_][qb_] = __builtin_amdgcn_mfma_f32_16x16x32_bf16(kf[kb_ * NDS + ds_], qf[qb_ * NDS + ds_], ds_ == 0 ? zero4 : c[kb_][qb_], 0, 0, 0); } while (0)
; #define ATT_EXP() do { _Pragma("unroll") for (int kb_ = 0; kb_ < NKW; ++kb_) _Pragma("unroll") for (int qb_ = 0; qb_ < NQB; ++qb_) _Pragma("unroll") for (int i_ = 0; i_ < 4; ++i_) \
;         c[kb_][qb_][i_] = __builtin_amdgcn_exp2f(c[kb_][qb_][i_]); } while (0)
; template <int DQK, int DV, bool LEAD> ...
;     ...
;     ATT_KLOAD(0);
;     asm volatile("s_waitcnt lgkmcnt(0)\n\ts_barrier" ::: "memory");
;     float lsum[NQB];
; #pragma unroll
;     for (int qb = 0; qb < NQB; ++qb) lsum[qb] = 0.f;
;     const f32x4 zero4 = {0.f, 0.f, 0.f, 0.f};
;     f32x4 o[NDB][NQB], c[NKW][NQB]; u32x4 pw[4];
; #pragma unroll
;     for (int i = 0; i < NDB; ++i)
; #pragma unroll
;         for (int qb = 0; qb < NQB; ++qb) o[i][qb] = zero4;
;     ATT_DMA_K(3, 0); ATT_DMA_V(1, 1);
;     ATT_QK(); ATT_SB();
;     ATT_KLOAD(1); ATT_SB();
;     if constexpr (LEAD) { ATT_EXP(); ATT_SUMPACK(); }
;     wait_bar<NDMA>();
;     int s_prev = 0, s_cur = 1, s_next = 2;
;     int one_ = 1; asm volatile("" : "+s"(one_));
	ds_read_b128 v[14:17], v174
	ds_read_b128 v[18:21], v174 offset:512
	v_add_u32_e32 v176, v170, v22
	s_waitcnt lgkmcnt(1)
	v_mfma_f32_16x16x32_bf16 v[28:31], v[14:17], v[6:9], 0
	ds_read_b128 v[40:43], v176
	ds_read_b128 v[44:47], v176 offset:512
	s_waitcnt lgkmcnt(0)
	s_barrier
	s_mov_b32 s4, 0
	v_mfma_f32_16x16x32_bf16 v[32:35], v[14:17], v[24:27], 0
	s_cselect_b64 vcc, -1, 0
	s_mov_b32 s7, s4
	v_mfma_f32_16x16x32_bf16 v[36:39], v[14:17], v[56:59], 0
	v_mfma_f32_16x16x32_bf16 v[14:17], v[14:17], v[76:79], 0
	s_waitcnt lgkmcnt(1)
	v_mfma_f32_16x16x32_bf16 v[116:119], v[40:43], v[84:87], v[14:17]
	v_mfma_f32_16x16x32_bf16 v[14:17], v[18:21], v[6:9], 0
	v_mfma_f32_16x16x32_bf16 v[144:147], v[40:43], v[2:5], v[28:31]
	v_mfma_f32_16x16x32_bf16 v[140:143], v[40:43], v[10:13], v[32:35]
	v_mfma_f32_16x16x32_bf16 v[28:31], v[18:21], v[24:27], 0
	v_mfma_f32_16x16x32_bf16 v[32:35], v[18:21], v[56:59], 0
	v_mfma_f32_16x16x32_bf16 v[18:21], v[18:21], v[76:79], 0
	s_waitcnt lgkmcnt(0)
	v_mfma_f32_16x16x32_bf16 v[136:139], v[44:47], v[2:5], v[14:17]
	s_nop 2
	v_lshl_add_u64 v[14:15], v[164:165], 0, s[96:97]
	s_mov_b32 s5, m0
	s_mov_b32 m0, s50
	s_nop 0
	global_load_lds_dwordx4 v[14:15], off
	s_mov_b32 m0, s5
	v_mfma_f32_16x16x32_bf16 v[128:131], v[40:43], v[60:63], v[36:39]
	v_lshl_add_u64 v[14:15], v[166:167], 0, s[66:67]
	s_add_i32 s5, s45, 0x2000
	s_mov_b32 s6, m0
	s_mov_b32 m0, s5
	s_nop 0
	global_load_lds_dwordx4 v[14:15], off
	s_mov_b32 m0, s6
	v_mfma_f32_16x16x32_bf16 v[132:135], v[44:47], v[10:13], v[28:31]
	s_mov_b32 s6, s4
	s_mov_b32 s5, s4
	v_mov_b64_e32 v[16:17], s[6:7]
	v_mfma_f32_16x16x32_bf16 v[124:127], v[44:47], v[60:63], v[32:35]
	v_mov_b64_e32 v[14:15], s[4:5]
	v_mfma_f32_16x16x32_bf16 v[120:123], v[44:47], v[84:87], v[18:21]
	ds_read_b128 v[100:103], v174 offset:8192
	ds_read_b128 v[108:111], v174 offset:8704
	ds_read_b128 v[104:107], v176 offset:8192
	ds_read_b128 v[112:115], v176 offset:8704
	v_cndmask_b32_e32 v18, v22, v168, vcc
	v_add3_u32 v175, 0, v163, v18
	s_waitcnt vmcnt(2) lgkmcnt(0)
	s_barrier
	s_mov_b32 s5, 1
	v_mov_b32_e32 v22, 0
	s_cmp_lg_u32 s5, 0
	v_mov_b64_e32 v[20:21], v[16:17]
	v_mov_b64_e32 v[30:31], v[16:17]
	v_mov_b64_e32 v[34:35], v[16:17]
	v_mov_b64_e32 v[38:39], v[16:17]
	v_mov_b64_e32 v[42:43], v[16:17]
	v_mov_b64_e32 v[46:47], v[16:17]
	v_mov_b64_e32 v[50:51], v[16:17]
	v_mov_b64_e32 v[54:55], v[16:17]
	v_mov_b64_e32 v[66:67], v[16:17]
	v_mov_b64_e32 v[70:71], v[16:17]
	v_mov_b64_e32 v[74:75], v[16:17]
	v_mov_b64_e32 v[82:83], v[16:17]
	v_mov_b64_e32 v[90:91], v[16:17]
	v_mov_b64_e32 v[94:95], v[16:17]
	v_mov_b64_e32 v[98:99], v[16:17]
	s_cselect_b64 s[6:7], -1, 0
	v_mov_b64_e32 v[18:19], v[14:15]
	v_mov_b64_e32 v[28:29], v[14:15]
	v_mov_b64_e32 v[32:33], v[14:15]
	v_mov_b64_e32 v[36:37], v[14:15]
	v_mov_b64_e32 v[40:41], v[14:15]
	v_mov_b64_e32 v[44:45], v[14:15]
	v_mov_b64_e32 v[48:49], v[14:15]
	v_mov_b64_e32 v[52:53], v[14:15]
	v_mov_b64_e32 v[64:65], v[14:15]
	v_mov_b64_e32 v[68:69], v[14:15]
	v_mov_b64_e32 v[72:73], v[14:15]
	v_mov_b64_e32 v[80:81], v[14:15]
	v_mov_b64_e32 v[88:89], v[14:15]
	v_mov_b64_e32 v[92:93], v[14:15]
	v_mov_b64_e32 v[96:97], v[14:15]
	s_mov_b32 s38, 2
	v_mov_b32_e32 v23, v22
	v_mov_b32_e32 v168, v22
	v_mov_b32_e32 v169, v22
	s_branch .LBB0_957

; #define ATT_SB() __builtin_amdgcn_sched_barrier(0)
; #define ATT_KLOAD(sl) do { _Pragma("unroll") for (int kb_ = 0; kb_ < NKW; ++kb_) _Pragma("unroll") for (int ds_ = 0; ds_ < NDS; ++ds_) { \
;         if (ds_ < 2) kf[kb_ * NDS + ds_] = *(const LAS bf16x8*)(kp[ds_ & 1] + (sl) * KSLOT + (kb_ & 1) * 512 + (kb_ >> 1) * 4096); \
;         else kf[kb_ * NDS + ds_] = *(const LAS bf16x8*)(krp + (sl) * KSLOT + (kb_ & 1) * 256 + (kb_ >> 1) * 2048); } } while (0)
; #define ATT_QK() do { _Pragma("unroll") for (int kb_ = 0; kb_ < NKW; ++kb_) _Pragma("unroll") for (int ds_ = 0; ds_ < NDS; ++ds_) _Pragma("unroll") for (int qb_ = 0; qb_ < NQB; ++qb_) \
;         c[kb_][qb_] = __builtin_amdgcn_mfma_f32_16x16x32_bf16(kf[kb_ * NDS + ds_], qf[qb_ * NDS + ds_], ds_ == 0 ? zero4 : c[kb_][qb_], 0, 0, 0); } while (0)
; #define ATT_PVP(h_) do { _Pragma("unroll") for (int g_ = 0; g_ < NVF; ++g_) _Pragma("unroll") for (int qb_ = 0; qb_ < NQB; ++qb_) { \
;         const int db_ = KS ? g_ : (h_) * 4 + (g_ >> 1), sq_ = KS ? 0 : (g_ & 1); \
;         o[db_][qb_] = __builtin_amdgcn_mfma_f32_16x16x32_bf16(vf[g_], __builtin_bit_cast(bf16x8, pw[sq_ * NQB + qb_]), o[db_][qb_], 0, 0, 0); } } while (0)
; template <int DQK, int DV, bool LEAD> ...
;     ...
;                 __builtin_amdgcn_s_setprio(1);
;                 ATT_QK(); ATT_SB();
;                 if (one_) { ATT_KLOAD(s_next); ATT_SB(); ATT_PVP(0); }
;                 ATT_SB();
;                 __builtin_amdgcn_s_setprio(0);
;             }
; #pragma unroll
;             for (int kb = 0; kb < NKW; ++kb)
; #pragma unroll
;                 for (int qb = 0; qb < NQB; ++qb) asm volatile("" : "+v"(c[kb][qb]));
;         }
;         ATT_SB();
;         wait_bar<NDMA>();
;         const int tmp = s_prev; s_prev = s_cur; s_cur = s_next; s_next = tmp;
.LBB0_959:
	v_add_f32_e32 v168, v168, v172
	v_add_f32_e32 v169, v169, v173
	v_add_f32_e32 v22, v22, v170
	v_add_f32_e32 v23, v23, v171
	s_setprio 0
	s_waitcnt vmcnt(2) lgkmcnt(0)
	s_add_i32 s16, s16, 1
	s_cmpk_lg_i32 s16, 0x85
	s_cbranch_scc0 .Lx_rot4_exit
	s_mov_b32 s38, s4
	s_mov_b32 s4, s5
	s_branch .Lx_rot4_head

; #define ATT_SB() __builtin_amdgcn_sched_barrier(0)
; #define ATT_KLOAD(sl) do { _Pragma("unroll") for (int kb_ = 0; kb_ < NKW; ++kb_) _Pragma("unroll") for (int ds_ = 0; ds_ < NDS; ++ds_) { \
;         if (ds_ < 2) kf[kb_ * NDS + ds_] = *(const LAS bf16x8*)(kp[ds_ & 1] + (sl) * KSLOT + (kb_ & 1) * 512 + (kb_ >> 1) * 4096); \
;         else kf[kb_ * NDS + ds_] = *(const LAS bf16x8*)(krp + (sl) * KSLOT + (kb_ & 1) * 256 + (kb_ >> 1) * 2048); } } while (0)
; #define ATT_QK() do { _Pragma("unroll") for (int kb_ = 0; kb_ < NKW; ++kb_) _Pragma("unroll") for (int ds_ = 0; ds_ < NDS; ++ds_) _Pragma("unroll") for (int qb_ = 0; qb_ < NQB; ++qb_) \
;         c[kb_][qb_] = __builtin_amdgcn_mfma_f32_16x16x32_bf16(kf[kb_ * NDS + ds_], qf[qb_ * NDS + ds_], ds_ == 0 ? zero4 : c[kb_][qb_], 0, 0, 0); } while (0)
; #define ATT_VLOAD(sl, h_) do { _Pragma("unroll") for (int g_ = 0; g_ < NVF; ++g_) { \
;         if constexpr (KS) vf[g_] = *(const LAS bf16x8*)(vpk + (sl) * VSLOT + g_ * 2048); \
;         else vf[g_] = *(const LAS bf16x8*)(vp[g_ & 1] + (sl) * VSLOT + ((h_) * 4 + (g_ >> 1)) * 2048); } } while (0)
; template <int DQK, int DV, bool LEAD> ...
;     ...
;             if constexpr (DV == 64) ATT_EXP();
;             ATT_SUMPACK();
;             asm volatile("" : "+v"(pw[0]), "+v"(pw[1]), "+v"(pw[2]), "+v"(pw[3]));
; #pragma unroll
;             for (int qb = 0; qb < NQB; ++qb) asm volatile("" : "+v"(lsum[qb]));
;         } else {
;             if constexpr (DV == 128) {
;                 ATT_PVP(0); ATT_SB();
;                 ATT_VLOAD(s_prev, 1); ATT_SB();
;                 ATT_QK(); ATT_SB();
;                 if (one_) { ATT_KLOAD(s_next); ATT_SB(); ATT_PVP(1); }
;                 ATT_SB();
;             } else {
;                 __builtin_amdgcn_s_setprio(1);
;                 ATT_QK(); ATT_SB();
;                 if (one_) { ATT_KLOAD(s_next); ATT_SB(); ATT_PVP(0); }
;                 ATT_SB();
;                 __builtin_amdgcn_s_setprio(0);
;             }
; #pragma unroll
;             for (int kb = 0; kb < NKW; ++kb)
; #pragma unroll
;                 for (int qb = 0; qb < NQB; ++qb) asm volatile("" : "+v"(c[kb][qb]));
;         }
;         ATT_SB();
;         wait_bar<NDMA>();
;         const int tmp = s_prev; s_prev = s_cur; s_cur = s_next; s_next = tmp;
.LBB0_964:
	v_exp_f32_e32 v102, v158
	v_exp_f32_e32 v103, v159
	v_exp_f32_e32 v104, v160
	v_exp_f32_e32 v105, v161
	v_exp_f32_e32 v114, v154
	v_exp_f32_e32 v115, v155
	v_exp_f32_e32 v116, v156
	v_exp_f32_e32 v117, v157
	v_exp_f32_e32 v122, v150
	v_exp_f32_e32 v123, v151
	v_exp_f32_e32 v124, v152
	v_exp_f32_e32 v125, v153
	v_exp_f32_e32 v126, v142
	v_exp_f32_e32 v127, v143
	v_exp_f32_e32 v128, v144
	v_exp_f32_e32 v129, v145
	v_exp_f32_e32 v142, v146
	v_exp_f32_e32 v143, v147
	v_add_f32_e32 v146, v102, v103
	v_add_f32_e32 v147, v104, v105
	v_exp_f32_e32 v144, v148
	v_exp_f32_e32 v138, v138
	v_exp_f32_e32 v134, v134
	v_exp_f32_e32 v130, v130
	v_add_f32_e32 v146, v146, v147
	v_add_f32_e32 v147, v114, v115
	v_add_f32_e32 v148, v116, v117
	v_exp_f32_e32 v145, v149
	v_add_f32_e32 v147, v147, v148
	v_add_f32_e32 v148, v122, v123
	v_add_f32_e32 v149, v124, v125
	v_exp_f32_e32 v139, v139
	v_exp_f32_e32 v135, v135
	v_exp_f32_e32 v131, v131
	v_add_f32_e32 v148, v148, v149
	v_add_f32_e32 v149, v126, v127
	v_add_f32_e32 v150, v128, v129
	v_add_f32_e32 v149, v149, v150
	v_exp_f32_e32 v140, v140
	v_exp_f32_e32 v136, v136
	v_exp_f32_e32 v132, v132
	v_add_f32_e32 v146, v146, v142
	v_add_f32_e32 v147, v147, v138
	v_add_f32_e32 v148, v148, v134
	v_add_f32_e32 v149, v149, v130
	v_exp_f32_e32 v141, v141
	v_exp_f32_e32 v137, v137
	v_exp_f32_e32 v133, v133
	v_add_f32_e32 v146, v143, v146
	v_add_f32_e32 v147, v139, v147
	v_add_f32_e32 v148, v135, v148
	v_add_f32_e32 v149, v131, v149
	v_cvt_pk_bf16_f32 v102, v102, v103
	v_add_f32_e32 v146, v144, v146
	v_add_f32_e32 v147, v140, v147
	v_add_f32_e32 v148, v136, v148
	v_add_f32_e32 v149, v132, v149
	v_cvt_pk_bf16_f32 v103, v104, v105
	v_add_f32_e32 v146, v145, v146
	v_add_f32_e32 v147, v141, v147
	v_add_f32_e32 v148, v137, v148
	v_add_f32_e32 v149, v133, v149
	v_cvt_pk_bf16_f32 v104, v142, v143
	v_add_f32_e32 v169, v169, v146
	v_add_f32_e32 v168, v168, v147
	v_add_f32_e32 v167, v167, v148
	v_add_f32_e32 v166, v166, v149
	v_cvt_pk_bf16_f32 v105, v144, v145
	v_cvt_pk_bf16_f32 v114, v114, v115
	v_cvt_pk_bf16_f32 v115, v116, v117
	v_cvt_pk_bf16_f32 v116, v138, v139
	v_cvt_pk_bf16_f32 v117, v140, v141
	v_cvt_pk_bf16_f32 v122, v122, v123
	v_cvt_pk_bf16_f32 v123, v124, v125
	v_cvt_pk_bf16_f32 v124, v134, v135
	v_cvt_pk_bf16_f32 v125, v136, v137
	v_cvt_pk_bf16_f32 v126, v126, v127
	v_cvt_pk_bf16_f32 v127, v128, v129
	v_cvt_pk_bf16_f32 v128, v130, v131
	v_cvt_pk_bf16_f32 v129, v132, v133
	s_waitcnt vmcnt(2) lgkmcnt(0)
	s_add_i32 s27, s27, 1
	s_cmpk_lg_i32 s27, 0x85
	s_mov_b32 s37, s29
	s_mov_b32 s29, s40
	s_cbranch_scc0 .Lx_rot5_exit
	s_barrier
